# in-projection epilogue: flat stores converted to global stores (no lgkmcnt coupling with the epilogue's LDS reads)
# speedup vs baseline: 1.0045x; 1.0045x over previous
; #define PG8_PACK8(y0, y1) (u32x4){cvt_pk_bf16((y0)[0], (y0)[1]), cvt_pk_bf16((y0)[2], (y0)[3]), cvt_pk_bf16((y1)[0], (y1)[1]), cvt_pk_bf16((y1)[2], (y1)[3])}
;     __device__ __forceinline__ void operator()(const f32x4 (&acc)[2][2][4][2], const Unit& u, int ui, int wr, int wc, int fr, int fq) const {
;     ...
;         } else {
; #pragma unroll
;             for (int ai = 0; ai < 2; ++ai)
; #pragma unroll
;                 for (int m = 0; m < 4; ++m) {
;                     const unsigned row = row0 + ai * HALF + m * 16; const float rs = rsp[ai * HALF + m * 16];
; #pragma unroll
;                     for (int bj = 0; bj < 2; ++bj) {
;                         const f32x4 y0 = acc[ai][bj][m][0] * rs, y1 = acc[ai][bj][m][1] * rs;
;                         if (pn == 12 || bj == 0) {
;                             const unsigned gcol = (unsigned)((pn == 12 ? 0 : 256) + 128 * bj + 32 * wc + 8 * fq);
;                             f32x4 s0, s1;
; #pragma unroll
;                             for (int e = 0; e < 4; ++e) { s0[e] = __builtin_amdgcn_rcpf(1.0f + __builtin_amdgcn_exp2f(y0[e] * -1.4426950408889634f)); s1[e] = __builtin_amdgcn_rcpf(1.0f + __builtin_amdgcn_exp2f(y1[e] * -1.4426950408889634f)); }
;                             *(u32x4*)(ws + E_GF + (size_t)((row * 384u + gcol) * 2u)) = PG8_PACK8(s0, s1);
.LBB0_559:
	s_cmp_eq_u32 s4, s42
	s_cselect_b32 s19, 0, 0x400
	v_lshl_add_u32 v158, s4, 8, v163
	v_add_u32_e32 v160, s19, v181
	s_cmp_gt_i32 s26, 7
	s_mov_b64 s[28:29], -1
	s_cbranch_scc0 .LBB0_613
	s_cmp_lt_u32 s26, 12
	s_cbranch_scc1 .LBB0_610
	ds_read_b32 v140, v160
	s_cmp_lg_u32 s26, 12
	s_cselect_b64 s[28:29], -1, 0
	s_cmp_eq_u32 s26, 12
	s_cselect_b32 s19, 0, 0x100
	s_waitcnt lgkmcnt(0)
	v_pk_mul_f32 v[130:131], v[124:125], v[140:141] op_sel_hi:[1,0]
	v_pk_mul_f32 v[134:135], v[126:127], v[140:141] op_sel_hi:[1,0]
	v_pk_mul_f32 v[136:137], v[128:129], v[140:141] op_sel_hi:[1,0]
	v_mul_f32_e32 v130, 0xbfb8aa3b, v130
	v_mul_f32_e32 v0, 0xbfb8aa3b, v134
	v_mul_f32_e32 v134, 0xbfb8aa3b, v135
	v_mul_f32_e32 v135, 0xbfb8aa3b, v136
	v_exp_f32_e32 v130, v130
	v_mul_f32_e32 v136, 0xbfb8aa3b, v137
	v_pk_mul_f32 v[132:133], v[122:123], v[140:141] op_sel_hi:[1,0]
	v_exp_f32_e32 v0, v0
	v_exp_f32_e32 v136, v136
	v_mul_f32_e32 v131, 0xbfb8aa3b, v131
	v_mul_f32_e32 v132, 0xbfb8aa3b, v132
	v_exp_f32_e32 v134, v134
	v_mul_f32_e32 v133, 0xbfb8aa3b, v133
	v_exp_f32_e32 v135, v135
	v_exp_f32_e32 v131, v131
	v_exp_f32_e32 v132, v132
	v_exp_f32_e32 v133, v133
	v_add_f32_e32 v130, 1.0, v130
	v_or_b32_e32 v161, s19, v237
	s_movk_i32 s19, 0x180
	v_add_f32_e32 v0, 1.0, v0
	v_rcp_f32_e32 v137, v130
	v_add_f32_e32 v130, 1.0, v136
	v_mul_lo_u32 v144, v158, s19
	v_rcp_f32_e32 v0, v0
	v_add_f32_e32 v134, 1.0, v134
	v_add_f32_e32 v135, 1.0, v135
	v_rcp_f32_e32 v136, v130
	v_add_f32_e32 v130, 1.0, v131
	v_add_f32_e32 v132, 1.0, v132
	v_rcp_f32_e32 v134, v134
	v_add_f32_e32 v133, 1.0, v133
	v_rcp_f32_e32 v135, v135
	v_rcp_f32_e32 v138, v130
	v_cvt_pk_bf16_f32 v130, v0, v134
	v_add_lshl_u32 v0, v144, v161, 1
	v_rcp_f32_e32 v132, v132
	v_rcp_f32_e32 v133, v133
	v_cvt_pk_bf16_f32 v131, v135, v136
	v_lshl_add_u64 v[134:135], s[10:11], 0, v[0:1]
	v_cvt_pk_bf16_f32 v132, v132, v133
	v_cvt_pk_bf16_f32 v133, v137, v138
	global_store_dwordx4 v[134:135], v[130:133], off
	v_pk_mul_f32 v[134:135], v[120:121], v[140:141] op_sel_hi:[1,0]
	v_pk_mul_f32 v[138:139], v[118:119], v[140:141] op_sel_hi:[1,0]
	v_pk_mul_f32 v[136:137], v[116:117], v[140:141] op_sel_hi:[1,0]
	v_pk_mul_f32 v[140:141], v[114:115], v[140:141] op_sel_hi:[1,0]
	s_mov_b64 s[30:31], -1
	s_and_b64 vcc, exec, s[28:29]
	s_cbranch_vccz .LBB0_565
	s_and_saveexec_b64 s[30:31], s[34:35]
	s_cbranch_execz .LBB0_564

; #define PG8_PACK8(y0, y1) (u32x4){cvt_pk_bf16((y0)[0], (y0)[1]), cvt_pk_bf16((y0)[2], (y0)[3]), cvt_pk_bf16((y1)[0], (y1)[1]), cvt_pk_bf16((y1)[2], (y1)[3])}
;     __device__ __forceinline__ void operator()(const f32x4 (&acc)[2][2][4][2], const Unit& u, int ui, int wr, int wc, int fr, int fq) const {
;     ...
;                     const unsigned row = row0 + ai * HALF + m * 16; const float rs = rsp[ai * HALF + m * 16];
; #pragma unroll
;                     for (int bj = 0; bj < 2; ++bj) {
;                         const f32x4 y0 = acc[ai][bj][m][0] * rs, y1 = acc[ai][bj][m][1] * rs;
;                         if (pn == 12 || bj == 0) {
;                             const unsigned gcol = (unsigned)((pn == 12 ? 0 : 256) + 128 * bj + 32 * wc + 8 * fq);
;                             f32x4 s0, s1;
; #pragma unroll
;                             for (int e = 0; e < 4; ++e) { s0[e] = __builtin_amdgcn_rcpf(1.0f + __builtin_amdgcn_exp2f(y0[e] * -1.4426950408889634f)); s1[e] = __builtin_amdgcn_rcpf(1.0f + __builtin_amdgcn_exp2f(y1[e] * -1.4426950408889634f)); }
;                             *(u32x4*)(ws + E_GF + (size_t)((row * 384u + gcol) * 2u)) = PG8_PACK8(s0, s1);
.LBB0_565:
	s_andn2_b64 vcc, exec, s[30:31]
	s_cbranch_vccnz .LBB0_567
	v_mul_f32_e32 v131, 0xbfb8aa3b, v140
	v_exp_f32_e32 v131, v131
	v_mul_f32_e32 v132, 0xbfb8aa3b, v139
	v_mul_f32_e32 v133, 0xbfb8aa3b, v141
	v_exp_f32_e32 v132, v132
	v_exp_f32_e32 v133, v133
	v_add_f32_e32 v131, 1.0, v131
	v_mul_f32_e32 v130, 0xbfb8aa3b, v138
	v_rcp_f32_e32 v138, v131
	v_add_f32_e32 v131, 1.0, v132
	v_add_f32_e32 v132, 1.0, v133
	v_mul_f32_e32 v133, 0xbfb8aa3b, v134
	v_mul_f32_e32 v134, 0xbfb8aa3b, v136
	v_mul_f32_e32 v135, 0xbfb8aa3b, v135
	v_exp_f32_e32 v130, v130
	v_exp_f32_e32 v133, v133
	v_exp_f32_e32 v134, v134
	v_exp_f32_e32 v135, v135
	v_mul_f32_e32 v136, 0xbfb8aa3b, v137
	v_exp_f32_e32 v136, v136
	v_add_f32_e32 v130, 1.0, v130
	v_add_f32_e32 v133, 1.0, v133
	v_add_f32_e32 v134, 1.0, v134
	v_add_f32_e32 v135, 1.0, v135
	v_rcp_f32_e32 v130, v130
	v_rcp_f32_e32 v131, v131
	v_rcp_f32_e32 v132, v132
	v_rcp_f32_e32 v133, v133
	v_rcp_f32_e32 v134, v134
	v_rcp_f32_e32 v135, v135
	v_add_f32_e32 v136, 1.0, v136
	v_add_u32_e32 v0, 0x100, v0
	v_rcp_f32_e32 v136, v136
	v_cvt_pk_bf16_f32 v130, v130, v131
	v_cvt_pk_bf16_f32 v131, v133, v135
	v_cvt_pk_bf16_f32 v132, v138, v132
	v_cvt_pk_bf16_f32 v133, v134, v136
	v_lshl_add_u64 v[134:135], s[10:11], 0, v[0:1]
	global_store_dwordx4 v[134:135], v[130:133], off
.LBB0_567:
	ds_read_b32 v140, v160 offset:64
	v_add_u32_e32 v159, 0x1800, v144
	s_andn2_b64 vcc, exec, s[28:29]
	s_waitcnt lgkmcnt(0)
	v_pk_mul_f32 v[130:131], v[106:107], v[140:141] op_sel_hi:[1,0]
	v_pk_mul_f32 v[132:133], v[110:111], v[140:141] op_sel_hi:[1,0]
	v_mul_f32_e32 v130, 0xbfb8aa3b, v130
	v_mul_f32_e32 v0, 0xbfb8aa3b, v132
	v_exp_f32_e32 v130, v130
	v_mul_f32_e32 v132, 0xbfb8aa3b, v133
	v_exp_f32_e32 v132, v132
	v_pk_mul_f32 v[134:135], v[108:109], v[140:141] op_sel_hi:[1,0]
	v_pk_mul_f32 v[136:137], v[112:113], v[140:141] op_sel_hi:[1,0]
	v_add_f32_e32 v130, 1.0, v130
	v_mul_f32_e32 v131, 0xbfb8aa3b, v131
	v_exp_f32_e32 v131, v131
	v_rcp_f32_e32 v133, v130
	v_add_f32_e32 v130, 1.0, v132
	v_mul_f32_e32 v132, 0xbfb8aa3b, v136
	v_mul_f32_e32 v134, 0xbfb8aa3b, v134
	v_exp_f32_e32 v132, v132
	v_exp_f32_e32 v134, v134
	v_add_f32_e32 v131, 1.0, v131
	v_exp_f32_e32 v0, v0
	v_rcp_f32_e32 v136, v131
	v_add_f32_e32 v131, 1.0, v132
	v_add_f32_e32 v132, 1.0, v134
	v_mul_f32_e32 v134, 0xbfb8aa3b, v137
	v_mul_f32_e32 v135, 0xbfb8aa3b, v135
	v_exp_f32_e32 v134, v134
	v_exp_f32_e32 v135, v135
	v_add_f32_e32 v0, 1.0, v0
	v_rcp_f32_e32 v0, v0
	v_rcp_f32_e32 v130, v130
	v_rcp_f32_e32 v137, v132
	v_add_f32_e32 v132, 1.0, v134
	v_add_f32_e32 v134, 1.0, v135
	v_rcp_f32_e32 v131, v131
	v_rcp_f32_e32 v132, v132
	v_rcp_f32_e32 v134, v134
	v_cvt_pk_bf16_f32 v130, v0, v130
	v_add_lshl_u32 v0, v159, v161, 1
	v_cvt_pk_bf16_f32 v131, v131, v132
	v_cvt_pk_bf16_f32 v132, v133, v136
	v_cvt_pk_bf16_f32 v133, v137, v134
	v_lshl_add_u64 v[134:135], s[10:11], 0, v[0:1]
	global_store_dwordx4 v[134:135], v[130:133], off
	v_pk_mul_f32 v[134:135], v[104:105], v[140:141] op_sel_hi:[1,0]
	v_pk_mul_f32 v[138:139], v[102:103], v[140:141] op_sel_hi:[1,0]
	v_cndmask_b32_e64 v130, 0, 1, s[28:29]
	v_pk_mul_f32 v[136:137], v[100:101], v[140:141] op_sel_hi:[1,0]
	v_pk_mul_f32 v[140:141], v[98:99], v[140:141] op_sel_hi:[1,0]
	v_cmp_ne_u32_e64 s[40:41], 1, v130
	s_mov_b64 s[28:29], -1
	s_cbranch_vccnz .LBB0_571
	s_and_saveexec_b64 s[28:29], s[34:35]
	s_cbranch_execz .LBB0_570

; #define PG8_PACK8(y0, y1) (u32x4){cvt_pk_bf16((y0)[0], (y0)[1]), cvt_pk_bf16((y0)[2], (y0)[3]), cvt_pk_bf16((y1)[0], (y1)[1]), cvt_pk_bf16((y1)[2], (y1)[3])}
;     __device__ __forceinline__ void operator()(const f32x4 (&acc)[2][2][4][2], const Unit& u, int ui, int wr, int wc, int fr, int fq) const {
;     ...
;                     const unsigned row = row0 + ai * HALF + m * 16; const float rs = rsp[ai * HALF + m * 16];
; #pragma unroll
;                     for (int bj = 0; bj < 2; ++bj) {
;                         const f32x4 y0 = acc[ai][bj][m][0] * rs, y1 = acc[ai][bj][m][1] * rs;
;                         if (pn == 12 || bj == 0) {
;                             const unsigned gcol = (unsigned)((pn == 12 ? 0 : 256) + 128 * bj + 32 * wc + 8 * fq);
;                             f32x4 s0, s1;
; #pragma unroll
;                             for (int e = 0; e < 4; ++e) { s0[e] = __builtin_amdgcn_rcpf(1.0f + __builtin_amdgcn_exp2f(y0[e] * -1.4426950408889634f)); s1[e] = __builtin_amdgcn_rcpf(1.0f + __builtin_amdgcn_exp2f(y1[e] * -1.4426950408889634f)); }
;                             *(u32x4*)(ws + E_GF + (size_t)((row * 384u + gcol) * 2u)) = PG8_PACK8(s0, s1);
.LBB0_571:
	s_andn2_b64 vcc, exec, s[28:29]
	s_cbranch_vccnz .LBB0_573
	v_mul_f32_e32 v131, 0xbfb8aa3b, v140
	v_exp_f32_e32 v131, v131
	v_mul_f32_e32 v132, 0xbfb8aa3b, v139
	v_mul_f32_e32 v133, 0xbfb8aa3b, v141
	v_exp_f32_e32 v132, v132
	v_exp_f32_e32 v133, v133
	v_add_f32_e32 v131, 1.0, v131
	v_mul_f32_e32 v130, 0xbfb8aa3b, v138
	v_rcp_f32_e32 v138, v131
	v_add_f32_e32 v131, 1.0, v132
	v_add_f32_e32 v132, 1.0, v133
	v_mul_f32_e32 v133, 0xbfb8aa3b, v134
	v_mul_f32_e32 v134, 0xbfb8aa3b, v136
	v_mul_f32_e32 v135, 0xbfb8aa3b, v135
	v_exp_f32_e32 v130, v130
	v_exp_f32_e32 v133, v133
	v_exp_f32_e32 v134, v134
	v_exp_f32_e32 v135, v135
	v_mul_f32_e32 v136, 0xbfb8aa3b, v137
	v_exp_f32_e32 v136, v136
	v_add_f32_e32 v130, 1.0, v130
	v_add_f32_e32 v133, 1.0, v133
	v_add_f32_e32 v134, 1.0, v134
	v_add_f32_e32 v135, 1.0, v135
	v_rcp_f32_e32 v130, v130
	v_rcp_f32_e32 v131, v131
	v_rcp_f32_e32 v132, v132
	v_rcp_f32_e32 v133, v133
	v_rcp_f32_e32 v134, v134
	v_rcp_f32_e32 v135, v135
	v_add_f32_e32 v136, 1.0, v136
	v_add_u32_e32 v0, 0x100, v0
	v_rcp_f32_e32 v136, v136
	v_cvt_pk_bf16_f32 v130, v130, v131
	v_cvt_pk_bf16_f32 v131, v133, v135
	v_cvt_pk_bf16_f32 v132, v138, v132
	v_cvt_pk_bf16_f32 v133, v134, v136
	v_lshl_add_u64 v[134:135], s[10:11], 0, v[0:1]
	global_store_dwordx4 v[134:135], v[130:133], off
.LBB0_573:
	ds_read_b32 v140, v160 offset:128
	v_add_u32_e32 v159, 0x1800, v159
	s_and_b64 vcc, exec, s[40:41]
	s_mov_b64 s[28:29], -1
	s_waitcnt lgkmcnt(0)
	v_pk_mul_f32 v[130:131], v[90:91], v[140:141] op_sel_hi:[1,0]
	v_pk_mul_f32 v[132:133], v[94:95], v[140:141] op_sel_hi:[1,0]
	v_mul_f32_e32 v130, 0xbfb8aa3b, v130
	v_mul_f32_e32 v0, 0xbfb8aa3b, v132
	v_exp_f32_e32 v130, v130
	v_mul_f32_e32 v132, 0xbfb8aa3b, v133
	v_exp_f32_e32 v132, v132
	v_pk_mul_f32 v[134:135], v[92:93], v[140:141] op_sel_hi:[1,0]
	v_pk_mul_f32 v[136:137], v[96:97], v[140:141] op_sel_hi:[1,0]
	v_add_f32_e32 v130, 1.0, v130
	v_mul_f32_e32 v131, 0xbfb8aa3b, v131
	v_exp_f32_e32 v131, v131
	v_rcp_f32_e32 v133, v130
	v_add_f32_e32 v130, 1.0, v132
	v_mul_f32_e32 v132, 0xbfb8aa3b, v136
	v_mul_f32_e32 v134, 0xbfb8aa3b, v134
	v_exp_f32_e32 v132, v132
	v_exp_f32_e32 v134, v134
	v_add_f32_e32 v131, 1.0, v131
	v_exp_f32_e32 v0, v0
	v_rcp_f32_e32 v136, v131
	v_add_f32_e32 v131, 1.0, v132
	v_add_f32_e32 v132, 1.0, v134
	v_mul_f32_e32 v134, 0xbfb8aa3b, v137
	v_mul_f32_e32 v135, 0xbfb8aa3b, v135
	v_exp_f32_e32 v134, v134
	v_exp_f32_e32 v135, v135
	v_add_f32_e32 v0, 1.0, v0
	v_rcp_f32_e32 v0, v0
	v_rcp_f32_e32 v130, v130
	v_rcp_f32_e32 v137, v132
	v_add_f32_e32 v132, 1.0, v134
	v_add_f32_e32 v134, 1.0, v135
	v_rcp_f32_e32 v131, v131
	v_rcp_f32_e32 v132, v132
	v_rcp_f32_e32 v134, v134
	v_cvt_pk_bf16_f32 v130, v0, v130
	v_add_lshl_u32 v0, v159, v161, 1
	v_cvt_pk_bf16_f32 v131, v131, v132
	v_cvt_pk_bf16_f32 v132, v133, v136
	v_cvt_pk_bf16_f32 v133, v137, v134
	v_lshl_add_u64 v[134:135], s[10:11], 0, v[0:1]
	global_store_dwordx4 v[134:135], v[130:133], off
	v_pk_mul_f32 v[134:135], v[88:89], v[140:141] op_sel_hi:[1,0]
	v_pk_mul_f32 v[138:139], v[86:87], v[140:141] op_sel_hi:[1,0]
	v_pk_mul_f32 v[136:137], v[84:85], v[140:141] op_sel_hi:[1,0]
	v_pk_mul_f32 v[140:141], v[82:83], v[140:141] op_sel_hi:[1,0]
	s_cbranch_vccnz .LBB0_577
	s_and_saveexec_b64 s[28:29], s[34:35]
	s_cbranch_execz .LBB0_576

; #define PG8_PACK8(y0, y1) (u32x4){cvt_pk_bf16((y0)[0], (y0)[1]), cvt_pk_bf16((y0)[2], (y0)[3]), cvt_pk_bf16((y1)[0], (y1)[1]), cvt_pk_bf16((y1)[2], (y1)[3])}
;     __device__ __forceinline__ void operator()(const f32x4 (&acc)[2][2][4][2], const Unit& u, int ui, int wr, int wc, int fr, int fq) const {
;     ...
;                     const unsigned row = row0 + ai * HALF + m * 16; const float rs = rsp[ai * HALF + m * 16];
; #pragma unroll
;                     for (int bj = 0; bj < 2; ++bj) {
;                         const f32x4 y0 = acc[ai][bj][m][0] * rs, y1 = acc[ai][bj][m][1] * rs;
;                         if (pn == 12 || bj == 0) {
;                             const unsigned gcol = (unsigned)((pn == 12 ? 0 : 256) + 128 * bj + 32 * wc + 8 * fq);
;                             f32x4 s0, s1;
; #pragma unroll
;                             for (int e = 0; e < 4; ++e) { s0[e] = __builtin_amdgcn_rcpf(1.0f + __builtin_amdgcn_exp2f(y0[e] * -1.4426950408889634f)); s1[e] = __builtin_amdgcn_rcpf(1.0f + __builtin_amdgcn_exp2f(y1[e] * -1.4426950408889634f)); }
;                             *(u32x4*)(ws + E_GF + (size_t)((row * 384u + gcol) * 2u)) = PG8_PACK8(s0, s1);
.LBB0_579:
	ds_read_b32 v140, v160 offset:192
	v_add_u32_e32 v159, 0x1800, v159
	s_and_b64 vcc, exec, s[40:41]
	s_mov_b64 s[28:29], -1
	s_waitcnt lgkmcnt(0)
	v_pk_mul_f32 v[130:131], v[74:75], v[140:141] op_sel_hi:[1,0]
	v_pk_mul_f32 v[132:133], v[78:79], v[140:141] op_sel_hi:[1,0]
	v_mul_f32_e32 v130, 0xbfb8aa3b, v130
	v_mul_f32_e32 v0, 0xbfb8aa3b, v132
	v_exp_f32_e32 v130, v130
	v_mul_f32_e32 v132, 0xbfb8aa3b, v133
	v_exp_f32_e32 v132, v132
	v_pk_mul_f32 v[134:135], v[76:77], v[140:141] op_sel_hi:[1,0]
	v_pk_mul_f32 v[136:137], v[80:81], v[140:141] op_sel_hi:[1,0]
	v_add_f32_e32 v130, 1.0, v130
	v_mul_f32_e32 v131, 0xbfb8aa3b, v131
	v_exp_f32_e32 v131, v131
	v_rcp_f32_e32 v133, v130
	v_add_f32_e32 v130, 1.0, v132
	v_mul_f32_e32 v132, 0xbfb8aa3b, v136
	v_mul_f32_e32 v134, 0xbfb8aa3b, v134
	v_exp_f32_e32 v132, v132
	v_exp_f32_e32 v134, v134
	v_add_f32_e32 v131, 1.0, v131
	v_exp_f32_e32 v0, v0
	v_rcp_f32_e32 v136, v131
	v_add_f32_e32 v131, 1.0, v132
	v_add_f32_e32 v132, 1.0, v134
	v_mul_f32_e32 v134, 0xbfb8aa3b, v137
	v_mul_f32_e32 v135, 0xbfb8aa3b, v135
	v_exp_f32_e32 v134, v134
	v_exp_f32_e32 v135, v135
	v_add_f32_e32 v0, 1.0, v0
	v_rcp_f32_e32 v0, v0
	v_rcp_f32_e32 v130, v130
	v_rcp_f32_e32 v137, v132
	v_add_f32_e32 v132, 1.0, v134
	v_add_f32_e32 v134, 1.0, v135
	v_rcp_f32_e32 v131, v131
	v_rcp_f32_e32 v132, v132
	v_rcp_f32_e32 v134, v134
	v_cvt_pk_bf16_f32 v130, v0, v130
	v_add_lshl_u32 v0, v159, v161, 1
	v_cvt_pk_bf16_f32 v131, v131, v132
	v_cvt_pk_bf16_f32 v132, v133, v136
	v_cvt_pk_bf16_f32 v133, v137, v134
	v_lshl_add_u64 v[134:135], s[10:11], 0, v[0:1]
	global_store_dwordx4 v[134:135], v[130:133], off
	v_pk_mul_f32 v[134:135], v[72:73], v[140:141] op_sel_hi:[1,0]
	v_pk_mul_f32 v[138:139], v[70:71], v[140:141] op_sel_hi:[1,0]
	v_pk_mul_f32 v[136:137], v[68:69], v[140:141] op_sel_hi:[1,0]
	v_pk_mul_f32 v[140:141], v[66:67], v[140:141] op_sel_hi:[1,0]
	s_cbranch_vccnz .LBB0_583
	s_and_saveexec_b64 s[28:29], s[34:35]
	s_cbranch_execz .LBB0_582

; #define PG8_PACK8(y0, y1) (u32x4){cvt_pk_bf16((y0)[0], (y0)[1]), cvt_pk_bf16((y0)[2], (y0)[3]), cvt_pk_bf16((y1)[0], (y1)[1]), cvt_pk_bf16((y1)[2], (y1)[3])}
;     __device__ __forceinline__ void operator()(const f32x4 (&acc)[2][2][4][2], const Unit& u, int ui, int wr, int wc, int fr, int fq) const {
;     ...
;                     const unsigned row = row0 + ai * HALF + m * 16; const float rs = rsp[ai * HALF + m * 16];
; #pragma unroll
;                     for (int bj = 0; bj < 2; ++bj) {
;                         const f32x4 y0 = acc[ai][bj][m][0] * rs, y1 = acc[ai][bj][m][1] * rs;
;                         if (pn == 12 || bj == 0) {
;                             const unsigned gcol = (unsigned)((pn == 12 ? 0 : 256) + 128 * bj + 32 * wc + 8 * fq);
;                             f32x4 s0, s1;
; #pragma unroll
;                             for (int e = 0; e < 4; ++e) { s0[e] = __builtin_amdgcn_rcpf(1.0f + __builtin_amdgcn_exp2f(y0[e] * -1.4426950408889634f)); s1[e] = __builtin_amdgcn_rcpf(1.0f + __builtin_amdgcn_exp2f(y1[e] * -1.4426950408889634f)); }
;                             *(u32x4*)(ws + E_GF + (size_t)((row * 384u + gcol) * 2u)) = PG8_PACK8(s0, s1);
.LBB0_585:
	ds_read_b32 v140, v160 offset:512
	v_add_u32_e32 v159, 0x7800, v159
	s_and_b64 vcc, exec, s[40:41]
	s_mov_b64 s[28:29], -1
	s_waitcnt lgkmcnt(0)
	v_pk_mul_f32 v[130:131], v[58:59], v[140:141] op_sel_hi:[1,0]
	v_pk_mul_f32 v[132:133], v[62:63], v[140:141] op_sel_hi:[1,0]
	v_mul_f32_e32 v130, 0xbfb8aa3b, v130
	v_mul_f32_e32 v0, 0xbfb8aa3b, v132
	v_exp_f32_e32 v130, v130
	v_mul_f32_e32 v132, 0xbfb8aa3b, v133
	v_exp_f32_e32 v132, v132
	v_pk_mul_f32 v[134:135], v[60:61], v[140:141] op_sel_hi:[1,0]
	v_pk_mul_f32 v[136:137], v[64:65], v[140:141] op_sel_hi:[1,0]
	v_add_f32_e32 v130, 1.0, v130
	v_mul_f32_e32 v131, 0xbfb8aa3b, v131
	v_exp_f32_e32 v131, v131
	v_rcp_f32_e32 v133, v130
	v_add_f32_e32 v130, 1.0, v132
	v_mul_f32_e32 v132, 0xbfb8aa3b, v136
	v_mul_f32_e32 v134, 0xbfb8aa3b, v134
	v_exp_f32_e32 v132, v132
	v_exp_f32_e32 v134, v134
	v_add_f32_e32 v131, 1.0, v131
	v_exp_f32_e32 v0, v0
	v_rcp_f32_e32 v136, v131
	v_add_f32_e32 v131, 1.0, v132
	v_add_f32_e32 v132, 1.0, v134
	v_mul_f32_e32 v134, 0xbfb8aa3b, v137
	v_mul_f32_e32 v135, 0xbfb8aa3b, v135
	v_exp_f32_e32 v134, v134
	v_exp_f32_e32 v135, v135
	v_add_f32_e32 v0, 1.0, v0
	v_rcp_f32_e32 v0, v0
	v_rcp_f32_e32 v130, v130
	v_rcp_f32_e32 v137, v132
	v_add_f32_e32 v132, 1.0, v134
	v_add_f32_e32 v134, 1.0, v135
	v_rcp_f32_e32 v131, v131
	v_rcp_f32_e32 v132, v132
	v_rcp_f32_e32 v134, v134
	v_cvt_pk_bf16_f32 v130, v0, v130
	v_add_lshl_u32 v0, v159, v161, 1
	v_cvt_pk_bf16_f32 v131, v131, v132
	v_cvt_pk_bf16_f32 v132, v133, v136
	v_cvt_pk_bf16_f32 v133, v137, v134
	v_lshl_add_u64 v[134:135], s[10:11], 0, v[0:1]
	global_store_dwordx4 v[134:135], v[130:133], off
	v_pk_mul_f32 v[134:135], v[56:57], v[140:141] op_sel_hi:[1,0]
	v_pk_mul_f32 v[138:139], v[54:55], v[140:141] op_sel_hi:[1,0]
	v_pk_mul_f32 v[136:137], v[52:53], v[140:141] op_sel_hi:[1,0]
	v_pk_mul_f32 v[140:141], v[50:51], v[140:141] op_sel_hi:[1,0]
	s_cbranch_vccnz .LBB0_589
	s_and_saveexec_b64 s[28:29], s[34:35]
	s_cbranch_execz .LBB0_588

; #define PG8_PACK8(y0, y1) (u32x4){cvt_pk_bf16((y0)[0], (y0)[1]), cvt_pk_bf16((y0)[2], (y0)[3]), cvt_pk_bf16((y1)[0], (y1)[1]), cvt_pk_bf16((y1)[2], (y1)[3])}
;     __device__ __forceinline__ void operator()(const f32x4 (&acc)[2][2][4][2], const Unit& u, int ui, int wr, int wc, int fr, int fq) const {
;     ...
;                     const unsigned row = row0 + ai * HALF + m * 16; const float rs = rsp[ai * HALF + m * 16];
; #pragma unroll
;                     for (int bj = 0; bj < 2; ++bj) {
;                         const f32x4 y0 = acc[ai][bj][m][0] * rs, y1 = acc[ai][bj][m][1] * rs;
;                         if (pn == 12 || bj == 0) {
;                             const unsigned gcol = (unsigned)((pn == 12 ? 0 : 256) + 128 * bj + 32 * wc + 8 * fq);
;                             f32x4 s0, s1;
; #pragma unroll
;                             for (int e = 0; e < 4; ++e) { s0[e] = __builtin_amdgcn_rcpf(1.0f + __builtin_amdgcn_exp2f(y0[e] * -1.4426950408889634f)); s1[e] = __builtin_amdgcn_rcpf(1.0f + __builtin_amdgcn_exp2f(y1[e] * -1.4426950408889634f)); }
;                             *(u32x4*)(ws + E_GF + (size_t)((row * 384u + gcol) * 2u)) = PG8_PACK8(s0, s1);
.LBB0_591:
	ds_read_b32 v140, v160 offset:576
	v_add_u32_e32 v159, 0x1800, v159
	s_and_b64 vcc, exec, s[40:41]
	s_mov_b64 s[28:29], -1
	s_waitcnt lgkmcnt(0)
	v_pk_mul_f32 v[130:131], v[42:43], v[140:141] op_sel_hi:[1,0]
	v_pk_mul_f32 v[132:133], v[46:47], v[140:141] op_sel_hi:[1,0]
	v_mul_f32_e32 v130, 0xbfb8aa3b, v130
	v_mul_f32_e32 v0, 0xbfb8aa3b, v132
	v_exp_f32_e32 v130, v130
	v_mul_f32_e32 v132, 0xbfb8aa3b, v133
	v_exp_f32_e32 v132, v132
	v_pk_mul_f32 v[134:135], v[44:45], v[140:141] op_sel_hi:[1,0]
	v_pk_mul_f32 v[136:137], v[48:49], v[140:141] op_sel_hi:[1,0]
	v_add_f32_e32 v130, 1.0, v130
	v_mul_f32_e32 v131, 0xbfb8aa3b, v131
	v_exp_f32_e32 v131, v131
	v_rcp_f32_e32 v133, v130
	v_add_f32_e32 v130, 1.0, v132
	v_mul_f32_e32 v132, 0xbfb8aa3b, v136
	v_mul_f32_e32 v134, 0xbfb8aa3b, v134
	v_exp_f32_e32 v132, v132
	v_exp_f32_e32 v134, v134
	v_add_f32_e32 v131, 1.0, v131
	v_exp_f32_e32 v0, v0
	v_rcp_f32_e32 v136, v131
	v_add_f32_e32 v131, 1.0, v132
	v_add_f32_e32 v132, 1.0, v134
	v_mul_f32_e32 v134, 0xbfb8aa3b, v137
	v_mul_f32_e32 v135, 0xbfb8aa3b, v135
	v_exp_f32_e32 v134, v134
	v_exp_f32_e32 v135, v135
	v_add_f32_e32 v0, 1.0, v0
	v_rcp_f32_e32 v0, v0
	v_rcp_f32_e32 v130, v130
	v_rcp_f32_e32 v137, v132
	v_add_f32_e32 v132, 1.0, v134
	v_add_f32_e32 v134, 1.0, v135
	v_rcp_f32_e32 v131, v131
	v_rcp_f32_e32 v132, v132
	v_rcp_f32_e32 v134, v134
	v_cvt_pk_bf16_f32 v130, v0, v130
	v_add_lshl_u32 v0, v159, v161, 1
	v_cvt_pk_bf16_f32 v131, v131, v132
	v_cvt_pk_bf16_f32 v132, v133, v136
	v_cvt_pk_bf16_f32 v133, v137, v134
	v_lshl_add_u64 v[134:135], s[10:11], 0, v[0:1]
	global_store_dwordx4 v[134:135], v[130:133], off
	v_pk_mul_f32 v[134:135], v[40:41], v[140:141] op_sel_hi:[1,0]
	v_pk_mul_f32 v[138:139], v[38:39], v[140:141] op_sel_hi:[1,0]
	v_pk_mul_f32 v[136:137], v[36:37], v[140:141] op_sel_hi:[1,0]
	v_pk_mul_f32 v[140:141], v[34:35], v[140:141] op_sel_hi:[1,0]
	s_cbranch_vccnz .LBB0_595
	s_and_saveexec_b64 s[28:29], s[34:35]
	s_cbranch_execz .LBB0_594

; #define PG8_PACK8(y0, y1) (u32x4){cvt_pk_bf16((y0)[0], (y0)[1]), cvt_pk_bf16((y0)[2], (y0)[3]), cvt_pk_bf16((y1)[0], (y1)[1]), cvt_pk_bf16((y1)[2], (y1)[3])}
;     __device__ __forceinline__ void operator()(const f32x4 (&acc)[2][2][4][2], const Unit& u, int ui, int wr, int wc, int fr, int fq) const {
;     ...
;                     const unsigned row = row0 + ai * HALF + m * 16; const float rs = rsp[ai * HALF + m * 16];
; #pragma unroll
;                     for (int bj = 0; bj < 2; ++bj) {
;                         const f32x4 y0 = acc[ai][bj][m][0] * rs, y1 = acc[ai][bj][m][1] * rs;
;                         if (pn == 12 || bj == 0) {
;                             const unsigned gcol = (unsigned)((pn == 12 ? 0 : 256) + 128 * bj + 32 * wc + 8 * fq);
;                             f32x4 s0, s1;
; #pragma unroll
;                             for (int e = 0; e < 4; ++e) { s0[e] = __builtin_amdgcn_rcpf(1.0f + __builtin_amdgcn_exp2f(y0[e] * -1.4426950408889634f)); s1[e] = __builtin_amdgcn_rcpf(1.0f + __builtin_amdgcn_exp2f(y1[e] * -1.4426950408889634f)); }
;                             *(u32x4*)(ws + E_GF + (size_t)((row * 384u + gcol) * 2u)) = PG8_PACK8(s0, s1);
.LBB0_597:
	ds_read_b32 v140, v160 offset:640
	v_add_u32_e32 v159, 0x1800, v159
	s_and_b64 vcc, exec, s[40:41]
	s_mov_b64 s[28:29], -1
	s_waitcnt lgkmcnt(0)
	v_pk_mul_f32 v[130:131], v[26:27], v[140:141] op_sel_hi:[1,0]
	v_pk_mul_f32 v[132:133], v[30:31], v[140:141] op_sel_hi:[1,0]
	v_mul_f32_e32 v130, 0xbfb8aa3b, v130
	v_mul_f32_e32 v0, 0xbfb8aa3b, v132
	v_exp_f32_e32 v130, v130
	v_mul_f32_e32 v132, 0xbfb8aa3b, v133
	v_exp_f32_e32 v132, v132
	v_pk_mul_f32 v[134:135], v[28:29], v[140:141] op_sel_hi:[1,0]
	v_pk_mul_f32 v[136:137], v[32:33], v[140:141] op_sel_hi:[1,0]
	v_add_f32_e32 v130, 1.0, v130
	v_mul_f32_e32 v131, 0xbfb8aa3b, v131
	v_exp_f32_e32 v131, v131
	v_rcp_f32_e32 v133, v130
	v_add_f32_e32 v130, 1.0, v132
	v_mul_f32_e32 v132, 0xbfb8aa3b, v136
	v_mul_f32_e32 v134, 0xbfb8aa3b, v134
	v_exp_f32_e32 v132, v132
	v_exp_f32_e32 v134, v134
	v_add_f32_e32 v131, 1.0, v131
	v_exp_f32_e32 v0, v0
	v_rcp_f32_e32 v136, v131
	v_add_f32_e32 v131, 1.0, v132
	v_add_f32_e32 v132, 1.0, v134
	v_mul_f32_e32 v134, 0xbfb8aa3b, v137
	v_mul_f32_e32 v135, 0xbfb8aa3b, v135
	v_exp_f32_e32 v134, v134
	v_exp_f32_e32 v135, v135
	v_add_f32_e32 v0, 1.0, v0
	v_rcp_f32_e32 v0, v0
	v_rcp_f32_e32 v130, v130
	v_rcp_f32_e32 v137, v132
	v_add_f32_e32 v132, 1.0, v134
	v_add_f32_e32 v134, 1.0, v135
	v_rcp_f32_e32 v131, v131
	v_rcp_f32_e32 v132, v132
	v_rcp_f32_e32 v134, v134
	v_cvt_pk_bf16_f32 v130, v0, v130
	v_add_lshl_u32 v0, v159, v161, 1
	v_cvt_pk_bf16_f32 v131, v131, v132
	v_cvt_pk_bf16_f32 v132, v133, v136
	v_cvt_pk_bf16_f32 v133, v137, v134
	v_lshl_add_u64 v[134:135], s[10:11], 0, v[0:1]
	global_store_dwordx4 v[134:135], v[130:133], off
	v_pk_mul_f32 v[134:135], v[24:25], v[140:141] op_sel_hi:[1,0]
	v_pk_mul_f32 v[138:139], v[22:23], v[140:141] op_sel_hi:[1,0]
	v_pk_mul_f32 v[136:137], v[20:21], v[140:141] op_sel_hi:[1,0]
	v_pk_mul_f32 v[140:141], v[18:19], v[140:141] op_sel_hi:[1,0]
	s_cbranch_vccnz .LBB0_601
	s_and_saveexec_b64 s[28:29], s[34:35]
	s_cbranch_execz .LBB0_600

; #define PG8_PACK8(y0, y1) (u32x4){cvt_pk_bf16((y0)[0], (y0)[1]), cvt_pk_bf16((y0)[2], (y0)[3]), cvt_pk_bf16((y1)[0], (y1)[1]), cvt_pk_bf16((y1)[2], (y1)[3])}
;     __device__ __forceinline__ void operator()(const f32x4 (&acc)[2][2][4][2], const Unit& u, int ui, int wr, int wc, int fr, int fq) const {
;     ...
;                     const unsigned row = row0 + ai * HALF + m * 16; const float rs = rsp[ai * HALF + m * 16];
; #pragma unroll
;                     for (int bj = 0; bj < 2; ++bj) {
;                         const f32x4 y0 = acc[ai][bj][m][0] * rs, y1 = acc[ai][bj][m][1] * rs;
;                         if (pn == 12 || bj == 0) {
;                             const unsigned gcol = (unsigned)((pn == 12 ? 0 : 256) + 128 * bj + 32 * wc + 8 * fq);
;                             f32x4 s0, s1;
; #pragma unroll
;                             for (int e = 0; e < 4; ++e) { s0[e] = __builtin_amdgcn_rcpf(1.0f + __builtin_amdgcn_exp2f(y0[e] * -1.4426950408889634f)); s1[e] = __builtin_amdgcn_rcpf(1.0f + __builtin_amdgcn_exp2f(y1[e] * -1.4426950408889634f)); }
;                             *(u32x4*)(ws + E_GF + (size_t)((row * 384u + gcol) * 2u)) = PG8_PACK8(s0, s1);
;                         } else if (wc == 0 && fq == 0) {
;                             float z[6] = {y0[0], y0[1], y0[2], y0[3], y1[0], y1[1]};
; #pragma unroll
;                             for (int e = 0; e < 6; ++e) { const float zz = z[e] + bfg[e]; z[e] = fminf(zz, 0.f) - log1pf(__expf(-fabsf(zz))); }
;                             float* lp = (float*)(ws + E_LS) + (size_t)row;
; #pragma unroll
;                             for (int e = 0; e < 6; ++e) lp[(size_t)(e * 32768u)] = z[e];
.LBB0_603:
	ds_read_b32 v140, v160 offset:704
	v_add_u32_e32 v0, v159, v161
	s_and_b64 vcc, exec, s[40:41]
	s_mov_b64 s[28:29], -1
	s_waitcnt lgkmcnt(0)
	v_pk_mul_f32 v[130:131], v[10:11], v[140:141] op_sel_hi:[1,0]
	v_pk_mul_f32 v[132:133], v[14:15], v[140:141] op_sel_hi:[1,0]
	v_mul_f32_e32 v130, 0xbfb8aa3b, v130
	v_exp_f32_e32 v130, v130
	v_mul_f32_e32 v133, 0xbfb8aa3b, v133
	v_exp_f32_e32 v133, v133
	v_pk_mul_f32 v[134:135], v[12:13], v[140:141] op_sel_hi:[1,0]
	v_pk_mul_f32 v[136:137], v[16:17], v[140:141] op_sel_hi:[1,0]
	v_add_f32_e32 v130, 1.0, v130
	v_mul_f32_e32 v131, 0xbfb8aa3b, v131
	v_exp_f32_e32 v131, v131
	v_rcp_f32_e32 v138, v130
	v_add_f32_e32 v130, 1.0, v133
	v_mul_f32_e32 v133, 0xbfb8aa3b, v136
	v_mul_f32_e32 v134, 0xbfb8aa3b, v134
	v_exp_f32_e32 v133, v133
	v_exp_f32_e32 v134, v134
	v_add_f32_e32 v131, 1.0, v131
	v_rcp_f32_e32 v136, v131
	v_add_f32_e32 v131, 1.0, v133
	v_add_f32_e32 v133, 1.0, v134
	v_mul_f32_e32 v134, 0xbfb8aa3b, v137
	v_mul_f32_e32 v132, 0xbfb8aa3b, v132
	v_exp_f32_e32 v134, v134
	v_exp_f32_e32 v132, v132
	v_mul_f32_e32 v135, 0xbfb8aa3b, v135
	v_exp_f32_e32 v135, v135
	v_add_f32_e32 v134, 1.0, v134
	v_add_f32_e32 v132, 1.0, v132
	v_rcp_f32_e32 v130, v130
	v_rcp_f32_e32 v131, v131
	v_rcp_f32_e32 v134, v134
	v_rcp_f32_e32 v132, v132
	v_add_f32_e32 v135, 1.0, v135
	v_cvt_pk_bf16_f32 v130, v132, v130
	v_cvt_pk_bf16_f32 v131, v131, v134
	v_mov_b32_e32 v134, 0x3000
	v_rcp_f32_e32 v133, v133
	v_rcp_f32_e32 v135, v135
	v_lshl_add_u32 v0, v0, 1, v134
	v_cvt_pk_bf16_f32 v132, v138, v136
	v_cvt_pk_bf16_f32 v133, v133, v135
	v_lshl_add_u64 v[134:135], s[10:11], 0, v[0:1]
	global_store_dwordx4 v[134:135], v[130:133], off
	v_pk_mul_f32 v[134:135], v[8:9], v[140:141] op_sel_hi:[1,0]
	v_pk_mul_f32 v[138:139], v[6:7], v[140:141] op_sel_hi:[1,0]
	v_pk_mul_f32 v[136:137], v[4:5], v[140:141] op_sel_hi:[1,0]
	v_pk_mul_f32 v[140:141], v[2:3], v[140:141] op_sel_hi:[1,0]
	s_cbranch_vccnz .LBB0_607
	s_cmp_eq_u64 s[34:35], 0
	s_cbranch_scc1 .Lflg_done
	global_load_dwordx4 v[10:13], v1, s[6:7]
	global_load_dwordx2 v[14:15], v1, s[6:7] offset:16
	v_mbcnt_lo_u32_b32 v16, -1, 0
	v_mbcnt_hi_u32_b32 v16, -1, v16
	v_lshrrev_b32_e32 v17, 5, v16
	v_bfe_u32 v16, v16, 4, 1
	v_lshlrev_b32_e32 v17, 9, v17
	v_lshl_add_u32 v17, v16, 7, v17
	v_add_u32_e32 v16, v160, v17
	ds_read_b32 v26, v16
	ds_read_b32 v27, v16 offset:64
	v_lshl_add_u32 v28, v158, 2, v17
	s_mov_b32 s3, 0xbfb8aa3b
	s_mov_b32 s19, 0x3f2aaaab
	s_mov_b32 s21, 0x3f317218
	s_mov_b32 s27, 0x7f800000
	s_mov_b32 s33, 0x33800000
	v_permlane32_swap_b32_e32 v118, v54
	v_permlane32_swap_b32_e32 v119, v55
	v_permlane32_swap_b32_e32 v120, v56
	v_permlane32_swap_b32_e32 v121, v57
	v_permlane32_swap_b32_e32 v114, v50
	v_permlane32_swap_b32_e32 v115, v51
	v_permlane32_swap_b32_e32 v102, v38
	v_permlane32_swap_b32_e32 v103, v39
	v_permlane32_swap_b32_e32 v104, v40
	v_permlane32_swap_b32_e32 v105, v41
	v_permlane32_swap_b32_e32 v98, v34
	v_permlane32_swap_b32_e32 v99, v35
	v_permlane32_swap_b32_e32 v86, v22
	v_permlane32_swap_b32_e32 v87, v23
	v_permlane32_swap_b32_e32 v88, v24
	v_permlane32_swap_b32_e32 v89, v25
	v_permlane32_swap_b32_e32 v82, v18
	v_permlane32_swap_b32_e32 v83, v19
	v_permlane32_swap_b32_e32 v70, v6
	v_permlane32_swap_b32_e32 v71, v7
	v_permlane32_swap_b32_e32 v72, v8
	v_permlane32_swap_b32_e32 v73, v9
	v_permlane32_swap_b32_e32 v66, v2
	v_permlane32_swap_b32_e32 v67, v3
	s_nop 1
	v_permlane16_swap_b32_e32 v118, v86
	v_permlane16_swap_b32_e32 v119, v87
	v_permlane16_swap_b32_e32 v120, v88
	v_permlane16_swap_b32_e32 v121, v89
	v_permlane16_swap_b32_e32 v114, v82
	v_permlane16_swap_b32_e32 v115, v83
	v_permlane16_swap_b32_e32 v102, v70
	v_permlane16_swap_b32_e32 v103, v71
	v_permlane16_swap_b32_e32 v104, v72
	v_permlane16_swap_b32_e32 v105, v73
	v_permlane16_swap_b32_e32 v98, v66
	v_permlane16_swap_b32_e32 v99, v67
	s_waitcnt vmcnt(0) lgkmcnt(0)
	s_nop 1
	v_mul_f32_e32 v118, v118, v26
	v_add_f32_e32 v30, v118, v10
	v_min_f32_e32 v29, 0, v30
	v_mul_f32_e64 v30, |v30|, s3
	v_exp_f32_e32 v30, v30
	s_nop 0
	v_add_f32_e32 v32, 1.0, v30
	v_add_f32_e32 v31, -1.0, v32
	v_sub_f32_e32 v33, v31, v32
	v_add_f32_e32 v33, 1.0, v33
	v_sub_f32_e32 v31, v30, v31
	v_add_f32_e32 v33, v31, v33
	v_frexp_mant_f32_e32 v31, v32
	v_cvt_f64_f32_e32 v[42:43], v32
	v_cmp_gt_f32_e32 vcc, s19, v31
	v_frexp_exp_i32_f64_e32 v31, v[42:43]
	s_nop 0
	v_subbrev_co_u32_e32 v31, vcc, 0, v31, vcc
	v_sub_u32_e32 v42, 0, v31
	v_ldexp_f32 v32, v32, v42
	v_ldexp_f32 v33, v33, v42
	v_add_f32_e32 v42, -1.0, v32
	v_add_f32_e32 v43, 1.0, v42
	v_sub_f32_e32 v43, v32, v43
	v_add_f32_e32 v43, v33, v43
	v_add_f32_e32 v44, v42, v43
	v_sub_f32_e32 v42, v44, v42
	v_sub_f32_e32 v42, v43, v42
	v_add_f32_e32 v43, 1.0, v32
	v_add_f32_e32 v45, -1.0, v43
	v_sub_f32_e32 v32, v32, v45
	v_add_f32_e32 v32, v33, v32
	v_add_f32_e32 v33, v43, v32
	v_sub_f32_e32 v43, v33, v43
	v_sub_f32_e32 v32, v32, v43
	v_rcp_f32_e32 v43, v33
	v_cvt_f32_i32_e32 v31, v31
	v_cmp_neq_f32_e32 vcc, s27, v30
	v_mul_f32_e32 v45, v44, v43
	v_mul_f32_e32 v46, v33, v45
	v_fma_f32 v47, v45, v33, -v46
	v_fmac_f32_e32 v47, v45, v32
	v_add_f32_e32 v48, v46, v47
	v_sub_f32_e32 v49, v44, v48
	v_sub_f32_e32 v44, v44, v49
	v_sub_f32_e32 v46, v48, v46
	v_sub_f32_e32 v44, v44, v48
	v_add_f32_e32 v42, v42, v44
	v_sub_f32_e32 v44, v46, v47
	v_add_f32_e32 v42, v44, v42
	v_add_f32_e32 v44, v49, v42
	v_mul_f32_e32 v46, v43, v44
	v_mul_f32_e32 v47, v33, v46
	v_fma_f32 v33, v46, v33, -v47
	v_fmac_f32_e32 v33, v46, v32
	v_sub_f32_e32 v32, v49, v44
	v_add_f32_e32 v32, v42, v32
	v_add_f32_e32 v42, v47, v33
	v_sub_f32_e32 v48, v44, v42
	v_sub_f32_e32 v44, v44, v48
	v_sub_f32_e32 v47, v42, v47
;     __device__ __forceinline__ void operator()(const f32x4 (&acc)[2][2][4][2], const Unit& u, int ui, int wr, int wc, int fr, int fq) const {
;     ...
;                         } else if (wc == 0 && fq == 0) {
;                             float z[6] = {y0[0], y0[1], y0[2], y0[3], y1[0], y1[1]};
; #pragma unroll
;                             for (int e = 0; e < 6; ++e) { const float zz = z[e] + bfg[e]; z[e] = fminf(zz, 0.f) - log1pf(__expf(-fabsf(zz))); }
	v_sub_f32_e32 v42, v44, v42
	v_add_f32_e32 v32, v32, v42
	v_sub_f32_e32 v33, v47, v33
	v_add_f32_e32 v32, v33, v32
	v_add_f32_e32 v33, v45, v46
	v_add_f32_e32 v32, v48, v32
	v_sub_f32_e32 v42, v33, v45
	v_mul_f32_e32 v32, v43, v32
	v_sub_f32_e32 v42, v46, v42
	v_add_f32_e32 v32, v42, v32
	v_mul_f32_e32 v45, 0x3f317218, v31
	v_add_f32_e32 v42, v33, v32
	v_fma_f32 v46, v31, s21, -v45
	v_mul_f32_e32 v43, v42, v42
	v_fmac_f32_e32 v46, 0xb102e308, v31
	v_sub_f32_e32 v31, v42, v33
	v_fmamk_f32 v44, v43, 0x3e9b6dac, v217
	v_sub_f32_e32 v31, v32, v31
	v_add_f32_e32 v32, v45, v46
	v_fmaak_f32 v44, v43, v44, 0x3f2aaada
	v_sub_f32_e32 v33, v32, v45
	v_ldexp_f32 v45, v42, 1
	v_mul_f32_e32 v42, v42, v43
	v_mul_f32_e32 v42, v42, v44
	v_add_f32_e32 v43, v45, v42
	v_sub_f32_e32 v44, v43, v45
	v_ldexp_f32 v31, v31, 1
	v_sub_f32_e32 v42, v42, v44
	v_add_f32_e32 v31, v31, v42
	v_add_f32_e32 v42, v43, v31
	v_sub_f32_e32 v43, v42, v43
	v_sub_f32_e32 v31, v31, v43
	v_add_f32_e32 v43, v32, v42
	v_sub_f32_e32 v44, v43, v32
	v_sub_f32_e32 v45, v43, v44
	v_sub_f32_e32 v33, v46, v33
	v_sub_f32_e32 v32, v32, v45
	v_sub_f32_e32 v42, v42, v44
	v_add_f32_e32 v32, v42, v32
	v_add_f32_e32 v42, v33, v31
	v_sub_f32_e32 v44, v42, v33
	v_sub_f32_e32 v45, v42, v44
	v_sub_f32_e32 v33, v33, v45
	v_sub_f32_e32 v31, v31, v44
	v_add_f32_e32 v32, v42, v32
	v_add_f32_e32 v31, v31, v33
	v_add_f32_e32 v33, v43, v32
	v_sub_f32_e32 v42, v33, v43
	v_sub_f32_e32 v32, v32, v42
	v_add_f32_e32 v31, v31, v32
	v_add_f32_e32 v31, v33, v31
	v_cndmask_b32_e32 v31, v230, v31, vcc
	v_cmp_ngt_f32_e32 vcc, -1.0, v30
	s_nop 1
	v_cndmask_b32_e32 v31, v231, v31, vcc
	v_cmp_neq_f32_e32 vcc, -1.0, v30
	s_nop 1
	v_cndmask_b32_e32 v31, v226, v31, vcc
	v_cmp_lt_f32_e64 vcc, |v30|, s33
	s_nop 1
	v_cndmask_b32_e32 v30, v31, v30, vcc
	v_sub_f32_e32 v118, v29, v30
	v_mul_f32_e32 v119, v119, v26
	v_add_f32_e32 v30, v119, v11
	v_min_f32_e32 v29, 0, v30
	v_mul_f32_e64 v30, |v30|, s3
	v_exp_f32_e32 v30, v30
	s_nop 0
	v_add_f32_e32 v32, 1.0, v30
	v_add_f32_e32 v31, -1.0, v32
	v_sub_f32_e32 v33, v31, v32
	v_add_f32_e32 v33, 1.0, v33
	v_sub_f32_e32 v31, v30, v31
	v_add_f32_e32 v33, v31, v33
	v_frexp_mant_f32_e32 v31, v32
	v_cvt_f64_f32_e32 v[42:43], v32
	v_cmp_gt_f32_e32 vcc, s19, v31
	v_frexp_exp_i32_f64_e32 v31, v[42:43]
	s_nop 0
	v_subbrev_co_u32_e32 v31, vcc, 0, v31, vcc
	v_sub_u32_e32 v42, 0, v31
	v_ldexp_f32 v32, v32, v42
	v_ldexp_f32 v33, v33, v42
	v_add_f32_e32 v42, -1.0, v32
	v_add_f32_e32 v43, 1.0, v42
	v_sub_f32_e32 v43, v32, v43
	v_add_f32_e32 v43, v33, v43
	v_add_f32_e32 v44, v42, v43
	v_sub_f32_e32 v42, v44, v42
	v_sub_f32_e32 v42, v43, v42
	v_add_f32_e32 v43, 1.0, v32
	v_add_f32_e32 v45, -1.0, v43
	v_sub_f32_e32 v32, v32, v45
	v_add_f32_e32 v32, v33, v32
	v_add_f32_e32 v33, v43, v32
	v_sub_f32_e32 v43, v33, v43
	v_sub_f32_e32 v32, v32, v43
	v_rcp_f32_e32 v43, v33
	v_cvt_f32_i32_e32 v31, v31
	v_cmp_neq_f32_e32 vcc, s27, v30
	v_mul_f32_e32 v45, v44, v43
	v_mul_f32_e32 v46, v33, v45
	v_fma_f32 v47, v45, v33, -v46
	v_fmac_f32_e32 v47, v45, v32
	v_add_f32_e32 v48, v46, v47
	v_sub_f32_e32 v49, v44, v48
	v_sub_f32_e32 v44, v44, v49
	v_sub_f32_e32 v46, v48, v46
	v_sub_f32_e32 v44, v44, v48
	v_add_f32_e32 v42, v42, v44
	v_sub_f32_e32 v44, v46, v47
	v_add_f32_e32 v42, v44, v42
	v_add_f32_e32 v44, v49, v42
	v_mul_f32_e32 v46, v43, v44
	v_mul_f32_e32 v47, v33, v46
	v_fma_f32 v33, v46, v33, -v47
	v_fmac_f32_e32 v33, v46, v32
	v_sub_f32_e32 v32, v49, v44
	v_add_f32_e32 v32, v42, v32
	v_add_f32_e32 v42, v47, v33
	v_sub_f32_e32 v48, v44, v42
	v_sub_f32_e32 v44, v44, v48
	v_sub_f32_e32 v47, v42, v47
	v_sub_f32_e32 v42, v44, v42
	v_add_f32_e32 v32, v32, v42
	v_sub_f32_e32 v33, v47, v33
	v_add_f32_e32 v32, v33, v32
	v_add_f32_e32 v33, v45, v46
	v_add_f32_e32 v32, v48, v32
	v_sub_f32_e32 v42, v33, v45
	v_mul_f32_e32 v32, v43, v32
	v_sub_f32_e32 v42, v46, v42
	v_add_f32_e32 v32, v42, v32
	v_mul_f32_e32 v45, 0x3f317218, v31
	v_add_f32_e32 v42, v33, v32
	v_fma_f32 v46, v31, s21, -v45
	v_mul_f32_e32 v43, v42, v42
	v_fmac_f32_e32 v46, 0xb102e308, v31
	v_sub_f32_e32 v31, v42, v33
	v_fmamk_f32 v44, v43, 0x3e9b6dac, v217
	v_sub_f32_e32 v31, v32, v31
	v_add_f32_e32 v32, v45, v46
	v_fmaak_f32 v44, v43, v44, 0x3f2aaada
	v_sub_f32_e32 v33, v32, v45
	v_ldexp_f32 v45, v42, 1
	v_mul_f32_e32 v42, v42, v43
	v_mul_f32_e32 v42, v42, v44
	v_add_f32_e32 v43, v45, v42
	v_sub_f32_e32 v44, v43, v45
	v_ldexp_f32 v31, v31, 1
	v_sub_f32_e32 v42, v42, v44
	v_add_f32_e32 v31, v31, v42
	v_add_f32_e32 v42, v43, v31
	v_sub_f32_e32 v43, v42, v43
	v_sub_f32_e32 v31, v31, v43
	v_add_f32_e32 v43, v32, v42
	v_sub_f32_e32 v44, v43, v32
	v_sub_f32_e32 v45, v43, v44
	v_sub_f32_e32 v33, v46, v33
	v_sub_f32_e32 v32, v32, v45
	v_sub_f32_e32 v42, v42, v44
	v_add_f32_e32 v32, v42, v32
	v_add_f32_e32 v42, v33, v31
	v_sub_f32_e32 v44, v42, v33
	v_sub_f32_e32 v45, v42, v44
	v_sub_f32_e32 v33, v33, v45
	v_sub_f32_e32 v31, v31, v44
	v_add_f32_e32 v32, v42, v32
	v_add_f32_e32 v31, v31, v33
	v_add_f32_e32 v33, v43, v32
	v_sub_f32_e32 v42, v33, v43
	v_sub_f32_e32 v32, v32, v42
	v_add_f32_e32 v31, v31, v32
	v_add_f32_e32 v31, v33, v31
	v_cndmask_b32_e32 v31, v230, v31, vcc
	v_cmp_ngt_f32_e32 vcc, -1.0, v30
	s_nop 1
	v_cndmask_b32_e32 v31, v231, v31, vcc
	v_cmp_neq_f32_e32 vcc, -1.0, v30
	s_nop 1
	v_cndmask_b32_e32 v31, v226, v31, vcc
	v_cmp_lt_f32_e64 vcc, |v30|, s33
	s_nop 1
	v_cndmask_b32_e32 v30, v31, v30, vcc
	v_sub_f32_e32 v119, v29, v30
	v_mul_f32_e32 v120, v120, v26
	v_add_f32_e32 v30, v120, v12
	v_min_f32_e32 v29, 0, v30
	v_mul_f32_e64 v30, |v30|, s3
	v_exp_f32_e32 v30, v30
	s_nop 0
	v_add_f32_e32 v32, 1.0, v30
	v_add_f32_e32 v31, -1.0, v32
	v_sub_f32_e32 v33, v31, v32
;     __device__ __forceinline__ void operator()(const f32x4 (&acc)[2][2][4][2], const Unit& u, int ui, int wr, int wc, int fr, int fq) const {
;     ...
;                         } else if (wc == 0 && fq == 0) {
;                             float z[6] = {y0[0], y0[1], y0[2], y0[3], y1[0], y1[1]};
; #pragma unroll
;                             for (int e = 0; e < 6; ++e) { const float zz = z[e] + bfg[e]; z[e] = fminf(zz, 0.f) - log1pf(__expf(-fabsf(zz))); }
	v_add_f32_e32 v33, 1.0, v33
	v_sub_f32_e32 v31, v30, v31
	v_add_f32_e32 v33, v31, v33
	v_frexp_mant_f32_e32 v31, v32
	v_cvt_f64_f32_e32 v[42:43], v32
	v_cmp_gt_f32_e32 vcc, s19, v31
	v_frexp_exp_i32_f64_e32 v31, v[42:43]
	s_nop 0
	v_subbrev_co_u32_e32 v31, vcc, 0, v31, vcc
	v_sub_u32_e32 v42, 0, v31
	v_ldexp_f32 v32, v32, v42
	v_ldexp_f32 v33, v33, v42
	v_add_f32_e32 v42, -1.0, v32
	v_add_f32_e32 v43, 1.0, v42
	v_sub_f32_e32 v43, v32, v43
	v_add_f32_e32 v43, v33, v43
	v_add_f32_e32 v44, v42, v43
	v_sub_f32_e32 v42, v44, v42
	v_sub_f32_e32 v42, v43, v42
	v_add_f32_e32 v43, 1.0, v32
	v_add_f32_e32 v45, -1.0, v43
	v_sub_f32_e32 v32, v32, v45
	v_add_f32_e32 v32, v33, v32
	v_add_f32_e32 v33, v43, v32
	v_sub_f32_e32 v43, v33, v43
	v_sub_f32_e32 v32, v32, v43
	v_rcp_f32_e32 v43, v33
	v_cvt_f32_i32_e32 v31, v31
	v_cmp_neq_f32_e32 vcc, s27, v30
	v_mul_f32_e32 v45, v44, v43
	v_mul_f32_e32 v46, v33, v45
	v_fma_f32 v47, v45, v33, -v46
	v_fmac_f32_e32 v47, v45, v32
	v_add_f32_e32 v48, v46, v47
	v_sub_f32_e32 v49, v44, v48
	v_sub_f32_e32 v44, v44, v49
	v_sub_f32_e32 v46, v48, v46
	v_sub_f32_e32 v44, v44, v48
	v_add_f32_e32 v42, v42, v44
	v_sub_f32_e32 v44, v46, v47
	v_add_f32_e32 v42, v44, v42
	v_add_f32_e32 v44, v49, v42
	v_mul_f32_e32 v46, v43, v44
	v_mul_f32_e32 v47, v33, v46
	v_fma_f32 v33, v46, v33, -v47
	v_fmac_f32_e32 v33, v46, v32
	v_sub_f32_e32 v32, v49, v44
	v_add_f32_e32 v32, v42, v32
	v_add_f32_e32 v42, v47, v33
	v_sub_f32_e32 v48, v44, v42
	v_sub_f32_e32 v44, v44, v48
	v_sub_f32_e32 v47, v42, v47
	v_sub_f32_e32 v42, v44, v42
	v_add_f32_e32 v32, v32, v42
	v_sub_f32_e32 v33, v47, v33
	v_add_f32_e32 v32, v33, v32
	v_add_f32_e32 v33, v45, v46
	v_add_f32_e32 v32, v48, v32
	v_sub_f32_e32 v42, v33, v45
	v_mul_f32_e32 v32, v43, v32
	v_sub_f32_e32 v42, v46, v42
	v_add_f32_e32 v32, v42, v32
	v_mul_f32_e32 v45, 0x3f317218, v31
	v_add_f32_e32 v42, v33, v32
	v_fma_f32 v46, v31, s21, -v45
	v_mul_f32_e32 v43, v42, v42
	v_fmac_f32_e32 v46, 0xb102e308, v31
	v_sub_f32_e32 v31, v42, v33
	v_fmamk_f32 v44, v43, 0x3e9b6dac, v217
	v_sub_f32_e32 v31, v32, v31
	v_add_f32_e32 v32, v45, v46
	v_fmaak_f32 v44, v43, v44, 0x3f2aaada
	v_sub_f32_e32 v33, v32, v45
	v_ldexp_f32 v45, v42, 1
	v_mul_f32_e32 v42, v42, v43
	v_mul_f32_e32 v42, v42, v44
	v_add_f32_e32 v43, v45, v42
	v_sub_f32_e32 v44, v43, v45
	v_ldexp_f32 v31, v31, 1
	v_sub_f32_e32 v42, v42, v44
	v_add_f32_e32 v31, v31, v42
	v_add_f32_e32 v42, v43, v31
	v_sub_f32_e32 v43, v42, v43
	v_sub_f32_e32 v31, v31, v43
	v_add_f32_e32 v43, v32, v42
	v_sub_f32_e32 v44, v43, v32
	v_sub_f32_e32 v45, v43, v44
	v_sub_f32_e32 v33, v46, v33
	v_sub_f32_e32 v32, v32, v45
	v_sub_f32_e32 v42, v42, v44
	v_add_f32_e32 v32, v42, v32
	v_add_f32_e32 v42, v33, v31
	v_sub_f32_e32 v44, v42, v33
	v_sub_f32_e32 v45, v42, v44
	v_sub_f32_e32 v33, v33, v45
	v_sub_f32_e32 v31, v31, v44
	v_add_f32_e32 v32, v42, v32
	v_add_f32_e32 v31, v31, v33
	v_add_f32_e32 v33, v43, v32
	v_sub_f32_e32 v42, v33, v43
	v_sub_f32_e32 v32, v32, v42
	v_add_f32_e32 v31, v31, v32
	v_add_f32_e32 v31, v33, v31
	v_cndmask_b32_e32 v31, v230, v31, vcc
	v_cmp_ngt_f32_e32 vcc, -1.0, v30
	s_nop 1
	v_cndmask_b32_e32 v31, v231, v31, vcc
	v_cmp_neq_f32_e32 vcc, -1.0, v30
	s_nop 1
	v_cndmask_b32_e32 v31, v226, v31, vcc
	v_cmp_lt_f32_e64 vcc, |v30|, s33
	s_nop 1
	v_cndmask_b32_e32 v30, v31, v30, vcc
	v_sub_f32_e32 v120, v29, v30
	v_mul_f32_e32 v121, v121, v26
	v_add_f32_e32 v30, v121, v13
	v_min_f32_e32 v29, 0, v30
	v_mul_f32_e64 v30, |v30|, s3
	v_exp_f32_e32 v30, v30
	s_nop 0
	v_add_f32_e32 v32, 1.0, v30
	v_add_f32_e32 v31, -1.0, v32
	v_sub_f32_e32 v33, v31, v32
	v_add_f32_e32 v33, 1.0, v33
	v_sub_f32_e32 v31, v30, v31
	v_add_f32_e32 v33, v31, v33
	v_frexp_mant_f32_e32 v31, v32
	v_cvt_f64_f32_e32 v[42:43], v32
	v_cmp_gt_f32_e32 vcc, s19, v31
	v_frexp_exp_i32_f64_e32 v31, v[42:43]
	s_nop 0
	v_subbrev_co_u32_e32 v31, vcc, 0, v31, vcc
	v_sub_u32_e32 v42, 0, v31
	v_ldexp_f32 v32, v32, v42
	v_ldexp_f32 v33, v33, v42
	v_add_f32_e32 v42, -1.0, v32
	v_add_f32_e32 v43, 1.0, v42
	v_sub_f32_e32 v43, v32, v43
	v_add_f32_e32 v43, v33, v43
	v_add_f32_e32 v44, v42, v43
	v_sub_f32_e32 v42, v44, v42
	v_sub_f32_e32 v42, v43, v42
	v_add_f32_e32 v43, 1.0, v32
	v_add_f32_e32 v45, -1.0, v43
	v_sub_f32_e32 v32, v32, v45
	v_add_f32_e32 v32, v33, v32
	v_add_f32_e32 v33, v43, v32
	v_sub_f32_e32 v43, v33, v43
	v_sub_f32_e32 v32, v32, v43
	v_rcp_f32_e32 v43, v33
	v_cvt_f32_i32_e32 v31, v31
	v_cmp_neq_f32_e32 vcc, s27, v30
	v_mul_f32_e32 v45, v44, v43
	v_mul_f32_e32 v46, v33, v45
	v_fma_f32 v47, v45, v33, -v46
	v_fmac_f32_e32 v47, v45, v32
	v_add_f32_e32 v48, v46, v47
	v_sub_f32_e32 v49, v44, v48
	v_sub_f32_e32 v44, v44, v49
	v_sub_f32_e32 v46, v48, v46
	v_sub_f32_e32 v44, v44, v48
	v_add_f32_e32 v42, v42, v44
	v_sub_f32_e32 v44, v46, v47
	v_add_f32_e32 v42, v44, v42
	v_add_f32_e32 v44, v49, v42
	v_mul_f32_e32 v46, v43, v44
	v_mul_f32_e32 v47, v33, v46
	v_fma_f32 v33, v46, v33, -v47
	v_fmac_f32_e32 v33, v46, v32
	v_sub_f32_e32 v32, v49, v44
	v_add_f32_e32 v32, v42, v32
	v_add_f32_e32 v42, v47, v33
	v_sub_f32_e32 v48, v44, v42
	v_sub_f32_e32 v44, v44, v48
	v_sub_f32_e32 v47, v42, v47
	v_sub_f32_e32 v42, v44, v42
	v_add_f32_e32 v32, v32, v42
	v_sub_f32_e32 v33, v47, v33
	v_add_f32_e32 v32, v33, v32
	v_add_f32_e32 v33, v45, v46
	v_add_f32_e32 v32, v48, v32
	v_sub_f32_e32 v42, v33, v45
	v_mul_f32_e32 v32, v43, v32
	v_sub_f32_e32 v42, v46, v42
	v_add_f32_e32 v32, v42, v32
	v_mul_f32_e32 v45, 0x3f317218, v31
	v_add_f32_e32 v42, v33, v32
	v_fma_f32 v46, v31, s21, -v45
	v_mul_f32_e32 v43, v42, v42
	v_fmac_f32_e32 v46, 0xb102e308, v31
	v_sub_f32_e32 v31, v42, v33
	v_fmamk_f32 v44, v43, 0x3e9b6dac, v217
;     __device__ __forceinline__ void operator()(const f32x4 (&acc)[2][2][4][2], const Unit& u, int ui, int wr, int wc, int fr, int fq) const {
;     ...
;                         } else if (wc == 0 && fq == 0) {
;                             float z[6] = {y0[0], y0[1], y0[2], y0[3], y1[0], y1[1]};
; #pragma unroll
;                             for (int e = 0; e < 6; ++e) { const float zz = z[e] + bfg[e]; z[e] = fminf(zz, 0.f) - log1pf(__expf(-fabsf(zz))); }
	v_sub_f32_e32 v31, v32, v31
	v_add_f32_e32 v32, v45, v46
	v_fmaak_f32 v44, v43, v44, 0x3f2aaada
	v_sub_f32_e32 v33, v32, v45
	v_ldexp_f32 v45, v42, 1
	v_mul_f32_e32 v42, v42, v43
	v_mul_f32_e32 v42, v42, v44
	v_add_f32_e32 v43, v45, v42
	v_sub_f32_e32 v44, v43, v45
	v_ldexp_f32 v31, v31, 1
	v_sub_f32_e32 v42, v42, v44
	v_add_f32_e32 v31, v31, v42
	v_add_f32_e32 v42, v43, v31
	v_sub_f32_e32 v43, v42, v43
	v_sub_f32_e32 v31, v31, v43
	v_add_f32_e32 v43, v32, v42
	v_sub_f32_e32 v44, v43, v32
	v_sub_f32_e32 v45, v43, v44
	v_sub_f32_e32 v33, v46, v33
	v_sub_f32_e32 v32, v32, v45
	v_sub_f32_e32 v42, v42, v44
	v_add_f32_e32 v32, v42, v32
	v_add_f32_e32 v42, v33, v31
	v_sub_f32_e32 v44, v42, v33
	v_sub_f32_e32 v45, v42, v44
	v_sub_f32_e32 v33, v33, v45
	v_sub_f32_e32 v31, v31, v44
	v_add_f32_e32 v32, v42, v32
	v_add_f32_e32 v31, v31, v33
	v_add_f32_e32 v33, v43, v32
	v_sub_f32_e32 v42, v33, v43
	v_sub_f32_e32 v32, v32, v42
	v_add_f32_e32 v31, v31, v32
	v_add_f32_e32 v31, v33, v31
	v_cndmask_b32_e32 v31, v230, v31, vcc
	v_cmp_ngt_f32_e32 vcc, -1.0, v30
	s_nop 1
	v_cndmask_b32_e32 v31, v231, v31, vcc
	v_cmp_neq_f32_e32 vcc, -1.0, v30
	s_nop 1
	v_cndmask_b32_e32 v31, v226, v31, vcc
	v_cmp_lt_f32_e64 vcc, |v30|, s33
	s_nop 1
	v_cndmask_b32_e32 v30, v31, v30, vcc
	v_sub_f32_e32 v121, v29, v30
	v_mul_f32_e32 v114, v114, v26
	v_add_f32_e32 v30, v114, v14
	v_min_f32_e32 v29, 0, v30
	v_mul_f32_e64 v30, |v30|, s3
	v_exp_f32_e32 v30, v30
	s_nop 0
	v_add_f32_e32 v32, 1.0, v30
	v_add_f32_e32 v31, -1.0, v32
	v_sub_f32_e32 v33, v31, v32
	v_add_f32_e32 v33, 1.0, v33
	v_sub_f32_e32 v31, v30, v31
	v_add_f32_e32 v33, v31, v33
	v_frexp_mant_f32_e32 v31, v32
	v_cvt_f64_f32_e32 v[42:43], v32
	v_cmp_gt_f32_e32 vcc, s19, v31
	v_frexp_exp_i32_f64_e32 v31, v[42:43]
	s_nop 0
	v_subbrev_co_u32_e32 v31, vcc, 0, v31, vcc
	v_sub_u32_e32 v42, 0, v31
	v_ldexp_f32 v32, v32, v42
	v_ldexp_f32 v33, v33, v42
	v_add_f32_e32 v42, -1.0, v32
	v_add_f32_e32 v43, 1.0, v42
	v_sub_f32_e32 v43, v32, v43
	v_add_f32_e32 v43, v33, v43
	v_add_f32_e32 v44, v42, v43
	v_sub_f32_e32 v42, v44, v42
	v_sub_f32_e32 v42, v43, v42
	v_add_f32_e32 v43, 1.0, v32
	v_add_f32_e32 v45, -1.0, v43
	v_sub_f32_e32 v32, v32, v45
	v_add_f32_e32 v32, v33, v32
	v_add_f32_e32 v33, v43, v32
	v_sub_f32_e32 v43, v33, v43
	v_sub_f32_e32 v32, v32, v43
	v_rcp_f32_e32 v43, v33
	v_cvt_f32_i32_e32 v31, v31
	v_cmp_neq_f32_e32 vcc, s27, v30
	v_mul_f32_e32 v45, v44, v43
	v_mul_f32_e32 v46, v33, v45
	v_fma_f32 v47, v45, v33, -v46
	v_fmac_f32_e32 v47, v45, v32
	v_add_f32_e32 v48, v46, v47
	v_sub_f32_e32 v49, v44, v48
	v_sub_f32_e32 v44, v44, v49
	v_sub_f32_e32 v46, v48, v46
	v_sub_f32_e32 v44, v44, v48
	v_add_f32_e32 v42, v42, v44
	v_sub_f32_e32 v44, v46, v47
	v_add_f32_e32 v42, v44, v42
	v_add_f32_e32 v44, v49, v42
	v_mul_f32_e32 v46, v43, v44
	v_mul_f32_e32 v47, v33, v46
	v_fma_f32 v33, v46, v33, -v47
	v_fmac_f32_e32 v33, v46, v32
	v_sub_f32_e32 v32, v49, v44
	v_add_f32_e32 v32, v42, v32
	v_add_f32_e32 v42, v47, v33
	v_sub_f32_e32 v48, v44, v42
	v_sub_f32_e32 v44, v44, v48
	v_sub_f32_e32 v47, v42, v47
	v_sub_f32_e32 v42, v44, v42
	v_add_f32_e32 v32, v32, v42
	v_sub_f32_e32 v33, v47, v33
	v_add_f32_e32 v32, v33, v32
	v_add_f32_e32 v33, v45, v46
	v_add_f32_e32 v32, v48, v32
	v_sub_f32_e32 v42, v33, v45
	v_mul_f32_e32 v32, v43, v32
	v_sub_f32_e32 v42, v46, v42
	v_add_f32_e32 v32, v42, v32
	v_mul_f32_e32 v45, 0x3f317218, v31
	v_add_f32_e32 v42, v33, v32
	v_fma_f32 v46, v31, s21, -v45
	v_mul_f32_e32 v43, v42, v42
	v_fmac_f32_e32 v46, 0xb102e308, v31
	v_sub_f32_e32 v31, v42, v33
	v_fmamk_f32 v44, v43, 0x3e9b6dac, v217
	v_sub_f32_e32 v31, v32, v31
	v_add_f32_e32 v32, v45, v46
	v_fmaak_f32 v44, v43, v44, 0x3f2aaada
	v_sub_f32_e32 v33, v32, v45
	v_ldexp_f32 v45, v42, 1
	v_mul_f32_e32 v42, v42, v43
	v_mul_f32_e32 v42, v42, v44
	v_add_f32_e32 v43, v45, v42
	v_sub_f32_e32 v44, v43, v45
	v_ldexp_f32 v31, v31, 1
	v_sub_f32_e32 v42, v42, v44
	v_add_f32_e32 v31, v31, v42
	v_add_f32_e32 v42, v43, v31
	v_sub_f32_e32 v43, v42, v43
	v_sub_f32_e32 v31, v31, v43
	v_add_f32_e32 v43, v32, v42
	v_sub_f32_e32 v44, v43, v32
	v_sub_f32_e32 v45, v43, v44
	v_sub_f32_e32 v33, v46, v33
	v_sub_f32_e32 v32, v32, v45
	v_sub_f32_e32 v42, v42, v44
	v_add_f32_e32 v32, v42, v32
	v_add_f32_e32 v42, v33, v31
	v_sub_f32_e32 v44, v42, v33
	v_sub_f32_e32 v45, v42, v44
	v_sub_f32_e32 v33, v33, v45
	v_sub_f32_e32 v31, v31, v44
	v_add_f32_e32 v32, v42, v32
	v_add_f32_e32 v31, v31, v33
	v_add_f32_e32 v33, v43, v32
	v_sub_f32_e32 v42, v33, v43
	v_sub_f32_e32 v32, v32, v42
	v_add_f32_e32 v31, v31, v32
	v_add_f32_e32 v31, v33, v31
	v_cndmask_b32_e32 v31, v230, v31, vcc
	v_cmp_ngt_f32_e32 vcc, -1.0, v30
	s_nop 1
	v_cndmask_b32_e32 v31, v231, v31, vcc
	v_cmp_neq_f32_e32 vcc, -1.0, v30
	s_nop 1
	v_cndmask_b32_e32 v31, v226, v31, vcc
	v_cmp_lt_f32_e64 vcc, |v30|, s33
	s_nop 1
	v_cndmask_b32_e32 v30, v31, v30, vcc
	v_sub_f32_e32 v114, v29, v30
	v_mul_f32_e32 v115, v115, v26
	v_add_f32_e32 v30, v115, v15
	v_min_f32_e32 v29, 0, v30
	v_mul_f32_e64 v30, |v30|, s3
	v_exp_f32_e32 v30, v30
	s_nop 0
	v_add_f32_e32 v32, 1.0, v30
	v_add_f32_e32 v31, -1.0, v32
	v_sub_f32_e32 v33, v31, v32
	v_add_f32_e32 v33, 1.0, v33
	v_sub_f32_e32 v31, v30, v31
	v_add_f32_e32 v33, v31, v33
	v_frexp_mant_f32_e32 v31, v32
	v_cvt_f64_f32_e32 v[42:43], v32
	v_cmp_gt_f32_e32 vcc, s19, v31
	v_frexp_exp_i32_f64_e32 v31, v[42:43]
	s_nop 0
	v_subbrev_co_u32_e32 v31, vcc, 0, v31, vcc
	v_sub_u32_e32 v42, 0, v31
	v_ldexp_f32 v32, v32, v42
	v_ldexp_f32 v33, v33, v42
	v_add_f32_e32 v42, -1.0, v32
	v_add_f32_e32 v43, 1.0, v42
	v_sub_f32_e32 v43, v32, v43
	v_add_f32_e32 v43, v33, v43
	v_add_f32_e32 v44, v42, v43
;     __device__ __forceinline__ void operator()(const f32x4 (&acc)[2][2][4][2], const Unit& u, int ui, int wr, int wc, int fr, int fq) const {
;     ...
;                         } else if (wc == 0 && fq == 0) {
;                             float z[6] = {y0[0], y0[1], y0[2], y0[3], y1[0], y1[1]};
; #pragma unroll
;                             for (int e = 0; e < 6; ++e) { const float zz = z[e] + bfg[e]; z[e] = fminf(zz, 0.f) - log1pf(__expf(-fabsf(zz))); }
	v_sub_f32_e32 v42, v44, v42
	v_sub_f32_e32 v42, v43, v42
	v_add_f32_e32 v43, 1.0, v32
	v_add_f32_e32 v45, -1.0, v43
	v_sub_f32_e32 v32, v32, v45
	v_add_f32_e32 v32, v33, v32
	v_add_f32_e32 v33, v43, v32
	v_sub_f32_e32 v43, v33, v43
	v_sub_f32_e32 v32, v32, v43
	v_rcp_f32_e32 v43, v33
	v_cvt_f32_i32_e32 v31, v31
	v_cmp_neq_f32_e32 vcc, s27, v30
	v_mul_f32_e32 v45, v44, v43
	v_mul_f32_e32 v46, v33, v45
	v_fma_f32 v47, v45, v33, -v46
	v_fmac_f32_e32 v47, v45, v32
	v_add_f32_e32 v48, v46, v47
	v_sub_f32_e32 v49, v44, v48
	v_sub_f32_e32 v44, v44, v49
	v_sub_f32_e32 v46, v48, v46
	v_sub_f32_e32 v44, v44, v48
	v_add_f32_e32 v42, v42, v44
	v_sub_f32_e32 v44, v46, v47
	v_add_f32_e32 v42, v44, v42
	v_add_f32_e32 v44, v49, v42
	v_mul_f32_e32 v46, v43, v44
	v_mul_f32_e32 v47, v33, v46
	v_fma_f32 v33, v46, v33, -v47
	v_fmac_f32_e32 v33, v46, v32
	v_sub_f32_e32 v32, v49, v44
	v_add_f32_e32 v32, v42, v32
	v_add_f32_e32 v42, v47, v33
	v_sub_f32_e32 v48, v44, v42
	v_sub_f32_e32 v44, v44, v48
	v_sub_f32_e32 v47, v42, v47
	v_sub_f32_e32 v42, v44, v42
	v_add_f32_e32 v32, v32, v42
	v_sub_f32_e32 v33, v47, v33
	v_add_f32_e32 v32, v33, v32
	v_add_f32_e32 v33, v45, v46
	v_add_f32_e32 v32, v48, v32
	v_sub_f32_e32 v42, v33, v45
	v_mul_f32_e32 v32, v43, v32
	v_sub_f32_e32 v42, v46, v42
	v_add_f32_e32 v32, v42, v32
	v_mul_f32_e32 v45, 0x3f317218, v31
	v_add_f32_e32 v42, v33, v32
	v_fma_f32 v46, v31, s21, -v45
	v_mul_f32_e32 v43, v42, v42
	v_fmac_f32_e32 v46, 0xb102e308, v31
	v_sub_f32_e32 v31, v42, v33
	v_fmamk_f32 v44, v43, 0x3e9b6dac, v217
	v_sub_f32_e32 v31, v32, v31
	v_add_f32_e32 v32, v45, v46
	v_fmaak_f32 v44, v43, v44, 0x3f2aaada
	v_sub_f32_e32 v33, v32, v45
	v_ldexp_f32 v45, v42, 1
	v_mul_f32_e32 v42, v42, v43
	v_mul_f32_e32 v42, v42, v44
	v_add_f32_e32 v43, v45, v42
	v_sub_f32_e32 v44, v43, v45
	v_ldexp_f32 v31, v31, 1
	v_sub_f32_e32 v42, v42, v44
	v_add_f32_e32 v31, v31, v42
	v_add_f32_e32 v42, v43, v31
	v_sub_f32_e32 v43, v42, v43
	v_sub_f32_e32 v31, v31, v43
	v_add_f32_e32 v43, v32, v42
	v_sub_f32_e32 v44, v43, v32
	v_sub_f32_e32 v45, v43, v44
	v_sub_f32_e32 v33, v46, v33
	v_sub_f32_e32 v32, v32, v45
	v_sub_f32_e32 v42, v42, v44
	v_add_f32_e32 v32, v42, v32
	v_add_f32_e32 v42, v33, v31
	v_sub_f32_e32 v44, v42, v33
	v_sub_f32_e32 v45, v42, v44
	v_sub_f32_e32 v33, v33, v45
	v_sub_f32_e32 v31, v31, v44
	v_add_f32_e32 v32, v42, v32
	v_add_f32_e32 v31, v31, v33
	v_add_f32_e32 v33, v43, v32
	v_sub_f32_e32 v42, v33, v43
	v_sub_f32_e32 v32, v32, v42
	v_add_f32_e32 v31, v31, v32
	v_add_f32_e32 v31, v33, v31
	v_cndmask_b32_e32 v31, v230, v31, vcc
	v_cmp_ngt_f32_e32 vcc, -1.0, v30
	s_nop 1
	v_cndmask_b32_e32 v31, v231, v31, vcc
	v_cmp_neq_f32_e32 vcc, -1.0, v30
	s_nop 1
	v_cndmask_b32_e32 v31, v226, v31, vcc
	v_cmp_lt_f32_e64 vcc, |v30|, s33
	s_nop 1
	v_cndmask_b32_e32 v30, v31, v30, vcc
	v_sub_f32_e32 v115, v29, v30
	v_mul_f32_e32 v102, v102, v27
	v_add_f32_e32 v30, v102, v10
	v_min_f32_e32 v29, 0, v30
	v_mul_f32_e64 v30, |v30|, s3
	v_exp_f32_e32 v30, v30
	s_nop 0
	v_add_f32_e32 v32, 1.0, v30
	v_add_f32_e32 v31, -1.0, v32
	v_sub_f32_e32 v33, v31, v32
	v_add_f32_e32 v33, 1.0, v33
	v_sub_f32_e32 v31, v30, v31
	v_add_f32_e32 v33, v31, v33
	v_frexp_mant_f32_e32 v31, v32
	v_cvt_f64_f32_e32 v[42:43], v32
	v_cmp_gt_f32_e32 vcc, s19, v31
	v_frexp_exp_i32_f64_e32 v31, v[42:43]
	s_nop 0
	v_subbrev_co_u32_e32 v31, vcc, 0, v31, vcc
	v_sub_u32_e32 v42, 0, v31
	v_ldexp_f32 v32, v32, v42
	v_ldexp_f32 v33, v33, v42
	v_add_f32_e32 v42, -1.0, v32
	v_add_f32_e32 v43, 1.0, v42
	v_sub_f32_e32 v43, v32, v43
	v_add_f32_e32 v43, v33, v43
	v_add_f32_e32 v44, v42, v43
	v_sub_f32_e32 v42, v44, v42
	v_sub_f32_e32 v42, v43, v42
	v_add_f32_e32 v43, 1.0, v32
	v_add_f32_e32 v45, -1.0, v43
	v_sub_f32_e32 v32, v32, v45
	v_add_f32_e32 v32, v33, v32
	v_add_f32_e32 v33, v43, v32
	v_sub_f32_e32 v43, v33, v43
	v_sub_f32_e32 v32, v32, v43
	v_rcp_f32_e32 v43, v33
	v_cvt_f32_i32_e32 v31, v31
	v_cmp_neq_f32_e32 vcc, s27, v30
	v_mul_f32_e32 v45, v44, v43
	v_mul_f32_e32 v46, v33, v45
	v_fma_f32 v47, v45, v33, -v46
	v_fmac_f32_e32 v47, v45, v32
	v_add_f32_e32 v48, v46, v47
	v_sub_f32_e32 v49, v44, v48
	v_sub_f32_e32 v44, v44, v49
	v_sub_f32_e32 v46, v48, v46
	v_sub_f32_e32 v44, v44, v48
	v_add_f32_e32 v42, v42, v44
	v_sub_f32_e32 v44, v46, v47
	v_add_f32_e32 v42, v44, v42
	v_add_f32_e32 v44, v49, v42
	v_mul_f32_e32 v46, v43, v44
	v_mul_f32_e32 v47, v33, v46
	v_fma_f32 v33, v46, v33, -v47
	v_fmac_f32_e32 v33, v46, v32
	v_sub_f32_e32 v32, v49, v44
	v_add_f32_e32 v32, v42, v32
	v_add_f32_e32 v42, v47, v33
	v_sub_f32_e32 v48, v44, v42
	v_sub_f32_e32 v44, v44, v48
	v_sub_f32_e32 v47, v42, v47
	v_sub_f32_e32 v42, v44, v42
	v_add_f32_e32 v32, v32, v42
	v_sub_f32_e32 v33, v47, v33
	v_add_f32_e32 v32, v33, v32
	v_add_f32_e32 v33, v45, v46
	v_add_f32_e32 v32, v48, v32
	v_sub_f32_e32 v42, v33, v45
	v_mul_f32_e32 v32, v43, v32
	v_sub_f32_e32 v42, v46, v42
	v_add_f32_e32 v32, v42, v32
	v_mul_f32_e32 v45, 0x3f317218, v31
	v_add_f32_e32 v42, v33, v32
	v_fma_f32 v46, v31, s21, -v45
	v_mul_f32_e32 v43, v42, v42
	v_fmac_f32_e32 v46, 0xb102e308, v31
	v_sub_f32_e32 v31, v42, v33
	v_fmamk_f32 v44, v43, 0x3e9b6dac, v217
	v_sub_f32_e32 v31, v32, v31
	v_add_f32_e32 v32, v45, v46
	v_fmaak_f32 v44, v43, v44, 0x3f2aaada
	v_sub_f32_e32 v33, v32, v45
	v_ldexp_f32 v45, v42, 1
	v_mul_f32_e32 v42, v42, v43
	v_mul_f32_e32 v42, v42, v44
	v_add_f32_e32 v43, v45, v42
	v_sub_f32_e32 v44, v43, v45
	v_ldexp_f32 v31, v31, 1
	v_sub_f32_e32 v42, v42, v44
	v_add_f32_e32 v31, v31, v42
	v_add_f32_e32 v42, v43, v31
	v_sub_f32_e32 v43, v42, v43
	v_sub_f32_e32 v31, v31, v43
	v_add_f32_e32 v43, v32, v42
	v_sub_f32_e32 v44, v43, v32
	v_sub_f32_e32 v45, v43, v44
;     __device__ __forceinline__ void operator()(const f32x4 (&acc)[2][2][4][2], const Unit& u, int ui, int wr, int wc, int fr, int fq) const {
;     ...
;                         } else if (wc == 0 && fq == 0) {
;                             float z[6] = {y0[0], y0[1], y0[2], y0[3], y1[0], y1[1]};
; #pragma unroll
;                             for (int e = 0; e < 6; ++e) { const float zz = z[e] + bfg[e]; z[e] = fminf(zz, 0.f) - log1pf(__expf(-fabsf(zz))); }
	v_sub_f32_e32 v33, v46, v33
	v_sub_f32_e32 v32, v32, v45
	v_sub_f32_e32 v42, v42, v44
	v_add_f32_e32 v32, v42, v32
	v_add_f32_e32 v42, v33, v31
	v_sub_f32_e32 v44, v42, v33
	v_sub_f32_e32 v45, v42, v44
	v_sub_f32_e32 v33, v33, v45
	v_sub_f32_e32 v31, v31, v44
	v_add_f32_e32 v32, v42, v32
	v_add_f32_e32 v31, v31, v33
	v_add_f32_e32 v33, v43, v32
	v_sub_f32_e32 v42, v33, v43
	v_sub_f32_e32 v32, v32, v42
	v_add_f32_e32 v31, v31, v32
	v_add_f32_e32 v31, v33, v31
	v_cndmask_b32_e32 v31, v230, v31, vcc
	v_cmp_ngt_f32_e32 vcc, -1.0, v30
	s_nop 1
	v_cndmask_b32_e32 v31, v231, v31, vcc
	v_cmp_neq_f32_e32 vcc, -1.0, v30
	s_nop 1
	v_cndmask_b32_e32 v31, v226, v31, vcc
	v_cmp_lt_f32_e64 vcc, |v30|, s33
	s_nop 1
	v_cndmask_b32_e32 v30, v31, v30, vcc
	v_sub_f32_e32 v102, v29, v30
	v_mul_f32_e32 v103, v103, v27
	v_add_f32_e32 v30, v103, v11
	v_min_f32_e32 v29, 0, v30
	v_mul_f32_e64 v30, |v30|, s3
	v_exp_f32_e32 v30, v30
	s_nop 0
	v_add_f32_e32 v32, 1.0, v30
	v_add_f32_e32 v31, -1.0, v32
	v_sub_f32_e32 v33, v31, v32
	v_add_f32_e32 v33, 1.0, v33
	v_sub_f32_e32 v31, v30, v31
	v_add_f32_e32 v33, v31, v33
	v_frexp_mant_f32_e32 v31, v32
	v_cvt_f64_f32_e32 v[42:43], v32
	v_cmp_gt_f32_e32 vcc, s19, v31
	v_frexp_exp_i32_f64_e32 v31, v[42:43]
	s_nop 0
	v_subbrev_co_u32_e32 v31, vcc, 0, v31, vcc
	v_sub_u32_e32 v42, 0, v31
	v_ldexp_f32 v32, v32, v42
	v_ldexp_f32 v33, v33, v42
	v_add_f32_e32 v42, -1.0, v32
	v_add_f32_e32 v43, 1.0, v42
	v_sub_f32_e32 v43, v32, v43
	v_add_f32_e32 v43, v33, v43
	v_add_f32_e32 v44, v42, v43
	v_sub_f32_e32 v42, v44, v42
	v_sub_f32_e32 v42, v43, v42
	v_add_f32_e32 v43, 1.0, v32
	v_add_f32_e32 v45, -1.0, v43
	v_sub_f32_e32 v32, v32, v45
	v_add_f32_e32 v32, v33, v32
	v_add_f32_e32 v33, v43, v32
	v_sub_f32_e32 v43, v33, v43
	v_sub_f32_e32 v32, v32, v43
	v_rcp_f32_e32 v43, v33
	v_cvt_f32_i32_e32 v31, v31
	v_cmp_neq_f32_e32 vcc, s27, v30
	v_mul_f32_e32 v45, v44, v43
	v_mul_f32_e32 v46, v33, v45
	v_fma_f32 v47, v45, v33, -v46
	v_fmac_f32_e32 v47, v45, v32
	v_add_f32_e32 v48, v46, v47
	v_sub_f32_e32 v49, v44, v48
	v_sub_f32_e32 v44, v44, v49
	v_sub_f32_e32 v46, v48, v46
	v_sub_f32_e32 v44, v44, v48
	v_add_f32_e32 v42, v42, v44
	v_sub_f32_e32 v44, v46, v47
	v_add_f32_e32 v42, v44, v42
	v_add_f32_e32 v44, v49, v42
	v_mul_f32_e32 v46, v43, v44
	v_mul_f32_e32 v47, v33, v46
	v_fma_f32 v33, v46, v33, -v47
	v_fmac_f32_e32 v33, v46, v32
	v_sub_f32_e32 v32, v49, v44
	v_add_f32_e32 v32, v42, v32
	v_add_f32_e32 v42, v47, v33
	v_sub_f32_e32 v48, v44, v42
	v_sub_f32_e32 v44, v44, v48
	v_sub_f32_e32 v47, v42, v47
	v_sub_f32_e32 v42, v44, v42
	v_add_f32_e32 v32, v32, v42
	v_sub_f32_e32 v33, v47, v33
	v_add_f32_e32 v32, v33, v32
	v_add_f32_e32 v33, v45, v46
	v_add_f32_e32 v32, v48, v32
	v_sub_f32_e32 v42, v33, v45
	v_mul_f32_e32 v32, v43, v32
	v_sub_f32_e32 v42, v46, v42
	v_add_f32_e32 v32, v42, v32
	v_mul_f32_e32 v45, 0x3f317218, v31
	v_add_f32_e32 v42, v33, v32
	v_fma_f32 v46, v31, s21, -v45
	v_mul_f32_e32 v43, v42, v42
	v_fmac_f32_e32 v46, 0xb102e308, v31
	v_sub_f32_e32 v31, v42, v33
	v_fmamk_f32 v44, v43, 0x3e9b6dac, v217
	v_sub_f32_e32 v31, v32, v31
	v_add_f32_e32 v32, v45, v46
	v_fmaak_f32 v44, v43, v44, 0x3f2aaada
	v_sub_f32_e32 v33, v32, v45
	v_ldexp_f32 v45, v42, 1
	v_mul_f32_e32 v42, v42, v43
	v_mul_f32_e32 v42, v42, v44
	v_add_f32_e32 v43, v45, v42
	v_sub_f32_e32 v44, v43, v45
	v_ldexp_f32 v31, v31, 1
	v_sub_f32_e32 v42, v42, v44
	v_add_f32_e32 v31, v31, v42
	v_add_f32_e32 v42, v43, v31
	v_sub_f32_e32 v43, v42, v43
	v_sub_f32_e32 v31, v31, v43
	v_add_f32_e32 v43, v32, v42
	v_sub_f32_e32 v44, v43, v32
	v_sub_f32_e32 v45, v43, v44
	v_sub_f32_e32 v33, v46, v33
	v_sub_f32_e32 v32, v32, v45
	v_sub_f32_e32 v42, v42, v44
	v_add_f32_e32 v32, v42, v32
	v_add_f32_e32 v42, v33, v31
	v_sub_f32_e32 v44, v42, v33
	v_sub_f32_e32 v45, v42, v44
	v_sub_f32_e32 v33, v33, v45
	v_sub_f32_e32 v31, v31, v44
	v_add_f32_e32 v32, v42, v32
	v_add_f32_e32 v31, v31, v33
	v_add_f32_e32 v33, v43, v32
	v_sub_f32_e32 v42, v33, v43
	v_sub_f32_e32 v32, v32, v42
	v_add_f32_e32 v31, v31, v32
	v_add_f32_e32 v31, v33, v31
	v_cndmask_b32_e32 v31, v230, v31, vcc
	v_cmp_ngt_f32_e32 vcc, -1.0, v30
	s_nop 1
	v_cndmask_b32_e32 v31, v231, v31, vcc
	v_cmp_neq_f32_e32 vcc, -1.0, v30
	s_nop 1
	v_cndmask_b32_e32 v31, v226, v31, vcc
	v_cmp_lt_f32_e64 vcc, |v30|, s33
	s_nop 1
	v_cndmask_b32_e32 v30, v31, v30, vcc
	v_sub_f32_e32 v103, v29, v30
	v_mul_f32_e32 v104, v104, v27
	v_add_f32_e32 v30, v104, v12
	v_min_f32_e32 v29, 0, v30
	v_mul_f32_e64 v30, |v30|, s3
	v_exp_f32_e32 v30, v30
	s_nop 0
	v_add_f32_e32 v32, 1.0, v30
	v_add_f32_e32 v31, -1.0, v32
	v_sub_f32_e32 v33, v31, v32
	v_add_f32_e32 v33, 1.0, v33
	v_sub_f32_e32 v31, v30, v31
	v_add_f32_e32 v33, v31, v33
	v_frexp_mant_f32_e32 v31, v32
	v_cvt_f64_f32_e32 v[42:43], v32
	v_cmp_gt_f32_e32 vcc, s19, v31
	v_frexp_exp_i32_f64_e32 v31, v[42:43]
	s_nop 0
	v_subbrev_co_u32_e32 v31, vcc, 0, v31, vcc
	v_sub_u32_e32 v42, 0, v31
	v_ldexp_f32 v32, v32, v42
	v_ldexp_f32 v33, v33, v42
	v_add_f32_e32 v42, -1.0, v32
	v_add_f32_e32 v43, 1.0, v42
	v_sub_f32_e32 v43, v32, v43
	v_add_f32_e32 v43, v33, v43
	v_add_f32_e32 v44, v42, v43
	v_sub_f32_e32 v42, v44, v42
	v_sub_f32_e32 v42, v43, v42
	v_add_f32_e32 v43, 1.0, v32
	v_add_f32_e32 v45, -1.0, v43
	v_sub_f32_e32 v32, v32, v45
	v_add_f32_e32 v32, v33, v32
	v_add_f32_e32 v33, v43, v32
	v_sub_f32_e32 v43, v33, v43
	v_sub_f32_e32 v32, v32, v43
	v_rcp_f32_e32 v43, v33
	v_cvt_f32_i32_e32 v31, v31
	v_cmp_neq_f32_e32 vcc, s27, v30
	v_mul_f32_e32 v45, v44, v43
	v_mul_f32_e32 v46, v33, v45
	v_fma_f32 v47, v45, v33, -v46
	v_fmac_f32_e32 v47, v45, v32
	v_add_f32_e32 v48, v46, v47
	v_sub_f32_e32 v49, v44, v48
;     __device__ __forceinline__ void operator()(const f32x4 (&acc)[2][2][4][2], const Unit& u, int ui, int wr, int wc, int fr, int fq) const {
;     ...
;                         } else if (wc == 0 && fq == 0) {
;                             float z[6] = {y0[0], y0[1], y0[2], y0[3], y1[0], y1[1]};
; #pragma unroll
;                             for (int e = 0; e < 6; ++e) { const float zz = z[e] + bfg[e]; z[e] = fminf(zz, 0.f) - log1pf(__expf(-fabsf(zz))); }
	v_sub_f32_e32 v44, v44, v49
	v_sub_f32_e32 v46, v48, v46
	v_sub_f32_e32 v44, v44, v48
	v_add_f32_e32 v42, v42, v44
	v_sub_f32_e32 v44, v46, v47
	v_add_f32_e32 v42, v44, v42
	v_add_f32_e32 v44, v49, v42
	v_mul_f32_e32 v46, v43, v44
	v_mul_f32_e32 v47, v33, v46
	v_fma_f32 v33, v46, v33, -v47
	v_fmac_f32_e32 v33, v46, v32
	v_sub_f32_e32 v32, v49, v44
	v_add_f32_e32 v32, v42, v32
	v_add_f32_e32 v42, v47, v33
	v_sub_f32_e32 v48, v44, v42
	v_sub_f32_e32 v44, v44, v48
	v_sub_f32_e32 v47, v42, v47
	v_sub_f32_e32 v42, v44, v42
	v_add_f32_e32 v32, v32, v42
	v_sub_f32_e32 v33, v47, v33
	v_add_f32_e32 v32, v33, v32
	v_add_f32_e32 v33, v45, v46
	v_add_f32_e32 v32, v48, v32
	v_sub_f32_e32 v42, v33, v45
	v_mul_f32_e32 v32, v43, v32
	v_sub_f32_e32 v42, v46, v42
	v_add_f32_e32 v32, v42, v32
	v_mul_f32_e32 v45, 0x3f317218, v31
	v_add_f32_e32 v42, v33, v32
	v_fma_f32 v46, v31, s21, -v45
	v_mul_f32_e32 v43, v42, v42
	v_fmac_f32_e32 v46, 0xb102e308, v31
	v_sub_f32_e32 v31, v42, v33
	v_fmamk_f32 v44, v43, 0x3e9b6dac, v217
	v_sub_f32_e32 v31, v32, v31
	v_add_f32_e32 v32, v45, v46
	v_fmaak_f32 v44, v43, v44, 0x3f2aaada
	v_sub_f32_e32 v33, v32, v45
	v_ldexp_f32 v45, v42, 1
	v_mul_f32_e32 v42, v42, v43
	v_mul_f32_e32 v42, v42, v44
	v_add_f32_e32 v43, v45, v42
	v_sub_f32_e32 v44, v43, v45
	v_ldexp_f32 v31, v31, 1
	v_sub_f32_e32 v42, v42, v44
	v_add_f32_e32 v31, v31, v42
	v_add_f32_e32 v42, v43, v31
	v_sub_f32_e32 v43, v42, v43
	v_sub_f32_e32 v31, v31, v43
	v_add_f32_e32 v43, v32, v42
	v_sub_f32_e32 v44, v43, v32
	v_sub_f32_e32 v45, v43, v44
	v_sub_f32_e32 v33, v46, v33
	v_sub_f32_e32 v32, v32, v45
	v_sub_f32_e32 v42, v42, v44
	v_add_f32_e32 v32, v42, v32
	v_add_f32_e32 v42, v33, v31
	v_sub_f32_e32 v44, v42, v33
	v_sub_f32_e32 v45, v42, v44
	v_sub_f32_e32 v33, v33, v45
	v_sub_f32_e32 v31, v31, v44
	v_add_f32_e32 v32, v42, v32
	v_add_f32_e32 v31, v31, v33
	v_add_f32_e32 v33, v43, v32
	v_sub_f32_e32 v42, v33, v43
	v_sub_f32_e32 v32, v32, v42
	v_add_f32_e32 v31, v31, v32
	v_add_f32_e32 v31, v33, v31
	v_cndmask_b32_e32 v31, v230, v31, vcc
	v_cmp_ngt_f32_e32 vcc, -1.0, v30
	s_nop 1
	v_cndmask_b32_e32 v31, v231, v31, vcc
	v_cmp_neq_f32_e32 vcc, -1.0, v30
	s_nop 1
	v_cndmask_b32_e32 v31, v226, v31, vcc
	v_cmp_lt_f32_e64 vcc, |v30|, s33
	s_nop 1
	v_cndmask_b32_e32 v30, v31, v30, vcc
	v_sub_f32_e32 v104, v29, v30
	v_mul_f32_e32 v105, v105, v27
	v_add_f32_e32 v30, v105, v13
	v_min_f32_e32 v29, 0, v30
	v_mul_f32_e64 v30, |v30|, s3
	v_exp_f32_e32 v30, v30
	s_nop 0
	v_add_f32_e32 v32, 1.0, v30
	v_add_f32_e32 v31, -1.0, v32
	v_sub_f32_e32 v33, v31, v32
	v_add_f32_e32 v33, 1.0, v33
	v_sub_f32_e32 v31, v30, v31
	v_add_f32_e32 v33, v31, v33
	v_frexp_mant_f32_e32 v31, v32
	v_cvt_f64_f32_e32 v[42:43], v32
	v_cmp_gt_f32_e32 vcc, s19, v31
	v_frexp_exp_i32_f64_e32 v31, v[42:43]
	s_nop 0
	v_subbrev_co_u32_e32 v31, vcc, 0, v31, vcc
	v_sub_u32_e32 v42, 0, v31
	v_ldexp_f32 v32, v32, v42
	v_ldexp_f32 v33, v33, v42
	v_add_f32_e32 v42, -1.0, v32
	v_add_f32_e32 v43, 1.0, v42
	v_sub_f32_e32 v43, v32, v43
	v_add_f32_e32 v43, v33, v43
	v_add_f32_e32 v44, v42, v43
	v_sub_f32_e32 v42, v44, v42
	v_sub_f32_e32 v42, v43, v42
	v_add_f32_e32 v43, 1.0, v32
	v_add_f32_e32 v45, -1.0, v43
	v_sub_f32_e32 v32, v32, v45
	v_add_f32_e32 v32, v33, v32
	v_add_f32_e32 v33, v43, v32
	v_sub_f32_e32 v43, v33, v43
	v_sub_f32_e32 v32, v32, v43
	v_rcp_f32_e32 v43, v33
	v_cvt_f32_i32_e32 v31, v31
	v_cmp_neq_f32_e32 vcc, s27, v30
	v_mul_f32_e32 v45, v44, v43
	v_mul_f32_e32 v46, v33, v45
	v_fma_f32 v47, v45, v33, -v46
	v_fmac_f32_e32 v47, v45, v32
	v_add_f32_e32 v48, v46, v47
	v_sub_f32_e32 v49, v44, v48
	v_sub_f32_e32 v44, v44, v49
	v_sub_f32_e32 v46, v48, v46
	v_sub_f32_e32 v44, v44, v48
	v_add_f32_e32 v42, v42, v44
	v_sub_f32_e32 v44, v46, v47
	v_add_f32_e32 v42, v44, v42
	v_add_f32_e32 v44, v49, v42
	v_mul_f32_e32 v46, v43, v44
	v_mul_f32_e32 v47, v33, v46
	v_fma_f32 v33, v46, v33, -v47
	v_fmac_f32_e32 v33, v46, v32
	v_sub_f32_e32 v32, v49, v44
	v_add_f32_e32 v32, v42, v32
	v_add_f32_e32 v42, v47, v33
	v_sub_f32_e32 v48, v44, v42
	v_sub_f32_e32 v44, v44, v48
	v_sub_f32_e32 v47, v42, v47
	v_sub_f32_e32 v42, v44, v42
	v_add_f32_e32 v32, v32, v42
	v_sub_f32_e32 v33, v47, v33
	v_add_f32_e32 v32, v33, v32
	v_add_f32_e32 v33, v45, v46
	v_add_f32_e32 v32, v48, v32
	v_sub_f32_e32 v42, v33, v45
	v_mul_f32_e32 v32, v43, v32
	v_sub_f32_e32 v42, v46, v42
	v_add_f32_e32 v32, v42, v32
	v_mul_f32_e32 v45, 0x3f317218, v31
	v_add_f32_e32 v42, v33, v32
	v_fma_f32 v46, v31, s21, -v45
	v_mul_f32_e32 v43, v42, v42
	v_fmac_f32_e32 v46, 0xb102e308, v31
	v_sub_f32_e32 v31, v42, v33
	v_fmamk_f32 v44, v43, 0x3e9b6dac, v217
	v_sub_f32_e32 v31, v32, v31
	v_add_f32_e32 v32, v45, v46
	v_fmaak_f32 v44, v43, v44, 0x3f2aaada
	v_sub_f32_e32 v33, v32, v45
	v_ldexp_f32 v45, v42, 1
	v_mul_f32_e32 v42, v42, v43
	v_mul_f32_e32 v42, v42, v44
	v_add_f32_e32 v43, v45, v42
	v_sub_f32_e32 v44, v43, v45
	v_ldexp_f32 v31, v31, 1
	v_sub_f32_e32 v42, v42, v44
	v_add_f32_e32 v31, v31, v42
	v_add_f32_e32 v42, v43, v31
	v_sub_f32_e32 v43, v42, v43
	v_sub_f32_e32 v31, v31, v43
	v_add_f32_e32 v43, v32, v42
	v_sub_f32_e32 v44, v43, v32
	v_sub_f32_e32 v45, v43, v44
	v_sub_f32_e32 v33, v46, v33
	v_sub_f32_e32 v32, v32, v45
	v_sub_f32_e32 v42, v42, v44
	v_add_f32_e32 v32, v42, v32
	v_add_f32_e32 v42, v33, v31
	v_sub_f32_e32 v44, v42, v33
	v_sub_f32_e32 v45, v42, v44
	v_sub_f32_e32 v33, v33, v45
	v_sub_f32_e32 v31, v31, v44
	v_add_f32_e32 v32, v42, v32
	v_add_f32_e32 v31, v31, v33
	v_add_f32_e32 v33, v43, v32
	v_sub_f32_e32 v42, v33, v43
	v_sub_f32_e32 v32, v32, v42
	v_add_f32_e32 v31, v31, v32
	v_add_f32_e32 v31, v33, v31
	v_cndmask_b32_e32 v31, v230, v31, vcc
;     __device__ __forceinline__ void operator()(const f32x4 (&acc)[2][2][4][2], const Unit& u, int ui, int wr, int wc, int fr, int fq) const {
;     ...
;                         } else if (wc == 0 && fq == 0) {
;                             float z[6] = {y0[0], y0[1], y0[2], y0[3], y1[0], y1[1]};
; #pragma unroll
;                             for (int e = 0; e < 6; ++e) { const float zz = z[e] + bfg[e]; z[e] = fminf(zz, 0.f) - log1pf(__expf(-fabsf(zz))); }
	v_cmp_ngt_f32_e32 vcc, -1.0, v30
	s_nop 1
	v_cndmask_b32_e32 v31, v231, v31, vcc
	v_cmp_neq_f32_e32 vcc, -1.0, v30
	s_nop 1
	v_cndmask_b32_e32 v31, v226, v31, vcc
	v_cmp_lt_f32_e64 vcc, |v30|, s33
	s_nop 1
	v_cndmask_b32_e32 v30, v31, v30, vcc
	v_sub_f32_e32 v105, v29, v30
	v_mul_f32_e32 v98, v98, v27
	v_add_f32_e32 v30, v98, v14
	v_min_f32_e32 v29, 0, v30
	v_mul_f32_e64 v30, |v30|, s3
	v_exp_f32_e32 v30, v30
	s_nop 0
	v_add_f32_e32 v32, 1.0, v30
	v_add_f32_e32 v31, -1.0, v32
	v_sub_f32_e32 v33, v31, v32
	v_add_f32_e32 v33, 1.0, v33
	v_sub_f32_e32 v31, v30, v31
	v_add_f32_e32 v33, v31, v33
	v_frexp_mant_f32_e32 v31, v32
	v_cvt_f64_f32_e32 v[42:43], v32
	v_cmp_gt_f32_e32 vcc, s19, v31
	v_frexp_exp_i32_f64_e32 v31, v[42:43]
	s_nop 0
	v_subbrev_co_u32_e32 v31, vcc, 0, v31, vcc
	v_sub_u32_e32 v42, 0, v31
	v_ldexp_f32 v32, v32, v42
	v_ldexp_f32 v33, v33, v42
	v_add_f32_e32 v42, -1.0, v32
	v_add_f32_e32 v43, 1.0, v42
	v_sub_f32_e32 v43, v32, v43
	v_add_f32_e32 v43, v33, v43
	v_add_f32_e32 v44, v42, v43
	v_sub_f32_e32 v42, v44, v42
	v_sub_f32_e32 v42, v43, v42
	v_add_f32_e32 v43, 1.0, v32
	v_add_f32_e32 v45, -1.0, v43
	v_sub_f32_e32 v32, v32, v45
	v_add_f32_e32 v32, v33, v32
	v_add_f32_e32 v33, v43, v32
	v_sub_f32_e32 v43, v33, v43
	v_sub_f32_e32 v32, v32, v43
	v_rcp_f32_e32 v43, v33
	v_cvt_f32_i32_e32 v31, v31
	v_cmp_neq_f32_e32 vcc, s27, v30
	v_mul_f32_e32 v45, v44, v43
	v_mul_f32_e32 v46, v33, v45
	v_fma_f32 v47, v45, v33, -v46
	v_fmac_f32_e32 v47, v45, v32
	v_add_f32_e32 v48, v46, v47
	v_sub_f32_e32 v49, v44, v48
	v_sub_f32_e32 v44, v44, v49
	v_sub_f32_e32 v46, v48, v46
	v_sub_f32_e32 v44, v44, v48
	v_add_f32_e32 v42, v42, v44
	v_sub_f32_e32 v44, v46, v47
	v_add_f32_e32 v42, v44, v42
	v_add_f32_e32 v44, v49, v42
	v_mul_f32_e32 v46, v43, v44
	v_mul_f32_e32 v47, v33, v46
	v_fma_f32 v33, v46, v33, -v47
	v_fmac_f32_e32 v33, v46, v32
	v_sub_f32_e32 v32, v49, v44
	v_add_f32_e32 v32, v42, v32
	v_add_f32_e32 v42, v47, v33
	v_sub_f32_e32 v48, v44, v42
	v_sub_f32_e32 v44, v44, v48
	v_sub_f32_e32 v47, v42, v47
	v_sub_f32_e32 v42, v44, v42
	v_add_f32_e32 v32, v32, v42
	v_sub_f32_e32 v33, v47, v33
	v_add_f32_e32 v32, v33, v32
	v_add_f32_e32 v33, v45, v46
	v_add_f32_e32 v32, v48, v32
	v_sub_f32_e32 v42, v33, v45
	v_mul_f32_e32 v32, v43, v32
	v_sub_f32_e32 v42, v46, v42
	v_add_f32_e32 v32, v42, v32
	v_mul_f32_e32 v45, 0x3f317218, v31
	v_add_f32_e32 v42, v33, v32
	v_fma_f32 v46, v31, s21, -v45
	v_mul_f32_e32 v43, v42, v42
	v_fmac_f32_e32 v46, 0xb102e308, v31
	v_sub_f32_e32 v31, v42, v33
	v_fmamk_f32 v44, v43, 0x3e9b6dac, v217
	v_sub_f32_e32 v31, v32, v31
	v_add_f32_e32 v32, v45, v46
	v_fmaak_f32 v44, v43, v44, 0x3f2aaada
	v_sub_f32_e32 v33, v32, v45
	v_ldexp_f32 v45, v42, 1
	v_mul_f32_e32 v42, v42, v43
	v_mul_f32_e32 v42, v42, v44
	v_add_f32_e32 v43, v45, v42
	v_sub_f32_e32 v44, v43, v45
	v_ldexp_f32 v31, v31, 1
	v_sub_f32_e32 v42, v42, v44
	v_add_f32_e32 v31, v31, v42
	v_add_f32_e32 v42, v43, v31
	v_sub_f32_e32 v43, v42, v43
	v_sub_f32_e32 v31, v31, v43
	v_add_f32_e32 v43, v32, v42
	v_sub_f32_e32 v44, v43, v32
	v_sub_f32_e32 v45, v43, v44
	v_sub_f32_e32 v33, v46, v33
	v_sub_f32_e32 v32, v32, v45
	v_sub_f32_e32 v42, v42, v44
	v_add_f32_e32 v32, v42, v32
	v_add_f32_e32 v42, v33, v31
	v_sub_f32_e32 v44, v42, v33
	v_sub_f32_e32 v45, v42, v44
	v_sub_f32_e32 v33, v33, v45
	v_sub_f32_e32 v31, v31, v44
	v_add_f32_e32 v32, v42, v32
	v_add_f32_e32 v31, v31, v33
	v_add_f32_e32 v33, v43, v32
	v_sub_f32_e32 v42, v33, v43
	v_sub_f32_e32 v32, v32, v42
	v_add_f32_e32 v31, v31, v32
	v_add_f32_e32 v31, v33, v31
	v_cndmask_b32_e32 v31, v230, v31, vcc
	v_cmp_ngt_f32_e32 vcc, -1.0, v30
	s_nop 1
	v_cndmask_b32_e32 v31, v231, v31, vcc
	v_cmp_neq_f32_e32 vcc, -1.0, v30
	s_nop 1
	v_cndmask_b32_e32 v31, v226, v31, vcc
	v_cmp_lt_f32_e64 vcc, |v30|, s33
	s_nop 1
	v_cndmask_b32_e32 v30, v31, v30, vcc
	v_sub_f32_e32 v98, v29, v30
	v_mul_f32_e32 v99, v99, v27
	v_add_f32_e32 v30, v99, v15
	v_min_f32_e32 v29, 0, v30
	v_mul_f32_e64 v30, |v30|, s3
	v_exp_f32_e32 v30, v30
	s_nop 0
	v_add_f32_e32 v32, 1.0, v30
	v_add_f32_e32 v31, -1.0, v32
	v_sub_f32_e32 v33, v31, v32
	v_add_f32_e32 v33, 1.0, v33
;     __device__ __forceinline__ void operator()(const f32x4 (&acc)[2][2][4][2], const Unit& u, int ui, int wr, int wc, int fr, int fq) const {
;     ...
;                             for (int e = 0; e < 6; ++e) { const float zz = z[e] + bfg[e]; z[e] = fminf(zz, 0.f) - log1pf(__expf(-fabsf(zz))); }
;                             float* lp = (float*)(ws + E_LS) + (size_t)row;
; #pragma unroll
;                             for (int e = 0; e < 6; ++e) lp[(size_t)(e * 32768u)] = z[e];
	v_sub_f32_e32 v31, v30, v31
	v_add_f32_e32 v33, v31, v33
	v_frexp_mant_f32_e32 v31, v32
	v_cvt_f64_f32_e32 v[42:43], v32
	v_cmp_gt_f32_e32 vcc, s19, v31
	v_frexp_exp_i32_f64_e32 v31, v[42:43]
	s_nop 0
	v_subbrev_co_u32_e32 v31, vcc, 0, v31, vcc
	v_sub_u32_e32 v42, 0, v31
	v_ldexp_f32 v32, v32, v42
	v_ldexp_f32 v33, v33, v42
	v_add_f32_e32 v42, -1.0, v32
	v_add_f32_e32 v43, 1.0, v42
	v_sub_f32_e32 v43, v32, v43
	v_add_f32_e32 v43, v33, v43
	v_add_f32_e32 v44, v42, v43
	v_sub_f32_e32 v42, v44, v42
	v_sub_f32_e32 v42, v43, v42
	v_add_f32_e32 v43, 1.0, v32
	v_add_f32_e32 v45, -1.0, v43
	v_sub_f32_e32 v32, v32, v45
	v_add_f32_e32 v32, v33, v32
	v_add_f32_e32 v33, v43, v32
	v_sub_f32_e32 v43, v33, v43
	v_sub_f32_e32 v32, v32, v43
	v_rcp_f32_e32 v43, v33
	v_cvt_f32_i32_e32 v31, v31
	v_cmp_neq_f32_e32 vcc, s27, v30
	v_mul_f32_e32 v45, v44, v43
	v_mul_f32_e32 v46, v33, v45
	v_fma_f32 v47, v45, v33, -v46
	v_fmac_f32_e32 v47, v45, v32
	v_add_f32_e32 v48, v46, v47
	v_sub_f32_e32 v49, v44, v48
	v_sub_f32_e32 v44, v44, v49
	v_sub_f32_e32 v46, v48, v46
	v_sub_f32_e32 v44, v44, v48
	v_add_f32_e32 v42, v42, v44
	v_sub_f32_e32 v44, v46, v47
	v_add_f32_e32 v42, v44, v42
	v_add_f32_e32 v44, v49, v42
	v_mul_f32_e32 v46, v43, v44
	v_mul_f32_e32 v47, v33, v46
	v_fma_f32 v33, v46, v33, -v47
	v_fmac_f32_e32 v33, v46, v32
	v_sub_f32_e32 v32, v49, v44
	v_add_f32_e32 v32, v42, v32
	v_add_f32_e32 v42, v47, v33
	v_sub_f32_e32 v48, v44, v42
	v_sub_f32_e32 v44, v44, v48
	v_sub_f32_e32 v47, v42, v47
	v_sub_f32_e32 v42, v44, v42
	v_add_f32_e32 v32, v32, v42
	v_sub_f32_e32 v33, v47, v33
	v_add_f32_e32 v32, v33, v32
	v_add_f32_e32 v33, v45, v46
	v_add_f32_e32 v32, v48, v32
	v_sub_f32_e32 v42, v33, v45
	v_mul_f32_e32 v32, v43, v32
	v_sub_f32_e32 v42, v46, v42
	v_add_f32_e32 v32, v42, v32
	v_mul_f32_e32 v45, 0x3f317218, v31
	v_add_f32_e32 v42, v33, v32
	v_fma_f32 v46, v31, s21, -v45
	v_mul_f32_e32 v43, v42, v42
	v_fmac_f32_e32 v46, 0xb102e308, v31
	v_sub_f32_e32 v31, v42, v33
	v_fmamk_f32 v44, v43, 0x3e9b6dac, v217
	v_sub_f32_e32 v31, v32, v31
	v_add_f32_e32 v32, v45, v46
	v_fmaak_f32 v44, v43, v44, 0x3f2aaada
	v_sub_f32_e32 v33, v32, v45
	v_ldexp_f32 v45, v42, 1
	v_mul_f32_e32 v42, v42, v43
	v_mul_f32_e32 v42, v42, v44
	v_add_f32_e32 v43, v45, v42
	v_sub_f32_e32 v44, v43, v45
	v_ldexp_f32 v31, v31, 1
	v_sub_f32_e32 v42, v42, v44
	v_add_f32_e32 v31, v31, v42
	v_add_f32_e32 v42, v43, v31
	v_sub_f32_e32 v43, v42, v43
	v_sub_f32_e32 v31, v31, v43
	v_add_f32_e32 v43, v32, v42
	v_sub_f32_e32 v44, v43, v32
	v_sub_f32_e32 v45, v43, v44
	v_sub_f32_e32 v33, v46, v33
	v_sub_f32_e32 v32, v32, v45
	v_sub_f32_e32 v42, v42, v44
	v_add_f32_e32 v32, v42, v32
	v_add_f32_e32 v42, v33, v31
	v_sub_f32_e32 v44, v42, v33
	v_sub_f32_e32 v45, v42, v44
	v_sub_f32_e32 v33, v33, v45
	v_sub_f32_e32 v31, v31, v44
	v_add_f32_e32 v32, v42, v32
	v_add_f32_e32 v31, v31, v33
	v_add_f32_e32 v33, v43, v32
	v_sub_f32_e32 v42, v33, v43
	v_sub_f32_e32 v32, v32, v42
	v_add_f32_e32 v31, v31, v32
	v_add_f32_e32 v31, v33, v31
	v_cndmask_b32_e32 v31, v230, v31, vcc
	v_cmp_ngt_f32_e32 vcc, -1.0, v30
	s_nop 1
	v_cndmask_b32_e32 v31, v231, v31, vcc
	v_cmp_neq_f32_e32 vcc, -1.0, v30
	s_nop 1
	v_cndmask_b32_e32 v31, v226, v31, vcc
	v_cmp_lt_f32_e64 vcc, |v30|, s33
	s_nop 1
	v_cndmask_b32_e32 v30, v31, v30, vcc
	v_sub_f32_e32 v99, v29, v30
	s_mov_b64 s[30:31], s[12:13]
	global_store_dword v28, v118, s[30:31]
	global_store_dword v28, v102, s[30:31] offset:64
	s_add_u32 s30, s30, 0x20000
	s_addc_u32 s31, s31, 0
	global_store_dword v28, v119, s[30:31]
	global_store_dword v28, v103, s[30:31] offset:64
	s_add_u32 s30, s30, 0x20000
	s_addc_u32 s31, s31, 0
	global_store_dword v28, v120, s[30:31]
	global_store_dword v28, v104, s[30:31] offset:64
	s_add_u32 s30, s30, 0x20000
	s_addc_u32 s31, s31, 0
	global_store_dword v28, v121, s[30:31]
	global_store_dword v28, v105, s[30:31] offset:64
	s_add_u32 s30, s30, 0x20000
	s_addc_u32 s31, s31, 0
	global_store_dword v28, v114, s[30:31]
	global_store_dword v28, v98, s[30:31] offset:64
	s_add_u32 s30, s30, 0x20000
	s_addc_u32 s31, s31, 0
	global_store_dword v28, v115, s[30:31]
	global_store_dword v28, v99, s[30:31] offset:64

; #define PG8_PACK8(y0, y1) (u32x4){cvt_pk_bf16((y0)[0], (y0)[1]), cvt_pk_bf16((y0)[2], (y0)[3]), cvt_pk_bf16((y1)[0], (y1)[1]), cvt_pk_bf16((y1)[2], (y1)[3])}
;     __device__ __forceinline__ void operator()(const f32x4 (&acc)[2][2][4][2], const Unit& u, int ui, int wr, int wc, int fr, int fq) const {
;     ...
;         } else if (pn < 12) {
;             unsigned char* dst = ws + E_QKVO + (size_t)((unsigned)(u.pm >> 4) * (24u << 20) + (16u << 20) + (unsigned)(((pn & 3) * 256 + wc * 64 + 8 * fq) * 2));
; #pragma unroll
;             for (int ai = 0; ai < 2; ++ai)
; #pragma unroll
;                 for (int m = 0; m < 4; ++m) {
;                     const unsigned row = row0 + ai * HALF + m * 16; const float rs = rsp[ai * HALF + m * 16];
; #pragma unroll
;                     for (int bj = 0; bj < 2; ++bj) { const f32x4 y0 = acc[ai][bj][m][0] * rs, y1 = acc[ai][bj][m][1] * rs;
;                         *(u32x4*)(dst + (size_t)(row * 2048u + 64u * bj)) = PG8_PACK8(y0, y1); }
;                 }
.LBB0_610:
	s_and_b64 vcc, exec, s[28:29]
	s_cbranch_vccz .LBB0_612
	s_lshr_b32 s19, s4, 4
	s_lshl_b32 s21, s26, 9
	ds_read_b32 v136, v160
	s_mul_i32 s19, s19, 0x1800000
	s_and_b32 s21, s21, 0x600
	s_or_b32 s19, s19, s21
	s_add_i32 s19, s19, 0x1000000
	v_or_b32_e32 v0, s19, v175
	v_lshl_add_u64 v[130:131], s[14:15], 0, v[0:1]
	v_lshlrev_b32_e32 v0, 11, v158
	s_waitcnt lgkmcnt(0)
	v_pk_mul_f32 v[134:135], v[128:129], v[136:137] op_sel_hi:[1,0]
	v_pk_mul_f32 v[132:133], v[126:127], v[136:137] op_sel_hi:[1,0]
	v_pk_mul_f32 v[138:139], v[124:125], v[136:137] op_sel_hi:[1,0]
	v_pk_mul_f32 v[140:141], v[122:123], v[136:137] op_sel_hi:[1,0]
	v_cvt_pk_bf16_f32 v132, v132, v133
	v_cvt_pk_bf16_f32 v133, v134, v135
	s_nop 0
	v_cvt_pk_bf16_f32 v134, v140, v141
	v_cvt_pk_bf16_f32 v135, v138, v139
	v_lshl_add_u64 v[138:139], v[130:131], 0, v[0:1]
	global_store_dwordx4 v[138:139], v[132:135], off
	v_pk_mul_f32 v[140:141], v[116:117], v[136:137] op_sel_hi:[1,0]
	s_nop 0
	v_pk_mul_f32 v[134:135], v[120:121], v[136:137] op_sel_hi:[1,0]
	v_pk_mul_f32 v[132:133], v[118:119], v[136:137] op_sel_hi:[1,0]
	v_pk_mul_f32 v[136:137], v[114:115], v[136:137] op_sel_hi:[1,0]
	v_cvt_pk_bf16_f32 v132, v132, v133
	v_cvt_pk_bf16_f32 v133, v134, v135
	s_nop 0
	v_cvt_pk_bf16_f32 v134, v136, v137
	v_cvt_pk_bf16_f32 v135, v140, v141
	global_store_dwordx4 v[138:139], v[132:135], off offset:64
	ds_read_b32 v136, v160 offset:64
	v_or_b32_e32 v138, 0x8000, v0
	v_mov_b32_e32 v139, v1
	v_lshl_add_u64 v[138:139], v[130:131], 0, v[138:139]
	s_waitcnt lgkmcnt(0)
	v_pk_mul_f32 v[134:135], v[112:113], v[136:137] op_sel_hi:[1,0]
	v_pk_mul_f32 v[132:133], v[110:111], v[136:137] op_sel_hi:[1,0]
	v_pk_mul_f32 v[140:141], v[108:109], v[136:137] op_sel_hi:[1,0]
	v_pk_mul_f32 v[142:143], v[106:107], v[136:137] op_sel_hi:[1,0]
	v_cvt_pk_bf16_f32 v132, v132, v133
	v_cvt_pk_bf16_f32 v133, v134, v135
	s_nop 0
	v_cvt_pk_bf16_f32 v134, v142, v143
	v_cvt_pk_bf16_f32 v135, v140, v141
	global_store_dwordx4 v[138:139], v[132:135], off
	v_pk_mul_f32 v[138:139], v[100:101], v[136:137] op_sel_hi:[1,0]
	s_nop 0
	v_pk_mul_f32 v[134:135], v[104:105], v[136:137] op_sel_hi:[1,0]
	v_pk_mul_f32 v[132:133], v[102:103], v[136:137] op_sel_hi:[1,0]
	v_pk_mul_f32 v[136:137], v[98:99], v[136:137] op_sel_hi:[1,0]
	v_cvt_pk_bf16_f32 v132, v132, v133
	v_cvt_pk_bf16_f32 v133, v134, v135
	s_nop 0
	v_cvt_pk_bf16_f32 v134, v136, v137
	v_or_b32_e32 v136, 0x8040, v0
	v_mov_b32_e32 v137, v1
	v_lshl_add_u64 v[136:137], v[130:131], 0, v[136:137]
	v_cvt_pk_bf16_f32 v135, v138, v139
	global_store_dwordx4 v[136:137], v[132:135], off
	ds_read_b32 v136, v160 offset:128
	v_or_b32_e32 v138, 0x10000, v0
	v_mov_b32_e32 v139, v1
	v_lshl_add_u64 v[138:139], v[130:131], 0, v[138:139]
	s_waitcnt lgkmcnt(0)
	v_pk_mul_f32 v[134:135], v[96:97], v[136:137] op_sel_hi:[1,0]
	v_pk_mul_f32 v[132:133], v[94:95], v[136:137] op_sel_hi:[1,0]
	v_pk_mul_f32 v[140:141], v[92:93], v[136:137] op_sel_hi:[1,0]
	v_pk_mul_f32 v[142:143], v[90:91], v[136:137] op_sel_hi:[1,0]
	v_cvt_pk_bf16_f32 v132, v132, v133
	v_cvt_pk_bf16_f32 v133, v134, v135
	s_nop 0
	v_cvt_pk_bf16_f32 v134, v142, v143
	v_cvt_pk_bf16_f32 v135, v140, v141
	global_store_dwordx4 v[138:139], v[132:135], off
	v_pk_mul_f32 v[138:139], v[84:85], v[136:137] op_sel_hi:[1,0]
	s_nop 0
	v_pk_mul_f32 v[134:135], v[88:89], v[136:137] op_sel_hi:[1,0]
	v_pk_mul_f32 v[132:133], v[86:87], v[136:137] op_sel_hi:[1,0]
	v_pk_mul_f32 v[136:137], v[82:83], v[136:137] op_sel_hi:[1,0]
	v_cvt_pk_bf16_f32 v132, v132, v133
	v_cvt_pk_bf16_f32 v133, v134, v135
	s_nop 0
	v_cvt_pk_bf16_f32 v134, v136, v137
	v_or_b32_e32 v136, 0x10040, v0
	v_mov_b32_e32 v137, v1
	v_lshl_add_u64 v[136:137], v[130:131], 0, v[136:137]
	v_cvt_pk_bf16_f32 v135, v138, v139
	global_store_dwordx4 v[136:137], v[132:135], off
	ds_read_b32 v136, v160 offset:192
	v_or_b32_e32 v138, 0x18000, v0
	v_mov_b32_e32 v139, v1
	v_lshl_add_u64 v[138:139], v[130:131], 0, v[138:139]
	s_waitcnt lgkmcnt(0)
	v_pk_mul_f32 v[134:135], v[80:81], v[136:137] op_sel_hi:[1,0]
	v_pk_mul_f32 v[132:133], v[78:79], v[136:137] op_sel_hi:[1,0]
	v_pk_mul_f32 v[140:141], v[76:77], v[136:137] op_sel_hi:[1,0]
	v_pk_mul_f32 v[142:143], v[74:75], v[136:137] op_sel_hi:[1,0]
	v_cvt_pk_bf16_f32 v132, v132, v133
	v_cvt_pk_bf16_f32 v133, v134, v135
	s_nop 0
	v_cvt_pk_bf16_f32 v134, v142, v143
	v_cvt_pk_bf16_f32 v135, v140, v141
	global_store_dwordx4 v[138:139], v[132:135], off
	v_pk_mul_f32 v[138:139], v[68:69], v[136:137] op_sel_hi:[1,0]
	s_nop 0
	v_pk_mul_f32 v[134:135], v[72:73], v[136:137] op_sel_hi:[1,0]
	v_pk_mul_f32 v[132:133], v[70:71], v[136:137] op_sel_hi:[1,0]
	v_pk_mul_f32 v[136:137], v[66:67], v[136:137] op_sel_hi:[1,0]
	v_cvt_pk_bf16_f32 v132, v132, v133
	v_cvt_pk_bf16_f32 v133, v134, v135
	s_nop 0
	v_cvt_pk_bf16_f32 v134, v136, v137
	v_or_b32_e32 v136, 0x18040, v0
	v_mov_b32_e32 v137, v1
	v_lshl_add_u64 v[136:137], v[130:131], 0, v[136:137]
	v_cvt_pk_bf16_f32 v135, v138, v139
	global_store_dwordx4 v[136:137], v[132:135], off
	ds_read_b32 v136, v160 offset:512
	v_add_u32_e32 v138, 0x40000, v0
	v_mov_b32_e32 v139, v1
	v_lshl_add_u64 v[138:139], v[130:131], 0, v[138:139]
	s_waitcnt lgkmcnt(0)
; #define PG8_PACK8(y0, y1) (u32x4){cvt_pk_bf16((y0)[0], (y0)[1]), cvt_pk_bf16((y0)[2], (y0)[3]), cvt_pk_bf16((y1)[0], (y1)[1]), cvt_pk_bf16((y1)[2], (y1)[3])}
;     __device__ __forceinline__ void operator()(const f32x4 (&acc)[2][2][4][2], const Unit& u, int ui, int wr, int wc, int fr, int fq) const {
;     ...
; #pragma unroll
;             for (int ai = 0; ai < 2; ++ai)
; #pragma unroll
;                 for (int m = 0; m < 4; ++m) {
;                     const unsigned row = row0 + ai * HALF + m * 16; const float rs = rsp[ai * HALF + m * 16];
; #pragma unroll
;                     for (int bj = 0; bj < 2; ++bj) { const f32x4 y0 = acc[ai][bj][m][0] * rs, y1 = acc[ai][bj][m][1] * rs;
;                         *(u32x4*)(dst + (size_t)(row * 2048u + 64u * bj)) = PG8_PACK8(y0, y1); }
;                 }
	v_pk_mul_f32 v[134:135], v[64:65], v[136:137] op_sel_hi:[1,0]
	v_pk_mul_f32 v[132:133], v[62:63], v[136:137] op_sel_hi:[1,0]
	v_pk_mul_f32 v[140:141], v[60:61], v[136:137] op_sel_hi:[1,0]
	v_pk_mul_f32 v[142:143], v[58:59], v[136:137] op_sel_hi:[1,0]
	v_cvt_pk_bf16_f32 v132, v132, v133
	v_cvt_pk_bf16_f32 v133, v134, v135
	s_nop 0
	v_cvt_pk_bf16_f32 v134, v142, v143
	v_cvt_pk_bf16_f32 v135, v140, v141
	global_store_dwordx4 v[138:139], v[132:135], off
	v_pk_mul_f32 v[140:141], v[52:53], v[136:137] op_sel_hi:[1,0]
	s_nop 0
	v_pk_mul_f32 v[134:135], v[56:57], v[136:137] op_sel_hi:[1,0]
	v_pk_mul_f32 v[132:133], v[54:55], v[136:137] op_sel_hi:[1,0]
	v_pk_mul_f32 v[136:137], v[50:51], v[136:137] op_sel_hi:[1,0]
	v_cvt_pk_bf16_f32 v132, v132, v133
	v_cvt_pk_bf16_f32 v133, v134, v135
	s_nop 0
	v_cvt_pk_bf16_f32 v134, v136, v137
	v_cvt_pk_bf16_f32 v135, v140, v141
	global_store_dwordx4 v[138:139], v[132:135], off offset:64
	ds_read_b32 v136, v160 offset:576
	v_add_u32_e32 v138, 0x48000, v0
	v_mov_b32_e32 v139, v1
	v_lshl_add_u64 v[138:139], v[130:131], 0, v[138:139]
	s_waitcnt lgkmcnt(0)
	v_pk_mul_f32 v[134:135], v[48:49], v[136:137] op_sel_hi:[1,0]
	v_pk_mul_f32 v[132:133], v[46:47], v[136:137] op_sel_hi:[1,0]
	v_pk_mul_f32 v[140:141], v[44:45], v[136:137] op_sel_hi:[1,0]
	v_pk_mul_f32 v[142:143], v[42:43], v[136:137] op_sel_hi:[1,0]
	v_cvt_pk_bf16_f32 v132, v132, v133
	v_cvt_pk_bf16_f32 v133, v134, v135
	s_nop 0
	v_cvt_pk_bf16_f32 v134, v142, v143
	v_cvt_pk_bf16_f32 v135, v140, v141
	global_store_dwordx4 v[138:139], v[132:135], off
	v_pk_mul_f32 v[138:139], v[36:37], v[136:137] op_sel_hi:[1,0]
	s_nop 0
	v_pk_mul_f32 v[134:135], v[40:41], v[136:137] op_sel_hi:[1,0]
	v_pk_mul_f32 v[132:133], v[38:39], v[136:137] op_sel_hi:[1,0]
	v_pk_mul_f32 v[136:137], v[34:35], v[136:137] op_sel_hi:[1,0]
	v_cvt_pk_bf16_f32 v132, v132, v133
	v_cvt_pk_bf16_f32 v133, v134, v135
	s_nop 0
	v_cvt_pk_bf16_f32 v134, v136, v137
	v_add_u32_e32 v136, 0x48040, v0
	v_mov_b32_e32 v137, v1
	v_lshl_add_u64 v[136:137], v[130:131], 0, v[136:137]
	v_cvt_pk_bf16_f32 v135, v138, v139
	global_store_dwordx4 v[136:137], v[132:135], off
	ds_read_b32 v136, v160 offset:640
	v_add_u32_e32 v138, 0x50000, v0
	v_mov_b32_e32 v139, v1
	v_lshl_add_u64 v[138:139], v[130:131], 0, v[138:139]
	s_waitcnt lgkmcnt(0)
	v_pk_mul_f32 v[134:135], v[32:33], v[136:137] op_sel_hi:[1,0]
	v_pk_mul_f32 v[132:133], v[30:31], v[136:137] op_sel_hi:[1,0]
	v_pk_mul_f32 v[140:141], v[28:29], v[136:137] op_sel_hi:[1,0]
	v_pk_mul_f32 v[142:143], v[26:27], v[136:137] op_sel_hi:[1,0]
	v_cvt_pk_bf16_f32 v132, v132, v133
	v_cvt_pk_bf16_f32 v133, v134, v135
	s_nop 0
	v_cvt_pk_bf16_f32 v134, v142, v143
	v_cvt_pk_bf16_f32 v135, v140, v141
	global_store_dwordx4 v[138:139], v[132:135], off
	v_pk_mul_f32 v[138:139], v[20:21], v[136:137] op_sel_hi:[1,0]
	s_nop 0
	v_pk_mul_f32 v[134:135], v[24:25], v[136:137] op_sel_hi:[1,0]
	v_pk_mul_f32 v[132:133], v[22:23], v[136:137] op_sel_hi:[1,0]
	v_pk_mul_f32 v[136:137], v[18:19], v[136:137] op_sel_hi:[1,0]
	v_cvt_pk_bf16_f32 v132, v132, v133
	v_cvt_pk_bf16_f32 v133, v134, v135
	s_nop 0
	v_cvt_pk_bf16_f32 v134, v136, v137
	v_add_u32_e32 v136, 0x50040, v0
	v_mov_b32_e32 v137, v1
	v_lshl_add_u64 v[136:137], v[130:131], 0, v[136:137]
	v_cvt_pk_bf16_f32 v135, v138, v139
	global_store_dwordx4 v[136:137], v[132:135], off
	ds_read_b32 v136, v160 offset:704
	v_add_u32_e32 v138, 0x58000, v0
	v_mov_b32_e32 v139, v1
	v_lshl_add_u64 v[138:139], v[130:131], 0, v[138:139]
	v_add_u32_e32 v0, 0x58040, v0
	s_waitcnt lgkmcnt(0)
	v_pk_mul_f32 v[134:135], v[16:17], v[136:137] op_sel_hi:[1,0]
	v_pk_mul_f32 v[132:133], v[14:15], v[136:137] op_sel_hi:[1,0]
	v_pk_mul_f32 v[140:141], v[12:13], v[136:137] op_sel_hi:[1,0]
	v_pk_mul_f32 v[142:143], v[10:11], v[136:137] op_sel_hi:[1,0]
	v_cvt_pk_bf16_f32 v132, v132, v133
	v_cvt_pk_bf16_f32 v133, v134, v135
	v_lshl_add_u64 v[130:131], v[130:131], 0, v[0:1]
	v_cvt_pk_bf16_f32 v134, v142, v143
	v_cvt_pk_bf16_f32 v135, v140, v141
	global_store_dwordx4 v[138:139], v[132:135], off
	v_pk_mul_f32 v[138:139], v[4:5], v[136:137] op_sel_hi:[1,0]
	s_nop 0
	v_pk_mul_f32 v[134:135], v[8:9], v[136:137] op_sel_hi:[1,0]
	v_pk_mul_f32 v[132:133], v[6:7], v[136:137] op_sel_hi:[1,0]
	v_pk_mul_f32 v[136:137], v[2:3], v[136:137] op_sel_hi:[1,0]
	v_cvt_pk_bf16_f32 v132, v132, v133
	v_cvt_pk_bf16_f32 v133, v134, v135
	s_nop 0
	v_cvt_pk_bf16_f32 v134, v136, v137
	v_cvt_pk_bf16_f32 v135, v138, v139
	global_store_dwordx4 v[130:131], v[132:135], off

; #define PG8_LAS __attribute__((address_space(3)))
;     __device__ __forceinline__ void operator()(const f32x4 (&acc)[2][2][4][2], const Unit& u, int ui, int wr, int wc, int fr, int fq) const {
;     ...
;         const PG8_LAS float* rsp = tab + (u.pm == pmA ? 0 : 256) + wr * 64 + fr;
;         if (pn < 8) {
;             const PG8_LAS float* gp = tab + TAB_G + ui * 256 + 64 * wc + 8 * fq;
;             f32x4 g[2][2];
; #pragma unroll
;             for (int bj = 0; bj < 2; ++bj)
; #pragma unroll
;                 for (int n = 0; n < 2; ++n) g[bj][n] = *(const PG8_LAS f32x4*)(gp + 32 * bj + 4 * n);
;             unsigned char* dst = ws + E_QKVO + (size_t)((unsigned)(u.pm >> 4) * (24u << 20) + (pn < 4 ? 0u : (8u << 20)) + (unsigned)(((pn & 3) * 256 + wc * 64 + 8 * fq) * 2));
;             float ss[2][4], e2[2][4];
; #pragma unroll
;             for (int ai = 0; ai < 2; ++ai)
; #pragma unroll
;                 for (int m = 0; m < 4; ++m) {
;                     const float rs = rsp[ai * HALF + m * 16]; e2[ai][m] = RMS_EPS * __builtin_amdgcn_rcpf(rs * rs);
;                     f32x4 s4 = acc[ai][0][m][0] * acc[ai][0][m][0]; s4 += acc[ai][0][m][1] * acc[ai][0][m][1]; s4 += acc[ai][1][m][0] * acc[ai][1][m][0]; s4 += acc[ai][1][m][1] * acc[ai][1][m][1];
;                     ss[ai][m] = (s4[0] + s4[1]) + (s4[2] + s4[3]);
;                 }
;             float sw[2][4];
; #pragma unroll
;             for (int ai = 0; ai < 2; ++ai)
; #pragma unroll
;                 for (int m = 0; m < 4; ++m) sw[ai][m] = __builtin_bit_cast(float, __builtin_amdgcn_ds_swizzle(__builtin_bit_cast(int, ss[ai][m]), 0x401F));
.LBB0_613:
	s_andn2_b64 vcc, exec, s[28:29]
	s_cbranch_vccnz .LBB0_620
	v_lshl_add_u32 v0, s5, 10, v187
	ds_read_b128 v[142:145], v0
	ds_read_b128 v[138:141], v0 offset:16
	ds_read_b128 v[134:137], v0 offset:128
	ds_read_b128 v[130:133], v0 offset:144
	ds_read2_b32 v[168:169], v160 offset1:16
	v_pk_mul_f32 v[172:173], v[124:125], v[124:125]
	v_pk_mul_f32 v[176:177], v[122:123], v[122:123]
	v_pk_fma_f32 v[172:173], v[128:129], v[128:129], v[172:173]
	v_pk_fma_f32 v[176:177], v[126:127], v[126:127], v[176:177]
	v_pk_fma_f32 v[172:173], v[120:121], v[120:121], v[172:173]
	v_pk_fma_f32 v[176:177], v[118:119], v[118:119], v[176:177]
	v_pk_fma_f32 v[172:173], v[116:117], v[116:117], v[172:173]
	v_pk_fma_f32 v[176:177], v[114:115], v[114:115], v[176:177]
	s_waitcnt lgkmcnt(0)
	v_mul_f32_e32 v159, v168, v168
	v_pk_mov_b32 v[178:179], v[176:177], v[172:173] op_sel:[1,0]
	v_mov_b32_e32 v177, v173
	v_pk_add_f32 v[172:173], v[178:179], v[176:177]
	v_rcp_f32_e32 v168, v159
	v_add_f32_e32 v159, v172, v173
	v_pk_mul_f32 v[172:173], v[108:109], v[108:109]
	v_pk_mul_f32 v[176:177], v[106:107], v[106:107]
	v_pk_fma_f32 v[172:173], v[112:113], v[112:113], v[172:173]
	v_pk_fma_f32 v[176:177], v[110:111], v[110:111], v[176:177]
	v_pk_fma_f32 v[172:173], v[104:105], v[104:105], v[172:173]
	v_pk_fma_f32 v[176:177], v[102:103], v[102:103], v[176:177]
	ds_read2_b32 v[178:179], v160 offset0:32 offset1:48
	v_mul_f32_e32 v161, v169, v169
	v_pk_fma_f32 v[172:173], v[100:101], v[100:101], v[172:173]
	v_pk_fma_f32 v[176:177], v[98:99], v[98:99], v[176:177]
	v_rcp_f32_e32 v162, v161
	v_add_f32_e32 v161, v176, v177
	v_add_f32_e32 v164, v172, v173
	v_pk_mul_f32 v[172:173], v[92:93], v[92:93]
	v_pk_mul_f32 v[176:177], v[90:91], v[90:91]
	v_pk_fma_f32 v[172:173], v[96:97], v[96:97], v[172:173]
	v_pk_fma_f32 v[176:177], v[94:95], v[94:95], v[176:177]
	v_pk_fma_f32 v[172:173], v[88:89], v[88:89], v[172:173]
	v_pk_fma_f32 v[176:177], v[86:87], v[86:87], v[176:177]
	v_add_f32_e32 v164, v161, v164
	s_waitcnt lgkmcnt(0)
	v_mul_f32_e32 v161, v178, v178
	v_pk_fma_f32 v[172:173], v[84:85], v[84:85], v[172:173]
	v_pk_fma_f32 v[176:177], v[82:83], v[82:83], v[176:177]
	v_rcp_f32_e32 v166, v161
	v_add_f32_e32 v161, v176, v177
	v_add_f32_e32 v169, v172, v173
	v_pk_mul_f32 v[172:173], v[76:77], v[76:77]
	v_pk_mul_f32 v[176:177], v[74:75], v[74:75]
	v_pk_fma_f32 v[172:173], v[80:81], v[80:81], v[172:173]
	v_pk_fma_f32 v[176:177], v[78:79], v[78:79], v[176:177]
	v_add_f32_e32 v170, v161, v169
	v_mul_f32_e32 v161, v179, v179
	v_pk_fma_f32 v[172:173], v[72:73], v[72:73], v[172:173]
	v_pk_fma_f32 v[176:177], v[70:71], v[70:71], v[176:177]
	ds_read2_b32 v[178:179], v160 offset0:128 offset1:144
	v_pk_fma_f32 v[172:173], v[68:69], v[68:69], v[172:173]
	v_pk_fma_f32 v[176:177], v[66:67], v[66:67], v[176:177]
	v_rcp_f32_e32 v174, v161
	v_add_f32_e32 v161, v176, v177
	v_add_f32_e32 v169, v172, v173
	v_pk_mul_f32 v[172:173], v[60:61], v[60:61]
	v_pk_mul_f32 v[176:177], v[58:59], v[58:59]
	v_pk_fma_f32 v[172:173], v[64:65], v[64:65], v[172:173]
	v_pk_fma_f32 v[176:177], v[62:63], v[62:63], v[176:177]
	v_pk_fma_f32 v[172:173], v[56:57], v[56:57], v[172:173]
	v_pk_fma_f32 v[176:177], v[54:55], v[54:55], v[176:177]
	v_add_f32_e32 v180, v161, v169
	s_waitcnt lgkmcnt(0)
	v_mul_f32_e32 v161, v178, v178
	v_pk_fma_f32 v[172:173], v[52:53], v[52:53], v[172:173]
	v_pk_fma_f32 v[176:177], v[50:51], v[50:51], v[176:177]
	v_rcp_f32_e32 v178, v161
	v_add_f32_e32 v161, v176, v177
	v_add_f32_e32 v169, v172, v173
	v_pk_mul_f32 v[172:173], v[44:45], v[44:45]
	v_pk_mul_f32 v[176:177], v[42:43], v[42:43]
	v_pk_fma_f32 v[172:173], v[48:49], v[48:49], v[172:173]
	v_pk_fma_f32 v[176:177], v[46:47], v[46:47], v[176:177]
	v_add_f32_e32 v182, v161, v169
	v_mul_f32_e32 v161, v179, v179
	v_pk_fma_f32 v[172:173], v[40:41], v[40:41], v[172:173]
	v_pk_fma_f32 v[176:177], v[38:39], v[38:39], v[176:177]
	v_rcp_f32_e32 v179, v161
	v_pk_fma_f32 v[172:173], v[36:37], v[36:37], v[172:173]
	ds_read2_b32 v[160:161], v160 offset0:160 offset1:176
	v_pk_fma_f32 v[176:177], v[34:35], v[34:35], v[176:177]
	v_add_f32_e32 v172, v172, v173
	v_add_f32_e32 v169, v176, v177
	v_add_f32_e32 v183, v169, v172
	v_pk_mul_f32 v[172:173], v[28:29], v[28:29]
	v_pk_mul_f32 v[176:177], v[26:27], v[26:27]
	v_pk_fma_f32 v[172:173], v[32:33], v[32:33], v[172:173]
	v_pk_fma_f32 v[176:177], v[30:31], v[30:31], v[176:177]
	v_pk_fma_f32 v[172:173], v[24:25], v[24:25], v[172:173]
	v_pk_fma_f32 v[176:177], v[22:23], v[22:23], v[176:177]
	s_waitcnt lgkmcnt(0)
	v_mul_f32_e32 v160, v160, v160
	v_pk_fma_f32 v[172:173], v[20:21], v[20:21], v[172:173]
	v_pk_fma_f32 v[176:177], v[18:19], v[18:19], v[176:177]
	v_rcp_f32_e32 v184, v160
	v_add_f32_e32 v160, v176, v177
	v_add_f32_e32 v169, v172, v173
	v_add_f32_e32 v176, v160, v169
	v_mul_f32_e32 v160, v161, v161
	v_rcp_f32_e32 v177, v160
	v_pk_mul_f32 v[160:161], v[12:13], v[12:13]
	v_pk_mul_f32 v[172:173], v[10:11], v[10:11]
	v_pk_fma_f32 v[160:161], v[16:17], v[16:17], v[160:161]
	v_pk_fma_f32 v[172:173], v[14:15], v[14:15], v[172:173]
	v_pk_fma_f32 v[160:161], v[8:9], v[8:9], v[160:161]
	v_pk_fma_f32 v[172:173], v[6:7], v[6:7], v[172:173]
	v_pk_fma_f32 v[160:161], v[4:5], v[4:5], v[160:161]
	v_pk_fma_f32 v[172:173], v[2:3], v[2:3], v[172:173]
	v_add_f32_e32 v160, v160, v161
	v_add_f32_e32 v169, v172, v173
	v_add_f32_e32 v172, v169, v160
	ds_swizzle_b32 v160, v159 offset:swizzle(SWAP,16)
	ds_swizzle_b32 v161, v164 offset:swizzle(SWAP,16)
	s_mov_b32 s28, 0x358637bd
	s_mov_b32 s29, 0x3c800000
	ds_swizzle_b32 v173, v170 offset:swizzle(SWAP,16)
	s_waitcnt lgkmcnt(0)
; #define PG8_PACK8(y0, y1) (u32x4){cvt_pk_bf16((y0)[0], (y0)[1]), cvt_pk_bf16((y0)[2], (y0)[3]), cvt_pk_bf16((y1)[0], (y1)[1]), cvt_pk_bf16((y1)[2], (y1)[3])}
;     __device__ __forceinline__ void operator()(const f32x4 (&acc)[2][2][4][2], const Unit& u, int ui, int wr, int wc, int fr, int fq) const {
;     ...
;                 for (int m = 0; m < 4; ++m) sw[ai][m] = __builtin_bit_cast(float, __builtin_amdgcn_ds_swizzle(__builtin_bit_cast(int, ss[ai][m]), 0x401F));
; #pragma unroll
;             for (int ai = 0; ai < 2; ++ai)
; #pragma unroll
;                 for (int m = 0; m < 4; ++m) { float s = ss[ai][m] + sw[ai][m]; s += __shfl_xor(s, 32);
;                     ss[ai][m] = __builtin_amdgcn_rsqf(s * (1.0f / 64.0f) + e2[ai][m]); }
;             if (pn != 4) {
; #pragma unroll
;                 for (int ai = 0; ai < 2; ++ai)
; #pragma unroll
;                     for (int m = 0; m < 4; ++m) {
;                         const unsigned row = row0 + ai * HALF + m * 16; const float r2 = ss[ai][m];
; #pragma unroll
;                         for (int bj = 0; bj < 2; ++bj) {
;                             const f32x4 z0 = acc[ai][bj][m][0] * (g[bj][0] * r2), z1 = acc[ai][bj][m][1] * (g[bj][1] * r2);
;                             *(u32x4*)(dst + (size_t)(row * 2048u + 64u * bj)) = PG8_PACK8(z0, z1);
	v_add_f32_e32 v159, v159, v160
	ds_bpermute_b32 v160, v195, v159
	v_add_f32_e32 v164, v164, v161
	ds_bpermute_b32 v186, v195, v164
	ds_swizzle_b32 v185, v180 offset:swizzle(SWAP,16)
	ds_swizzle_b32 v188, v182 offset:swizzle(SWAP,16)
	s_waitcnt lgkmcnt(0)
	v_add_f32_e32 v169, v159, v160
	v_pk_mul_f32 v[160:161], v[168:169], s[28:29]
	ds_swizzle_b32 v189, v183 offset:swizzle(SWAP,16)
	v_add_f32_e32 v159, v160, v161
	v_rsq_f32_e32 v198, v159
	v_add_f32_e32 v159, v164, v186
	v_mul_f32_e32 v159, 0x3c800000, v159
	v_fmac_f32_e32 v159, 0x358637bd, v162
	v_add_f32_e32 v160, v170, v173
	v_rsq_f32_e32 v186, v159
	v_add_f32_e32 v159, v180, v185
	ds_bpermute_b32 v161, v195, v160
	ds_bpermute_b32 v162, v195, v159
	ds_swizzle_b32 v190, v176 offset:swizzle(SWAP,16)
	ds_swizzle_b32 v191, v172 offset:swizzle(SWAP,16)
	s_lshr_b32 s5, s4, 4
	s_waitcnt lgkmcnt(0)
	v_add_f32_e32 v160, v160, v161
	v_add_f32_e32 v159, v159, v162
	v_mul_f32_e32 v160, 0x3c800000, v160
	v_mul_f32_e32 v159, 0x3c800000, v159
	v_fmac_f32_e32 v160, 0x358637bd, v166
	v_fmac_f32_e32 v159, 0x358637bd, v174
	v_rsq_f32_e32 v180, v160
	v_add_f32_e32 v160, v182, v188
	v_rsq_f32_e32 v174, v159
	v_add_f32_e32 v159, v183, v189
	ds_bpermute_b32 v161, v195, v160
	ds_bpermute_b32 v162, v195, v159
	s_cmp_lt_i32 s26, 4
	s_mul_i32 s5, s5, 0x1800000
	s_cselect_b32 s19, 0, 0x800000
	s_waitcnt lgkmcnt(0)
	v_add_f32_e32 v160, v160, v161
	v_add_f32_e32 v159, v159, v162
	v_mul_f32_e32 v160, 0x3c800000, v160
	v_mul_f32_e32 v159, 0x3c800000, v159
	v_fmac_f32_e32 v160, 0x358637bd, v178
	v_fmac_f32_e32 v159, 0x358637bd, v179
	v_rsq_f32_e32 v170, v160
	v_add_f32_e32 v160, v176, v190
	v_rsq_f32_e32 v166, v159
	v_add_f32_e32 v159, v172, v191
	ds_bpermute_b32 v161, v195, v160
	ds_bpermute_b32 v162, v195, v159
	s_add_i32 s5, s5, s19
	s_lshl_b32 s19, s26, 8
	s_and_b32 s19, s19, 0x300
	s_waitcnt lgkmcnt(0)
	v_add_f32_e32 v160, v160, v161
	v_add_f32_e32 v159, v159, v162
	v_mul_f32_e32 v160, 0x3c800000, v160
	v_mul_f32_e32 v159, 0x3c800000, v159
	v_or_b32_e32 v0, s19, v238
	v_fmac_f32_e32 v160, 0x358637bd, v184
	v_fmac_f32_e32 v159, 0x358637bd, v177
	v_lshl_or_b32 v0, v0, 1, s5
	v_rsq_f32_e32 v164, v160
	v_rsq_f32_e32 v162, v159
	v_mov_b32_e32 v199, v198
	v_lshl_add_u64 v[160:161], s[14:15], 0, v[0:1]
	v_lshlrev_b32_e32 v0, 11, v158
	v_pk_mul_f32 v[158:159], v[142:143], v[198:199] op_sel_hi:[1,0]
	v_pk_mul_f32 v[168:169], v[144:145], v[198:199] op_sel_hi:[1,0]
	v_pk_mul_f32 v[208:209], v[126:127], v[158:159]
	v_pk_mul_f32 v[206:207], v[128:129], v[168:169]
	v_pk_mul_f32 v[126:127], v[138:139], v[198:199] op_sel_hi:[1,0]
	v_pk_mul_f32 v[128:129], v[140:141], v[198:199] op_sel_hi:[1,0]
	s_cmp_eq_u32 s26, 4
	v_pk_mul_f32 v[210:211], v[124:125], v[128:129]
	v_pk_mul_f32 v[212:213], v[122:123], v[126:127]
	s_mov_b64 s[26:27], -1
	v_or_b32_e32 v200, 0x8000, v0
	v_or_b32_e32 v196, 0x8040, v0
	v_or_b32_e32 v188, 0x10000, v0
	v_or_b32_e32 v184, 0x10040, v0
	v_or_b32_e32 v182, 0x18000, v0
	v_or_b32_e32 v178, 0x18040, v0
	v_add_u32_e32 v176, 0x40000, v0
	v_add_u32_e32 v172, 0x40040, v0
	v_add_u32_e32 v168, 0x48000, v0
	v_add_u32_e32 v158, 0x48040, v0
	v_add_u32_e32 v128, 0x50000, v0
	v_add_u32_e32 v126, 0x50040, v0
	v_add_u32_e32 v124, 0x58000, v0
	v_pk_mul_f32 v[204:205], v[134:135], v[198:199]
	v_pk_mul_f32 v[202:203], v[130:131], v[198:199]
	v_add_u32_e32 v122, 0x58040, v0
	s_cbranch_scc1 .LBB0_616
	v_cvt_pk_bf16_f32 v218, v208, v209
	v_cvt_pk_bf16_f32 v219, v206, v207
	v_lshl_add_u64 v[190:191], v[160:161], 0, v[0:1]
	v_mov_b32_e32 v199, v198
	v_cvt_pk_bf16_f32 v220, v212, v213
	v_cvt_pk_bf16_f32 v221, v210, v211
	global_store_dwordx4 v[190:191], v[218:221], off
	v_pk_mul_f32 v[222:223], v[132:133], v[198:199]
	v_pk_mul_f32 v[228:229], v[114:115], v[202:203]
	v_pk_mul_f32 v[218:219], v[136:137], v[198:199]
	v_pk_mul_f32 v[222:223], v[116:117], v[222:223]
	v_pk_mul_f32 v[220:221], v[120:121], v[218:219]
	v_pk_mul_f32 v[218:219], v[118:119], v[204:205]
	v_mov_b32_e32 v201, v1
	v_cvt_pk_bf16_f32 v218, v218, v219
	v_cvt_pk_bf16_f32 v219, v220, v221
	v_cvt_pk_bf16_f32 v220, v228, v229
	v_cvt_pk_bf16_f32 v221, v222, v223
	global_store_dwordx4 v[190:191], v[218:221], off offset:64
	v_pk_mul_f32 v[190:191], v[144:145], v[186:187] op_sel_hi:[1,0]
	v_pk_mul_f32 v[222:223], v[138:139], v[186:187] op_sel_hi:[1,0]
	v_pk_mul_f32 v[218:219], v[142:143], v[186:187] op_sel_hi:[1,0]
	v_pk_mul_f32 v[190:191], v[112:113], v[190:191]
	v_pk_mul_f32 v[218:219], v[110:111], v[218:219]
	v_pk_mul_f32 v[220:221], v[140:141], v[186:187] op_sel_hi:[1,0]
	v_cvt_pk_bf16_f32 v218, v218, v219
	v_cvt_pk_bf16_f32 v219, v190, v191
	v_lshl_add_u64 v[190:191], v[160:161], 0, v[200:201]
	v_pk_mul_f32 v[228:229], v[108:109], v[220:221]
	v_pk_mul_f32 v[220:221], v[106:107], v[222:223]
	v_pk_mul_f32 v[222:223], v[130:131], v[186:187] op_sel_hi:[1,0]
	v_cvt_pk_bf16_f32 v220, v220, v221
	v_cvt_pk_bf16_f32 v221, v228, v229
	global_store_dwordx4 v[190:191], v[218:221], off
	v_pk_mul_f32 v[190:191], v[136:137], v[186:187] op_sel_hi:[1,0]
	v_mov_b32_e32 v197, v1
	v_pk_mul_f32 v[218:219], v[134:135], v[186:187] op_sel_hi:[1,0]
	v_pk_mul_f32 v[190:191], v[104:105], v[190:191]
	v_pk_mul_f32 v[218:219], v[102:103], v[218:219]
	v_pk_mul_f32 v[220:221], v[132:133], v[186:187] op_sel_hi:[1,0]
	v_cvt_pk_bf16_f32 v218, v218, v219
	v_cvt_pk_bf16_f32 v219, v190, v191
	v_lshl_add_u64 v[190:191], v[160:161], 0, v[196:197]
	v_pk_mul_f32 v[228:229], v[100:101], v[220:221]
	v_pk_mul_f32 v[220:221], v[98:99], v[222:223]
	v_pk_mul_f32 v[222:223], v[138:139], v[180:181] op_sel_hi:[1,0]
	v_cvt_pk_bf16_f32 v220, v220, v221
	v_cvt_pk_bf16_f32 v221, v228, v229
	global_store_dwordx4 v[190:191], v[218:221], off
; #define PG8_PACK8(y0, y1) (u32x4){cvt_pk_bf16((y0)[0], (y0)[1]), cvt_pk_bf16((y0)[2], (y0)[3]), cvt_pk_bf16((y1)[0], (y1)[1]), cvt_pk_bf16((y1)[2], (y1)[3])}
;     __device__ __forceinline__ void operator()(const f32x4 (&acc)[2][2][4][2], const Unit& u, int ui, int wr, int wc, int fr, int fq) const {
;     ...
;                 for (int ai = 0; ai < 2; ++ai)
; #pragma unroll
;                     for (int m = 0; m < 4; ++m) {
;                         const unsigned row = row0 + ai * HALF + m * 16; const float r2 = ss[ai][m];
; #pragma unroll
;                         for (int bj = 0; bj < 2; ++bj) {
;                             const f32x4 z0 = acc[ai][bj][m][0] * (g[bj][0] * r2), z1 = acc[ai][bj][m][1] * (g[bj][1] * r2);
;                             *(u32x4*)(dst + (size_t)(row * 2048u + 64u * bj)) = PG8_PACK8(z0, z1);
	v_pk_mul_f32 v[190:191], v[144:145], v[180:181] op_sel_hi:[1,0]
	v_mov_b32_e32 v189, v1
	v_pk_mul_f32 v[218:219], v[142:143], v[180:181] op_sel_hi:[1,0]
	v_pk_mul_f32 v[190:191], v[96:97], v[190:191]
	v_pk_mul_f32 v[218:219], v[94:95], v[218:219]
	v_pk_mul_f32 v[220:221], v[140:141], v[180:181] op_sel_hi:[1,0]
	v_cvt_pk_bf16_f32 v218, v218, v219
	v_cvt_pk_bf16_f32 v219, v190, v191
	v_lshl_add_u64 v[190:191], v[160:161], 0, v[188:189]
	v_pk_mul_f32 v[228:229], v[92:93], v[220:221]
	v_pk_mul_f32 v[220:221], v[90:91], v[222:223]
	v_pk_mul_f32 v[222:223], v[130:131], v[180:181] op_sel_hi:[1,0]
	v_cvt_pk_bf16_f32 v220, v220, v221
	v_cvt_pk_bf16_f32 v221, v228, v229
	global_store_dwordx4 v[190:191], v[218:221], off
	v_pk_mul_f32 v[190:191], v[136:137], v[180:181] op_sel_hi:[1,0]
	v_mov_b32_e32 v185, v1
	v_pk_mul_f32 v[218:219], v[134:135], v[180:181] op_sel_hi:[1,0]
	v_pk_mul_f32 v[190:191], v[88:89], v[190:191]
	v_pk_mul_f32 v[218:219], v[86:87], v[218:219]
	v_pk_mul_f32 v[220:221], v[132:133], v[180:181] op_sel_hi:[1,0]
	v_cvt_pk_bf16_f32 v218, v218, v219
	v_cvt_pk_bf16_f32 v219, v190, v191
	v_lshl_add_u64 v[190:191], v[160:161], 0, v[184:185]
	v_pk_mul_f32 v[228:229], v[84:85], v[220:221]
	v_pk_mul_f32 v[220:221], v[82:83], v[222:223]
	v_pk_mul_f32 v[222:223], v[138:139], v[174:175] op_sel_hi:[1,0]
	v_cvt_pk_bf16_f32 v220, v220, v221
	v_cvt_pk_bf16_f32 v221, v228, v229
	global_store_dwordx4 v[190:191], v[218:221], off
	v_pk_mul_f32 v[190:191], v[144:145], v[174:175] op_sel_hi:[1,0]
	v_mov_b32_e32 v183, v1
	v_pk_mul_f32 v[218:219], v[142:143], v[174:175] op_sel_hi:[1,0]
	v_pk_mul_f32 v[190:191], v[80:81], v[190:191]
	v_pk_mul_f32 v[218:219], v[78:79], v[218:219]
	v_pk_mul_f32 v[220:221], v[140:141], v[174:175] op_sel_hi:[1,0]
	v_cvt_pk_bf16_f32 v218, v218, v219
	v_cvt_pk_bf16_f32 v219, v190, v191
	v_lshl_add_u64 v[190:191], v[160:161], 0, v[182:183]
	v_pk_mul_f32 v[228:229], v[76:77], v[220:221]
	v_pk_mul_f32 v[220:221], v[74:75], v[222:223]
	v_pk_mul_f32 v[222:223], v[130:131], v[174:175] op_sel_hi:[1,0]
	v_cvt_pk_bf16_f32 v220, v220, v221
	v_cvt_pk_bf16_f32 v221, v228, v229
	global_store_dwordx4 v[190:191], v[218:221], off
	v_pk_mul_f32 v[190:191], v[136:137], v[174:175] op_sel_hi:[1,0]
	v_mov_b32_e32 v179, v1
	v_pk_mul_f32 v[218:219], v[134:135], v[174:175] op_sel_hi:[1,0]
	v_pk_mul_f32 v[190:191], v[72:73], v[190:191]
	v_pk_mul_f32 v[218:219], v[70:71], v[218:219]
	v_pk_mul_f32 v[220:221], v[132:133], v[174:175] op_sel_hi:[1,0]
	v_cvt_pk_bf16_f32 v218, v218, v219
	v_cvt_pk_bf16_f32 v219, v190, v191
	v_lshl_add_u64 v[190:191], v[160:161], 0, v[178:179]
	v_pk_mul_f32 v[228:229], v[68:69], v[220:221]
	v_pk_mul_f32 v[220:221], v[66:67], v[222:223]
	v_pk_mul_f32 v[222:223], v[138:139], v[170:171] op_sel_hi:[1,0]
	v_cvt_pk_bf16_f32 v220, v220, v221
	v_cvt_pk_bf16_f32 v221, v228, v229
	global_store_dwordx4 v[190:191], v[218:221], off
	v_pk_mul_f32 v[190:191], v[144:145], v[170:171] op_sel_hi:[1,0]
	v_mov_b32_e32 v177, v1
	v_pk_mul_f32 v[218:219], v[142:143], v[170:171] op_sel_hi:[1,0]
	v_pk_mul_f32 v[190:191], v[64:65], v[190:191]
	v_pk_mul_f32 v[218:219], v[62:63], v[218:219]
	v_pk_mul_f32 v[220:221], v[140:141], v[170:171] op_sel_hi:[1,0]
	v_cvt_pk_bf16_f32 v218, v218, v219
	v_cvt_pk_bf16_f32 v219, v190, v191
	v_lshl_add_u64 v[190:191], v[160:161], 0, v[176:177]
	v_pk_mul_f32 v[228:229], v[60:61], v[220:221]
	v_pk_mul_f32 v[220:221], v[58:59], v[222:223]
	v_pk_mul_f32 v[222:223], v[130:131], v[170:171] op_sel_hi:[1,0]
	v_cvt_pk_bf16_f32 v220, v220, v221
	v_cvt_pk_bf16_f32 v221, v228, v229
	global_store_dwordx4 v[190:191], v[218:221], off
	v_pk_mul_f32 v[190:191], v[136:137], v[170:171] op_sel_hi:[1,0]
	v_mov_b32_e32 v173, v1
	v_pk_mul_f32 v[218:219], v[134:135], v[170:171] op_sel_hi:[1,0]
	v_pk_mul_f32 v[190:191], v[56:57], v[190:191]
	v_pk_mul_f32 v[218:219], v[54:55], v[218:219]
	v_pk_mul_f32 v[220:221], v[132:133], v[170:171] op_sel_hi:[1,0]
	v_cvt_pk_bf16_f32 v218, v218, v219
	v_cvt_pk_bf16_f32 v219, v190, v191
	v_lshl_add_u64 v[190:191], v[160:161], 0, v[172:173]
	v_pk_mul_f32 v[228:229], v[52:53], v[220:221]
	v_pk_mul_f32 v[220:221], v[50:51], v[222:223]
	v_pk_mul_f32 v[222:223], v[138:139], v[166:167] op_sel_hi:[1,0]
	v_cvt_pk_bf16_f32 v220, v220, v221
	v_cvt_pk_bf16_f32 v221, v228, v229
	global_store_dwordx4 v[190:191], v[218:221], off
	v_pk_mul_f32 v[190:191], v[144:145], v[166:167] op_sel_hi:[1,0]
	v_mov_b32_e32 v169, v1
	v_pk_mul_f32 v[218:219], v[142:143], v[166:167] op_sel_hi:[1,0]
	v_pk_mul_f32 v[190:191], v[48:49], v[190:191]
	v_pk_mul_f32 v[218:219], v[46:47], v[218:219]
	v_pk_mul_f32 v[220:221], v[140:141], v[166:167] op_sel_hi:[1,0]
	v_cvt_pk_bf16_f32 v218, v218, v219
	v_cvt_pk_bf16_f32 v219, v190, v191
	v_lshl_add_u64 v[190:191], v[160:161], 0, v[168:169]
	v_pk_mul_f32 v[228:229], v[44:45], v[220:221]
	v_pk_mul_f32 v[220:221], v[42:43], v[222:223]
	v_pk_mul_f32 v[222:223], v[130:131], v[166:167] op_sel_hi:[1,0]
	v_cvt_pk_bf16_f32 v220, v220, v221
	v_cvt_pk_bf16_f32 v221, v228, v229
	global_store_dwordx4 v[190:191], v[218:221], off
	v_pk_mul_f32 v[190:191], v[136:137], v[166:167] op_sel_hi:[1,0]
	v_mov_b32_e32 v159, v1
	v_pk_mul_f32 v[218:219], v[134:135], v[166:167] op_sel_hi:[1,0]
	v_pk_mul_f32 v[190:191], v[40:41], v[190:191]
	v_pk_mul_f32 v[218:219], v[38:39], v[218:219]
	v_pk_mul_f32 v[220:221], v[132:133], v[166:167] op_sel_hi:[1,0]
	v_cvt_pk_bf16_f32 v218, v218, v219
	v_cvt_pk_bf16_f32 v219, v190, v191
	v_lshl_add_u64 v[190:191], v[160:161], 0, v[158:159]
	v_pk_mul_f32 v[228:229], v[36:37], v[220:221]
	v_pk_mul_f32 v[220:221], v[34:35], v[222:223]
	v_pk_mul_f32 v[222:223], v[138:139], v[164:165] op_sel_hi:[1,0]
; #define PG8_PACK8(y0, y1) (u32x4){cvt_pk_bf16((y0)[0], (y0)[1]), cvt_pk_bf16((y0)[2], (y0)[3]), cvt_pk_bf16((y1)[0], (y1)[1]), cvt_pk_bf16((y1)[2], (y1)[3])}
;     __device__ __forceinline__ void operator()(const f32x4 (&acc)[2][2][4][2], const Unit& u, int ui, int wr, int wc, int fr, int fq) const {
;     ...
;             if (pn != 4) {
; #pragma unroll
;                 for (int ai = 0; ai < 2; ++ai)
; #pragma unroll
;                     for (int m = 0; m < 4; ++m) {
;                         const unsigned row = row0 + ai * HALF + m * 16; const float r2 = ss[ai][m];
; #pragma unroll
;                         for (int bj = 0; bj < 2; ++bj) {
;                             const f32x4 z0 = acc[ai][bj][m][0] * (g[bj][0] * r2), z1 = acc[ai][bj][m][1] * (g[bj][1] * r2);
;                             *(u32x4*)(dst + (size_t)(row * 2048u + 64u * bj)) = PG8_PACK8(z0, z1);
;                         }
;                     }
;             } else {
;                 f32x4 ks[2][2];
; #pragma unroll
;                 for (int bj = 0; bj < 2; ++bj)
; #pragma unroll
;                     for (int n = 0; n < 2; ++n) ks[bj][n] = (f32x4){0.f, 0.f, 0.f, 0.f};
; #pragma unroll
;                 for (int ai = 0; ai < 2; ++ai)
; #pragma unroll
;                     for (int m = 0; m < 4; ++m) {
;                         const unsigned row = row0 + ai * HALF + m * 16; const float r2 = ss[ai][m];
; #pragma unroll
;                         for (int bj = 0; bj < 2; ++bj) {
;                             const f32x4 z0 = acc[ai][bj][m][0] * (g[bj][0] * r2), z1 = acc[ai][bj][m][1] * (g[bj][1] * r2);
;                             ks[bj][0] += z0; ks[bj][1] += z1;
;                             *(u32x4*)(dst + (size_t)(row * 2048u + 64u * bj)) = PG8_PACK8(z0, z1);
;                         }
;                     }
	v_cvt_pk_bf16_f32 v220, v220, v221
	v_cvt_pk_bf16_f32 v221, v228, v229
	global_store_dwordx4 v[190:191], v[218:221], off
	v_pk_mul_f32 v[190:191], v[144:145], v[164:165] op_sel_hi:[1,0]
	v_mov_b32_e32 v129, v1
	v_pk_mul_f32 v[218:219], v[142:143], v[164:165] op_sel_hi:[1,0]
	v_pk_mul_f32 v[190:191], v[32:33], v[190:191]
	v_pk_mul_f32 v[218:219], v[30:31], v[218:219]
	v_pk_mul_f32 v[220:221], v[140:141], v[164:165] op_sel_hi:[1,0]
	v_cvt_pk_bf16_f32 v218, v218, v219
	v_cvt_pk_bf16_f32 v219, v190, v191
	v_lshl_add_u64 v[190:191], v[160:161], 0, v[128:129]
	v_pk_mul_f32 v[228:229], v[28:29], v[220:221]
	v_pk_mul_f32 v[220:221], v[26:27], v[222:223]
	v_pk_mul_f32 v[222:223], v[130:131], v[164:165] op_sel_hi:[1,0]
	v_cvt_pk_bf16_f32 v220, v220, v221
	v_cvt_pk_bf16_f32 v221, v228, v229
	global_store_dwordx4 v[190:191], v[218:221], off
	v_pk_mul_f32 v[190:191], v[136:137], v[164:165] op_sel_hi:[1,0]
	v_mov_b32_e32 v127, v1
	v_pk_mul_f32 v[218:219], v[134:135], v[164:165] op_sel_hi:[1,0]
	v_pk_mul_f32 v[190:191], v[24:25], v[190:191]
	v_pk_mul_f32 v[218:219], v[22:23], v[218:219]
	v_pk_mul_f32 v[220:221], v[132:133], v[164:165] op_sel_hi:[1,0]
	v_cvt_pk_bf16_f32 v218, v218, v219
	v_cvt_pk_bf16_f32 v219, v190, v191
	v_lshl_add_u64 v[190:191], v[160:161], 0, v[126:127]
	v_pk_mul_f32 v[228:229], v[20:21], v[220:221]
	v_pk_mul_f32 v[220:221], v[18:19], v[222:223]
	v_pk_mul_f32 v[222:223], v[138:139], v[162:163] op_sel_hi:[1,0]
	v_cvt_pk_bf16_f32 v220, v220, v221
	v_cvt_pk_bf16_f32 v221, v228, v229
	global_store_dwordx4 v[190:191], v[218:221], off
	v_pk_mul_f32 v[190:191], v[144:145], v[162:163] op_sel_hi:[1,0]
	v_mov_b32_e32 v125, v1
	v_pk_mul_f32 v[218:219], v[142:143], v[162:163] op_sel_hi:[1,0]
	v_pk_mul_f32 v[190:191], v[16:17], v[190:191]
	v_pk_mul_f32 v[218:219], v[14:15], v[218:219]
	v_pk_mul_f32 v[220:221], v[140:141], v[162:163] op_sel_hi:[1,0]
	v_cvt_pk_bf16_f32 v218, v218, v219
	v_cvt_pk_bf16_f32 v219, v190, v191
	v_lshl_add_u64 v[190:191], v[160:161], 0, v[124:125]
	v_pk_mul_f32 v[228:229], v[12:13], v[220:221]
	v_pk_mul_f32 v[220:221], v[10:11], v[222:223]
	v_pk_mul_f32 v[222:223], v[130:131], v[162:163] op_sel_hi:[1,0]
	v_cvt_pk_bf16_f32 v220, v220, v221
	v_cvt_pk_bf16_f32 v221, v228, v229
	global_store_dwordx4 v[190:191], v[218:221], off
	v_pk_mul_f32 v[190:191], v[136:137], v[162:163] op_sel_hi:[1,0]
	v_mov_b32_e32 v123, v1
	v_pk_mul_f32 v[218:219], v[134:135], v[162:163] op_sel_hi:[1,0]
	v_pk_mul_f32 v[190:191], v[8:9], v[190:191]
	v_pk_mul_f32 v[218:219], v[6:7], v[218:219]
	v_pk_mul_f32 v[220:221], v[132:133], v[162:163] op_sel_hi:[1,0]
	v_cvt_pk_bf16_f32 v218, v218, v219
	v_cvt_pk_bf16_f32 v219, v190, v191
	v_lshl_add_u64 v[190:191], v[160:161], 0, v[122:123]
	v_pk_mul_f32 v[228:229], v[4:5], v[220:221]
	v_pk_mul_f32 v[220:221], v[2:3], v[222:223]
	s_mov_b64 s[26:27], 0
	v_cvt_pk_bf16_f32 v220, v220, v221
	v_cvt_pk_bf16_f32 v221, v228, v229
	global_store_dwordx4 v[190:191], v[218:221], off
.LBB0_616:
	s_andn2_b64 vcc, exec, s[26:27]
	s_cbranch_vccnz .LBB0_620
	v_mov_b32_e32 v199, v198
	v_pk_add_f32 v[190:191], v[206:207], 0 op_sel_hi:[1,0]
	v_pk_add_f32 v[222:223], v[208:209], 0 op_sel_hi:[1,0]
	v_cvt_pk_bf16_f32 v218, v208, v209
	v_cvt_pk_bf16_f32 v219, v206, v207
	v_cvt_pk_bf16_f32 v220, v212, v213
	v_cvt_pk_bf16_f32 v221, v210, v211
	v_lshl_add_u64 v[206:207], v[160:161], 0, v[0:1]
	v_pk_mul_f32 v[208:209], v[136:137], v[198:199]
	v_pk_mul_f32 v[198:199], v[132:133], v[198:199]
	v_pk_add_f32 v[228:229], v[210:211], 0 op_sel_hi:[1,0]
	v_pk_add_f32 v[240:241], v[212:213], 0 op_sel_hi:[1,0]
	global_store_dwordx4 v[206:207], v[218:221], off
	v_pk_mul_f32 v[210:211], v[120:121], v[208:209]
	v_pk_mul_f32 v[212:213], v[118:119], v[204:205]
	v_pk_mul_f32 v[218:219], v[116:117], v[198:199]
	v_pk_mul_f32 v[220:221], v[114:115], v[202:203]
	v_pk_fma_f32 v[198:199], v[116:117], v[198:199], 0 op_sel_hi:[1,1,0]
	v_pk_fma_f32 v[202:203], v[114:115], v[202:203], 0 op_sel_hi:[1,1,0]
	v_cvt_pk_bf16_f32 v114, v212, v213
	v_cvt_pk_bf16_f32 v115, v210, v211
	v_cvt_pk_bf16_f32 v116, v220, v221
	v_cvt_pk_bf16_f32 v117, v218, v219
	v_pk_fma_f32 v[120:121], v[120:121], v[208:209], 0 op_sel_hi:[1,1,0]
	global_store_dwordx4 v[206:207], v[114:117], off offset:64
	v_pk_mul_f32 v[208:209], v[140:141], v[186:187] op_sel_hi:[1,0]
	v_pk_mul_f32 v[210:211], v[138:139], v[186:187] op_sel_hi:[1,0]
	v_pk_mul_f32 v[114:115], v[144:145], v[186:187] op_sel_hi:[1,0]
	v_pk_mul_f32 v[116:117], v[142:143], v[186:187] op_sel_hi:[1,0]
	v_mov_b32_e32 v201, v1
	v_pk_fma_f32 v[118:119], v[118:119], v[204:205], 0 op_sel_hi:[1,1,0]
	v_pk_mul_f32 v[204:205], v[112:113], v[114:115]
	v_pk_mul_f32 v[206:207], v[110:111], v[116:117]
	v_pk_mul_f32 v[212:213], v[108:109], v[208:209]
	v_pk_mul_f32 v[218:219], v[106:107], v[210:211]
	v_pk_fma_f32 v[112:113], v[112:113], v[114:115], v[190:191]
	v_pk_fma_f32 v[110:111], v[110:111], v[116:117], v[222:223]
	v_pk_fma_f32 v[114:115], v[108:109], v[208:209], v[228:229]
	v_pk_fma_f32 v[116:117], v[106:107], v[210:211], v[240:241]
	v_cvt_pk_bf16_f32 v106, v206, v207
	v_cvt_pk_bf16_f32 v107, v204, v205
	v_cvt_pk_bf16_f32 v108, v218, v219
	v_cvt_pk_bf16_f32 v109, v212, v213
	v_lshl_add_u64 v[190:191], v[160:161], 0, v[200:201]
	global_store_dwordx4 v[190:191], v[106:109], off
	v_pk_mul_f32 v[204:205], v[132:133], v[186:187] op_sel_hi:[1,0]
	v_pk_mul_f32 v[206:207], v[130:131], v[186:187] op_sel_hi:[1,0]
	v_pk_mul_f32 v[106:107], v[136:137], v[186:187] op_sel_hi:[1,0]
	v_pk_mul_f32 v[108:109], v[134:135], v[186:187] op_sel_hi:[1,0]
	v_mov_b32_e32 v197, v1
	v_pk_mul_f32 v[190:191], v[104:105], v[106:107]
	v_pk_mul_f32 v[200:201], v[102:103], v[108:109]
; #define PG8_PACK8(y0, y1) (u32x4){cvt_pk_bf16((y0)[0], (y0)[1]), cvt_pk_bf16((y0)[2], (y0)[3]), cvt_pk_bf16((y1)[0], (y1)[1]), cvt_pk_bf16((y1)[2], (y1)[3])}
;     __device__ __forceinline__ void operator()(const f32x4 (&acc)[2][2][4][2], const Unit& u, int ui, int wr, int wc, int fr, int fq) const {
;     ...
;                 for (int ai = 0; ai < 2; ++ai)
; #pragma unroll
;                     for (int m = 0; m < 4; ++m) {
;                         const unsigned row = row0 + ai * HALF + m * 16; const float r2 = ss[ai][m];
; #pragma unroll
;                         for (int bj = 0; bj < 2; ++bj) {
;                             const f32x4 z0 = acc[ai][bj][m][0] * (g[bj][0] * r2), z1 = acc[ai][bj][m][1] * (g[bj][1] * r2);
;                             ks[bj][0] += z0; ks[bj][1] += z1;
;                             *(u32x4*)(dst + (size_t)(row * 2048u + 64u * bj)) = PG8_PACK8(z0, z1);
;                         }
;                     }
	v_pk_mul_f32 v[208:209], v[100:101], v[204:205]
	v_pk_mul_f32 v[210:211], v[98:99], v[206:207]
	v_pk_fma_f32 v[104:105], v[104:105], v[106:107], v[120:121]
	v_pk_fma_f32 v[102:103], v[102:103], v[108:109], v[118:119]
	v_pk_fma_f32 v[106:107], v[100:101], v[204:205], v[198:199]
	v_pk_fma_f32 v[108:109], v[98:99], v[206:207], v[202:203]
	v_cvt_pk_bf16_f32 v98, v200, v201
	v_cvt_pk_bf16_f32 v99, v190, v191
	v_cvt_pk_bf16_f32 v100, v210, v211
	v_cvt_pk_bf16_f32 v101, v208, v209
	v_lshl_add_u64 v[118:119], v[160:161], 0, v[196:197]
	global_store_dwordx4 v[118:119], v[98:101], off
	v_pk_mul_f32 v[190:191], v[140:141], v[180:181] op_sel_hi:[1,0]
	v_pk_mul_f32 v[196:197], v[138:139], v[180:181] op_sel_hi:[1,0]
	v_pk_mul_f32 v[98:99], v[144:145], v[180:181] op_sel_hi:[1,0]
	v_pk_mul_f32 v[100:101], v[142:143], v[180:181] op_sel_hi:[1,0]
	v_mov_b32_e32 v189, v1
	v_pk_mul_f32 v[118:119], v[96:97], v[98:99]
	v_pk_mul_f32 v[120:121], v[94:95], v[100:101]
	v_pk_mul_f32 v[198:199], v[92:93], v[190:191]
	v_pk_mul_f32 v[200:201], v[90:91], v[196:197]
	v_pk_fma_f32 v[96:97], v[96:97], v[98:99], v[112:113]
	v_pk_fma_f32 v[94:95], v[94:95], v[100:101], v[110:111]
	v_pk_fma_f32 v[98:99], v[92:93], v[190:191], v[114:115]
	v_pk_fma_f32 v[100:101], v[90:91], v[196:197], v[116:117]
	v_cvt_pk_bf16_f32 v90, v120, v121
	v_cvt_pk_bf16_f32 v91, v118, v119
	v_cvt_pk_bf16_f32 v92, v200, v201
	v_cvt_pk_bf16_f32 v93, v198, v199
	v_lshl_add_u64 v[110:111], v[160:161], 0, v[188:189]
	global_store_dwordx4 v[110:111], v[90:93], off
	v_pk_mul_f32 v[114:115], v[132:133], v[180:181] op_sel_hi:[1,0]
	v_pk_mul_f32 v[116:117], v[130:131], v[180:181] op_sel_hi:[1,0]
	v_pk_mul_f32 v[90:91], v[136:137], v[180:181] op_sel_hi:[1,0]
	v_pk_mul_f32 v[92:93], v[134:135], v[180:181] op_sel_hi:[1,0]
	v_mov_b32_e32 v185, v1
	v_pk_mul_f32 v[110:111], v[88:89], v[90:91]
	v_pk_mul_f32 v[112:113], v[86:87], v[92:93]
	v_pk_mul_f32 v[118:119], v[84:85], v[114:115]
	v_pk_mul_f32 v[120:121], v[82:83], v[116:117]
	v_pk_fma_f32 v[88:89], v[88:89], v[90:91], v[104:105]
	v_pk_fma_f32 v[86:87], v[86:87], v[92:93], v[102:103]
	v_pk_fma_f32 v[90:91], v[84:85], v[114:115], v[106:107]
	v_pk_fma_f32 v[92:93], v[82:83], v[116:117], v[108:109]
	v_cvt_pk_bf16_f32 v82, v112, v113
	v_cvt_pk_bf16_f32 v83, v110, v111
	v_cvt_pk_bf16_f32 v84, v120, v121
	v_cvt_pk_bf16_f32 v85, v118, v119
	v_lshl_add_u64 v[102:103], v[160:161], 0, v[184:185]
	global_store_dwordx4 v[102:103], v[82:85], off
	v_pk_mul_f32 v[106:107], v[140:141], v[174:175] op_sel_hi:[1,0]
	v_pk_mul_f32 v[108:109], v[138:139], v[174:175] op_sel_hi:[1,0]
	v_pk_mul_f32 v[82:83], v[144:145], v[174:175] op_sel_hi:[1,0]
	v_pk_mul_f32 v[84:85], v[142:143], v[174:175] op_sel_hi:[1,0]
	v_mov_b32_e32 v183, v1
	v_pk_mul_f32 v[102:103], v[80:81], v[82:83]
	v_pk_mul_f32 v[104:105], v[78:79], v[84:85]
	v_pk_mul_f32 v[110:111], v[76:77], v[106:107]
	v_pk_mul_f32 v[112:113], v[74:75], v[108:109]
	v_pk_fma_f32 v[80:81], v[80:81], v[82:83], v[96:97]
	v_pk_fma_f32 v[78:79], v[78:79], v[84:85], v[94:95]
	v_pk_fma_f32 v[82:83], v[76:77], v[106:107], v[98:99]
	v_pk_fma_f32 v[84:85], v[74:75], v[108:109], v[100:101]
	v_cvt_pk_bf16_f32 v74, v104, v105
	v_cvt_pk_bf16_f32 v75, v102, v103
	v_cvt_pk_bf16_f32 v76, v112, v113
	v_cvt_pk_bf16_f32 v77, v110, v111
	v_lshl_add_u64 v[94:95], v[160:161], 0, v[182:183]
	global_store_dwordx4 v[94:95], v[74:77], off
	v_pk_mul_f32 v[98:99], v[132:133], v[174:175] op_sel_hi:[1,0]
	v_pk_mul_f32 v[100:101], v[130:131], v[174:175] op_sel_hi:[1,0]
	v_pk_mul_f32 v[74:75], v[136:137], v[174:175] op_sel_hi:[1,0]
	v_pk_mul_f32 v[76:77], v[134:135], v[174:175] op_sel_hi:[1,0]
	v_mov_b32_e32 v179, v1
	v_pk_mul_f32 v[94:95], v[72:73], v[74:75]
	v_pk_mul_f32 v[96:97], v[70:71], v[76:77]
	v_pk_mul_f32 v[102:103], v[68:69], v[98:99]
	v_pk_mul_f32 v[104:105], v[66:67], v[100:101]
	v_pk_fma_f32 v[72:73], v[72:73], v[74:75], v[88:89]
	v_pk_fma_f32 v[70:71], v[70:71], v[76:77], v[86:87]
	v_pk_fma_f32 v[74:75], v[68:69], v[98:99], v[90:91]
	v_pk_fma_f32 v[76:77], v[66:67], v[100:101], v[92:93]
	v_cvt_pk_bf16_f32 v66, v96, v97
	v_cvt_pk_bf16_f32 v67, v94, v95
	v_cvt_pk_bf16_f32 v68, v104, v105
	v_cvt_pk_bf16_f32 v69, v102, v103
	v_lshl_add_u64 v[86:87], v[160:161], 0, v[178:179]
	global_store_dwordx4 v[86:87], v[66:69], off
	v_pk_mul_f32 v[90:91], v[140:141], v[170:171] op_sel_hi:[1,0]
	v_pk_mul_f32 v[92:93], v[138:139], v[170:171] op_sel_hi:[1,0]
	v_pk_mul_f32 v[66:67], v[144:145], v[170:171] op_sel_hi:[1,0]
	v_pk_mul_f32 v[68:69], v[142:143], v[170:171] op_sel_hi:[1,0]
	v_mov_b32_e32 v177, v1
	v_pk_mul_f32 v[86:87], v[64:65], v[66:67]
	v_pk_mul_f32 v[88:89], v[62:63], v[68:69]
	v_pk_mul_f32 v[94:95], v[60:61], v[90:91]
	v_pk_mul_f32 v[96:97], v[58:59], v[92:93]
	v_pk_fma_f32 v[64:65], v[64:65], v[66:67], v[80:81]
	v_pk_fma_f32 v[62:63], v[62:63], v[68:69], v[78:79]
	v_pk_fma_f32 v[66:67], v[60:61], v[90:91], v[82:83]
	v_pk_fma_f32 v[68:69], v[58:59], v[92:93], v[84:85]
	v_cvt_pk_bf16_f32 v58, v88, v89
	v_cvt_pk_bf16_f32 v59, v86, v87
	v_cvt_pk_bf16_f32 v60, v96, v97
	v_cvt_pk_bf16_f32 v61, v94, v95
	v_lshl_add_u64 v[78:79], v[160:161], 0, v[176:177]
	global_store_dwordx4 v[78:79], v[58:61], off
	v_pk_mul_f32 v[82:83], v[132:133], v[170:171] op_sel_hi:[1,0]
	v_pk_mul_f32 v[84:85], v[130:131], v[170:171] op_sel_hi:[1,0]
	v_pk_mul_f32 v[58:59], v[136:137], v[170:171] op_sel_hi:[1,0]
	v_pk_mul_f32 v[60:61], v[134:135], v[170:171] op_sel_hi:[1,0]
	v_mov_b32_e32 v173, v1
	v_pk_mul_f32 v[78:79], v[56:57], v[58:59]
	v_pk_mul_f32 v[80:81], v[54:55], v[60:61]
	v_pk_mul_f32 v[86:87], v[52:53], v[82:83]
	v_pk_mul_f32 v[88:89], v[50:51], v[84:85]
	v_pk_fma_f32 v[56:57], v[56:57], v[58:59], v[72:73]
; #define PG8_PACK8(y0, y1) (u32x4){cvt_pk_bf16((y0)[0], (y0)[1]), cvt_pk_bf16((y0)[2], (y0)[3]), cvt_pk_bf16((y1)[0], (y1)[1]), cvt_pk_bf16((y1)[2], (y1)[3])}
;     __device__ __forceinline__ void operator()(const f32x4 (&acc)[2][2][4][2], const Unit& u, int ui, int wr, int wc, int fr, int fq) const {
;     ...
;                 for (int ai = 0; ai < 2; ++ai)
; #pragma unroll
;                     for (int m = 0; m < 4; ++m) {
;                         const unsigned row = row0 + ai * HALF + m * 16; const float r2 = ss[ai][m];
; #pragma unroll
;                         for (int bj = 0; bj < 2; ++bj) {
;                             const f32x4 z0 = acc[ai][bj][m][0] * (g[bj][0] * r2), z1 = acc[ai][bj][m][1] * (g[bj][1] * r2);
;                             ks[bj][0] += z0; ks[bj][1] += z1;
;                             *(u32x4*)(dst + (size_t)(row * 2048u + 64u * bj)) = PG8_PACK8(z0, z1);
;                         }
;                     }
; #pragma unroll
;                 for (int bj = 0; bj < 2; ++bj)
; #pragma unroll
;                     for (int n = 0; n < 2; ++n)
; #pragma unroll
;                         for (int e = 0; e < 4; ++e) { float s = ks[bj][n][e]; s += __shfl_xor(s, 1); s += __shfl_xor(s, 2); s += __shfl_xor(s, 4); s += __shfl_xor(s, 8); ks[bj][n][e] = s; }
	v_pk_fma_f32 v[54:55], v[54:55], v[60:61], v[70:71]
	v_pk_fma_f32 v[58:59], v[52:53], v[82:83], v[74:75]
	v_pk_fma_f32 v[60:61], v[50:51], v[84:85], v[76:77]
	v_cvt_pk_bf16_f32 v50, v80, v81
	v_cvt_pk_bf16_f32 v51, v78, v79
	v_cvt_pk_bf16_f32 v52, v88, v89
	v_cvt_pk_bf16_f32 v53, v86, v87
	v_lshl_add_u64 v[70:71], v[160:161], 0, v[172:173]
	global_store_dwordx4 v[70:71], v[50:53], off
	v_pk_mul_f32 v[74:75], v[140:141], v[166:167] op_sel_hi:[1,0]
	v_pk_mul_f32 v[76:77], v[138:139], v[166:167] op_sel_hi:[1,0]
	v_pk_mul_f32 v[50:51], v[144:145], v[166:167] op_sel_hi:[1,0]
	v_pk_mul_f32 v[52:53], v[142:143], v[166:167] op_sel_hi:[1,0]
	v_mov_b32_e32 v169, v1
	v_pk_mul_f32 v[70:71], v[48:49], v[50:51]
	v_pk_mul_f32 v[72:73], v[46:47], v[52:53]
	v_pk_mul_f32 v[78:79], v[44:45], v[74:75]
	v_pk_mul_f32 v[80:81], v[42:43], v[76:77]
	v_pk_fma_f32 v[48:49], v[48:49], v[50:51], v[64:65]
	v_pk_fma_f32 v[46:47], v[46:47], v[52:53], v[62:63]
	v_pk_fma_f32 v[50:51], v[44:45], v[74:75], v[66:67]
	v_pk_fma_f32 v[52:53], v[42:43], v[76:77], v[68:69]
	v_cvt_pk_bf16_f32 v42, v72, v73
	v_cvt_pk_bf16_f32 v43, v70, v71
	v_cvt_pk_bf16_f32 v44, v80, v81
	v_cvt_pk_bf16_f32 v45, v78, v79
	v_lshl_add_u64 v[62:63], v[160:161], 0, v[168:169]
	global_store_dwordx4 v[62:63], v[42:45], off
	v_pk_mul_f32 v[66:67], v[132:133], v[166:167] op_sel_hi:[1,0]
	v_pk_mul_f32 v[68:69], v[130:131], v[166:167] op_sel_hi:[1,0]
	v_pk_mul_f32 v[42:43], v[136:137], v[166:167] op_sel_hi:[1,0]
	v_pk_mul_f32 v[44:45], v[134:135], v[166:167] op_sel_hi:[1,0]
	v_mov_b32_e32 v159, v1
	v_pk_mul_f32 v[62:63], v[40:41], v[42:43]
	v_pk_mul_f32 v[64:65], v[38:39], v[44:45]
	v_pk_mul_f32 v[70:71], v[36:37], v[66:67]
	v_pk_mul_f32 v[72:73], v[34:35], v[68:69]
	v_pk_fma_f32 v[40:41], v[40:41], v[42:43], v[56:57]
	v_pk_fma_f32 v[38:39], v[38:39], v[44:45], v[54:55]
	v_pk_fma_f32 v[42:43], v[36:37], v[66:67], v[58:59]
	v_pk_fma_f32 v[44:45], v[34:35], v[68:69], v[60:61]
	v_cvt_pk_bf16_f32 v34, v64, v65
	v_cvt_pk_bf16_f32 v35, v62, v63
	v_cvt_pk_bf16_f32 v36, v72, v73
	v_cvt_pk_bf16_f32 v37, v70, v71
	v_lshl_add_u64 v[54:55], v[160:161], 0, v[158:159]
	global_store_dwordx4 v[54:55], v[34:37], off
	v_pk_mul_f32 v[58:59], v[140:141], v[164:165] op_sel_hi:[1,0]
	v_pk_mul_f32 v[60:61], v[138:139], v[164:165] op_sel_hi:[1,0]
	v_pk_mul_f32 v[34:35], v[144:145], v[164:165] op_sel_hi:[1,0]
	v_pk_mul_f32 v[36:37], v[142:143], v[164:165] op_sel_hi:[1,0]
	v_mov_b32_e32 v129, v1
	v_pk_mul_f32 v[54:55], v[32:33], v[34:35]
	v_pk_mul_f32 v[56:57], v[30:31], v[36:37]
	v_pk_mul_f32 v[62:63], v[28:29], v[58:59]
	v_pk_mul_f32 v[64:65], v[26:27], v[60:61]
	v_pk_fma_f32 v[32:33], v[32:33], v[34:35], v[48:49]
	v_pk_fma_f32 v[30:31], v[30:31], v[36:37], v[46:47]
	v_pk_fma_f32 v[34:35], v[28:29], v[58:59], v[50:51]
	v_pk_fma_f32 v[36:37], v[26:27], v[60:61], v[52:53]
	v_cvt_pk_bf16_f32 v26, v56, v57
	v_cvt_pk_bf16_f32 v27, v54, v55
	v_cvt_pk_bf16_f32 v28, v64, v65
	v_cvt_pk_bf16_f32 v29, v62, v63
	v_lshl_add_u64 v[46:47], v[160:161], 0, v[128:129]
	global_store_dwordx4 v[46:47], v[26:29], off
	v_pk_mul_f32 v[50:51], v[132:133], v[164:165] op_sel_hi:[1,0]
	v_pk_mul_f32 v[52:53], v[130:131], v[164:165] op_sel_hi:[1,0]
	v_pk_mul_f32 v[26:27], v[136:137], v[164:165] op_sel_hi:[1,0]
	v_pk_mul_f32 v[28:29], v[134:135], v[164:165] op_sel_hi:[1,0]
	v_mov_b32_e32 v127, v1
	v_pk_mul_f32 v[46:47], v[24:25], v[26:27]
	v_pk_mul_f32 v[48:49], v[22:23], v[28:29]
	v_pk_mul_f32 v[54:55], v[20:21], v[50:51]
	v_pk_mul_f32 v[56:57], v[18:19], v[52:53]
	v_pk_fma_f32 v[24:25], v[24:25], v[26:27], v[40:41]
	v_pk_fma_f32 v[22:23], v[22:23], v[28:29], v[38:39]
	v_pk_fma_f32 v[26:27], v[20:21], v[50:51], v[42:43]
	v_pk_fma_f32 v[28:29], v[18:19], v[52:53], v[44:45]
	v_cvt_pk_bf16_f32 v18, v48, v49
	v_cvt_pk_bf16_f32 v19, v46, v47
	v_cvt_pk_bf16_f32 v20, v56, v57
	v_cvt_pk_bf16_f32 v21, v54, v55
	v_lshl_add_u64 v[38:39], v[160:161], 0, v[126:127]
	global_store_dwordx4 v[38:39], v[18:21], off
	v_pk_mul_f32 v[42:43], v[140:141], v[162:163] op_sel_hi:[1,0]
	v_pk_mul_f32 v[44:45], v[138:139], v[162:163] op_sel_hi:[1,0]
	v_pk_mul_f32 v[20:21], v[142:143], v[162:163] op_sel_hi:[1,0]
	v_pk_mul_f32 v[18:19], v[144:145], v[162:163] op_sel_hi:[1,0]
	v_pk_mul_f32 v[40:41], v[14:15], v[20:21]
	v_pk_fma_f32 v[14:15], v[14:15], v[20:21], v[30:31]
	v_pk_mul_f32 v[38:39], v[16:17], v[18:19]
	v_pk_mul_f32 v[46:47], v[12:13], v[42:43]
	v_pk_fma_f32 v[16:17], v[16:17], v[18:19], v[32:33]
	v_pk_fma_f32 v[18:19], v[12:13], v[42:43], v[34:35]
	ds_bpermute_b32 v42, v233, v14
	ds_bpermute_b32 v43, v233, v15
	v_pk_fma_f32 v[20:21], v[10:11], v[44:45], v[36:37]
	v_pk_mul_f32 v[36:37], v[130:131], v[162:163] op_sel_hi:[1,0]
	v_pk_mul_f32 v[48:49], v[10:11], v[44:45]
	v_cvt_pk_bf16_f32 v10, v40, v41
	v_pk_mul_f32 v[40:41], v[2:3], v[36:37]
	v_pk_fma_f32 v[28:29], v[2:3], v[36:37], v[28:29]
	s_waitcnt lgkmcnt(0)
;     __device__ __forceinline__ void operator()(const f32x4 (&acc)[2][2][4][2], const Unit& u, int ui, int wr, int wc, int fr, int fq) const {
;     ...
;                 for (int bj = 0; bj < 2; ++bj)
; #pragma unroll
;                     for (int n = 0; n < 2; ++n)
; #pragma unroll
;                         for (int e = 0; e < 4; ++e) { float s = ks[bj][n][e]; s += __shfl_xor(s, 1); s += __shfl_xor(s, 2); s += __shfl_xor(s, 4); s += __shfl_xor(s, 8); ks[bj][n][e] = s; }
;                 if (fr == 0) { float* kp = (float*)(ws + E_KMP) + (size_t)(unsigned)((((u.pm * 4 + wc) * 2 + wr) * 64 + 8 * fq));
; #pragma unroll
;                     for (int bj = 0; bj < 2; ++bj)
; #pragma unroll
;                         for (int n = 0; n < 2; ++n) *(f32x4*)(kp + 32 * bj + 4 * n) = ks[bj][n]; }
	v_pk_add_f32 v[2:3], v[14:15], v[42:43]
	ds_bpermute_b32 v14, v233, v18
	ds_bpermute_b32 v15, v233, v19
	v_mov_b32_e32 v125, v1
	v_cvt_pk_bf16_f32 v11, v38, v39
	v_cvt_pk_bf16_f32 v12, v48, v49
	v_cvt_pk_bf16_f32 v13, v46, v47
	v_lshl_add_u64 v[30:31], v[160:161], 0, v[124:125]
	global_store_dwordx4 v[30:31], v[10:13], off
	s_waitcnt lgkmcnt(0)
	v_pk_add_f32 v[14:15], v[18:19], v[14:15]
	v_pk_mul_f32 v[34:35], v[132:133], v[162:163] op_sel_hi:[1,0]
	v_pk_mul_f32 v[12:13], v[134:135], v[162:163] op_sel_hi:[1,0]
	v_pk_mul_f32 v[10:11], v[136:137], v[162:163] op_sel_hi:[1,0]
	v_pk_fma_f32 v[22:23], v[6:7], v[12:13], v[22:23]
	ds_bpermute_b32 v18, v233, v22
	ds_bpermute_b32 v19, v233, v23
	v_pk_mul_f32 v[30:31], v[8:9], v[10:11]
	v_pk_mul_f32 v[32:33], v[6:7], v[12:13]
	v_pk_fma_f32 v[24:25], v[8:9], v[10:11], v[24:25]
	v_pk_fma_f32 v[26:27], v[4:5], v[34:35], v[26:27]
	v_pk_mul_f32 v[38:39], v[4:5], v[34:35]
	v_cvt_pk_bf16_f32 v34, v32, v33
	v_cvt_pk_bf16_f32 v35, v30, v31
	ds_bpermute_b32 v6, v233, v16
	ds_bpermute_b32 v7, v233, v17
	ds_bpermute_b32 v10, v233, v20
	ds_bpermute_b32 v11, v233, v21
	s_waitcnt lgkmcnt(0)
	v_pk_add_f32 v[18:19], v[22:23], v[18:19]
	ds_bpermute_b32 v22, v233, v24
	ds_bpermute_b32 v23, v233, v25
	ds_bpermute_b32 v30, v233, v28
	ds_bpermute_b32 v31, v233, v29
	ds_bpermute_b32 v32, v233, v26
	ds_bpermute_b32 v33, v233, v27
	v_pk_add_f32 v[6:7], v[16:17], v[6:7]
	v_pk_add_f32 v[10:11], v[20:21], v[10:11]
	s_waitcnt lgkmcnt(0)
	v_pk_add_f32 v[22:23], v[24:25], v[22:23]
	v_pk_add_f32 v[28:29], v[28:29], v[30:31]
	v_pk_add_f32 v[26:27], v[26:27], v[32:33]
	ds_bpermute_b32 v4, v234, v2
	ds_bpermute_b32 v5, v234, v3
	ds_bpermute_b32 v8, v234, v6
	ds_bpermute_b32 v9, v234, v7
	ds_bpermute_b32 v12, v234, v10
	ds_bpermute_b32 v13, v234, v11
	ds_bpermute_b32 v16, v234, v14
	ds_bpermute_b32 v17, v234, v15
	ds_bpermute_b32 v20, v234, v18
	ds_bpermute_b32 v21, v234, v19
	ds_bpermute_b32 v24, v234, v22
	ds_bpermute_b32 v25, v234, v23
	ds_bpermute_b32 v30, v234, v28
	ds_bpermute_b32 v31, v234, v29
	ds_bpermute_b32 v32, v234, v26
	ds_bpermute_b32 v33, v234, v27
	s_waitcnt lgkmcnt(0)
	v_pk_add_f32 v[2:3], v[2:3], v[4:5]
	v_pk_add_f32 v[6:7], v[6:7], v[8:9]
	v_pk_add_f32 v[10:11], v[10:11], v[12:13]
	v_pk_add_f32 v[14:15], v[14:15], v[16:17]
	v_pk_add_f32 v[18:19], v[18:19], v[20:21]
	v_pk_add_f32 v[22:23], v[22:23], v[24:25]
	v_pk_add_f32 v[28:29], v[28:29], v[30:31]
	v_pk_add_f32 v[32:33], v[26:27], v[32:33]
	ds_bpermute_b32 v4, v235, v2
	ds_bpermute_b32 v5, v235, v3
	v_cvt_pk_bf16_f32 v36, v40, v41
	ds_bpermute_b32 v8, v235, v6
	ds_bpermute_b32 v9, v235, v7
	ds_bpermute_b32 v12, v235, v10
	ds_bpermute_b32 v13, v235, v11
	ds_bpermute_b32 v16, v235, v14
	ds_bpermute_b32 v17, v235, v15
	ds_bpermute_b32 v20, v235, v18
	ds_bpermute_b32 v21, v235, v19
	ds_bpermute_b32 v24, v235, v22
	ds_bpermute_b32 v25, v235, v23
	ds_bpermute_b32 v30, v235, v28
	ds_bpermute_b32 v31, v235, v29
	ds_bpermute_b32 v40, v235, v32
	ds_bpermute_b32 v41, v235, v33
	s_waitcnt lgkmcnt(0)
	v_pk_add_f32 v[2:3], v[2:3], v[4:5]
	v_pk_add_f32 v[6:7], v[6:7], v[8:9]
	v_pk_add_f32 v[10:11], v[10:11], v[12:13]
	v_pk_add_f32 v[14:15], v[14:15], v[16:17]
	v_pk_add_f32 v[18:19], v[18:19], v[20:21]
	v_pk_add_f32 v[22:23], v[22:23], v[24:25]
	v_pk_add_f32 v[26:27], v[28:29], v[30:31]
	v_pk_add_f32 v[30:31], v[32:33], v[40:41]
	ds_bpermute_b32 v4, v236, v2
	ds_bpermute_b32 v5, v236, v3
	ds_bpermute_b32 v8, v236, v6
	ds_bpermute_b32 v9, v236, v7
	ds_bpermute_b32 v12, v236, v10
	ds_bpermute_b32 v13, v236, v11
	ds_bpermute_b32 v16, v236, v14
	ds_bpermute_b32 v17, v236, v15
	ds_bpermute_b32 v20, v236, v18
	ds_bpermute_b32 v21, v236, v19
	ds_bpermute_b32 v24, v236, v22
	ds_bpermute_b32 v25, v236, v23
	ds_bpermute_b32 v28, v236, v26
	ds_bpermute_b32 v29, v236, v27
	ds_bpermute_b32 v32, v236, v30
	ds_bpermute_b32 v33, v236, v31
	v_mov_b32_e32 v123, v1
	v_cvt_pk_bf16_f32 v37, v38, v39
	v_lshl_add_u64 v[38:39], v[160:161], 0, v[122:123]
	global_store_dwordx4 v[38:39], v[34:37], off
	s_and_saveexec_b64 s[26:27], s[36:37]
	s_cbranch_execz .LBB0_619
	v_lshl_add_u32 v0, s4, 9, v171
	s_waitcnt lgkmcnt(0)
	v_pk_add_f32 v[6:7], v[6:7], v[8:9]
	v_pk_add_f32 v[4:5], v[2:3], v[4:5]
	v_lshl_add_u64 v[2:3], v[0:1], 2, s[16:17]
	v_pk_add_f32 v[30:31], v[30:31], v[32:33]
	v_pk_add_f32 v[28:29], v[26:27], v[28:29]
	v_pk_add_f32 v[22:23], v[22:23], v[24:25]
	v_pk_add_f32 v[20:21], v[18:19], v[20:21]
	v_pk_add_f32 v[14:15], v[14:15], v[16:17]
	v_pk_add_f32 v[12:13], v[10:11], v[12:13]
	global_store_dwordx4 v[2:3], v[4:7], off
	global_store_dwordx4 v[2:3], v[12:15], off offset:16
	global_store_dwordx4 v[2:3], v[20:23], off offset:128
	global_store_dwordx4 v[2:3], v[28:31], off offset:144
